# GEMM 8-phase loops: hipcc's per-MFMA-cluster s_setprio 1/0 flips removed (96 instructions, strategy 7.4b), on top of v9_prohoist
# baseline (speedup 1.0000x reference)
.LBB0_376:
	s_add_u32 s34, s12, s2
	s_addc_u32 s35, s13, s3
	s_add_u32 s36, s34, 0x1701b100
	s_addc_u32 s44, s35, 0
	s_add_u32 s74, s21, s2
	s_addc_u32 s75, s30, s3
	s_add_i32 s76, 0, 0x10000
	v_add_u32_e32 v139, s76, v155
	ds_read_b128 v[162:165], v139
	ds_read_b128 v[166:169], v139 offset:1024
	ds_read_b128 v[170:173], v139 offset:2048
	ds_read_b128 v[174:177], v139 offset:3072
	s_cmpk_eq_i32 s2, 0x700
	s_cselect_b64 vcc, -1, 0
	s_and_b64 s[34:35], vcc, exec
	v_cndmask_b32_e32 v2, v138, v158, vcc
	s_cselect_b32 s45, s15, s44
	s_cselect_b32 s44, s14, s36
	v_cndmask_b32_e32 v178, v140, v159, vcc
	v_cndmask_b32_e32 v139, v142, v160, vcc
	v_cndmask_b32_e32 v141, v144, v161, vcc
	s_cselect_b32 s35, s0, s75
	s_cselect_b32 s34, s1, s74
	v_lshl_add_u64 v[206:207], v[148:149], 0, s[2:3]
	s_add_i32 m0, s27, 0xc000
	ds_read_b128 v[182:185], v157
	ds_read_b128 v[186:189], v157 offset:1024
	ds_read_b128 v[190:193], v157 offset:2048
	ds_read_b128 v[194:197], v157 offset:3072
	ds_read_b128 v[198:201], v157 offset:4096
	ds_read_b128 v[202:205], v157 offset:5120
	ds_read_b128 v[214:217], v157 offset:6144
	ds_read_b128 v[218:221], v157 offset:7168
	global_load_lds_dwordx4 v[206:207], off
	v_lshl_add_u64 v[206:207], v[146:147], 0, s[2:3]
	s_add_i32 m0, s27, 0xe000
	s_nop 0
	global_load_lds_dwordx4 v[206:207], off
	s_waitcnt lgkmcnt(8)
	s_barrier
	s_waitcnt lgkmcnt(0)
	s_waitcnt lgkmcnt(0)
	v_mfma_f32_16x16x32_bf16 v[128:131], v[162:165], v[182:185], v[128:131]
	v_mfma_f32_16x16x32_bf16 v[124:127], v[170:173], v[182:185], v[124:127]
	v_mfma_f32_16x16x32_bf16 v[112:115], v[162:165], v[190:193], v[112:115]
	v_mfma_f32_16x16x32_bf16 v[108:111], v[170:173], v[190:193], v[108:111]
	v_mfma_f32_16x16x32_bf16 v[96:99], v[162:165], v[198:201], v[96:99]
	v_mfma_f32_16x16x32_bf16 v[92:95], v[170:173], v[198:201], v[92:95]
	v_mfma_f32_16x16x32_bf16 v[80:83], v[162:165], v[214:217], v[80:83]
	v_mfma_f32_16x16x32_bf16 v[76:79], v[170:173], v[214:217], v[76:79]
	v_mfma_f32_16x16x32_bf16 v[128:131], v[166:169], v[186:189], v[128:131]
	v_mfma_f32_16x16x32_bf16 v[124:127], v[174:177], v[186:189], v[124:127]
	v_mfma_f32_16x16x32_bf16 v[112:115], v[166:169], v[194:197], v[112:115]
	v_mfma_f32_16x16x32_bf16 v[108:111], v[174:177], v[194:197], v[108:111]
	v_mfma_f32_16x16x32_bf16 v[96:99], v[166:169], v[202:205], v[96:99]
	v_mfma_f32_16x16x32_bf16 v[92:95], v[174:177], v[202:205], v[92:95]
	v_mfma_f32_16x16x32_bf16 v[80:83], v[166:169], v[218:221], v[80:83]
	v_mfma_f32_16x16x32_bf16 v[76:79], v[174:177], v[218:221], v[76:79]
	s_barrier
	s_add_i32 s36, 0, 0x14000
	s_add_i32 s74, s76, s26
	v_add_u32_e32 v143, s36, v155
	v_lshl_add_u64 v[206:207], s[34:35], 0, v[132:133]
	s_mov_b32 m0, s74
	ds_read_b128 v[222:225], v143
	ds_read_b128 v[226:229], v143 offset:1024
	ds_read_b128 v[230:233], v143 offset:2048
	ds_read_b128 v[234:237], v143 offset:3072
	global_load_lds_dwordx4 v[206:207], off
	v_lshl_add_u64 v[238:239], s[34:35], 0, v[134:135]
	s_add_i32 m0, s74, 0x2000
	s_nop 0
	global_load_lds_dwordx4 v[238:239], off
	s_barrier
	s_waitcnt lgkmcnt(0)
	s_waitcnt lgkmcnt(0)
	v_mfma_f32_16x16x32_bf16 v[120:123], v[222:225], v[182:185], v[120:123]
	v_mfma_f32_16x16x32_bf16 v[116:119], v[230:233], v[182:185], v[116:119]
	v_mfma_f32_16x16x32_bf16 v[104:107], v[222:225], v[190:193], v[104:107]
	v_mfma_f32_16x16x32_bf16 v[100:103], v[230:233], v[190:193], v[100:103]
	v_mfma_f32_16x16x32_bf16 v[88:91], v[222:225], v[198:201], v[88:91]
	v_mfma_f32_16x16x32_bf16 v[84:87], v[230:233], v[198:201], v[84:87]
	v_mfma_f32_16x16x32_bf16 v[72:75], v[222:225], v[214:217], v[72:75]
	v_mfma_f32_16x16x32_bf16 v[68:71], v[230:233], v[214:217], v[68:71]
	v_mfma_f32_16x16x32_bf16 v[120:123], v[226:229], v[186:189], v[120:123]
	v_mfma_f32_16x16x32_bf16 v[116:119], v[234:237], v[186:189], v[116:119]
	v_mfma_f32_16x16x32_bf16 v[104:107], v[226:229], v[194:197], v[104:107]
	v_mfma_f32_16x16x32_bf16 v[100:103], v[234:237], v[194:197], v[100:103]
	v_mfma_f32_16x16x32_bf16 v[88:91], v[226:229], v[202:205], v[88:91]
	v_mfma_f32_16x16x32_bf16 v[84:87], v[234:237], v[202:205], v[84:87]
	v_mfma_f32_16x16x32_bf16 v[72:75], v[226:229], v[218:221], v[72:75]
	v_mfma_f32_16x16x32_bf16 v[68:71], v[234:237], v[218:221], v[68:71]
	s_mov_b32 m0, s27
	s_barrier
	ds_read_b128 v[182:185], v157 offset:16384
	ds_read_b128 v[186:189], v157 offset:17408
	ds_read_b128 v[190:193], v157 offset:18432
	ds_read_b128 v[194:197], v157 offset:19456
	ds_read_b128 v[198:201], v157 offset:20480
	ds_read_b128 v[202:205], v157 offset:21504
	ds_read_b128 v[214:217], v157 offset:22528
	ds_read_b128 v[218:221], v157 offset:23552
	global_load_lds_dwordx4 v2, s[44:45]
	s_mov_b32 m0, s47
	v_mov_b32_e32 v179, v3
	global_load_lds_dwordx4 v178, s[44:45]
	s_barrier
	s_waitcnt lgkmcnt(0)
	v_lshl_add_u64 v[240:241], s[44:45], 0, v[2:3]
	v_lshl_add_u64 v[178:179], s[44:45], 0, v[178:179]
	s_waitcnt lgkmcnt(0)
	v_mfma_f32_16x16x32_bf16 v[64:67], v[162:165], v[182:185], v[64:67]
	v_mfma_f32_16x16x32_bf16 v[60:63], v[170:173], v[182:185], v[60:63]
	v_mfma_f32_16x16x32_bf16 v[48:51], v[162:165], v[190:193], v[48:51]
	v_mfma_f32_16x16x32_bf16 v[44:47], v[170:173], v[190:193], v[44:47]
	v_mfma_f32_16x16x32_bf16 v[32:35], v[162:165], v[198:201], v[32:35]
	v_mfma_f32_16x16x32_bf16 v[28:31], v[170:173], v[198:201], v[28:31]
	v_mfma_f32_16x16x32_bf16 v[16:19], v[162:165], v[214:217], v[16:19]
	v_mfma_f32_16x16x32_bf16 v[12:15], v[170:173], v[214:217], v[12:15]
	v_mfma_f32_16x16x32_bf16 v[64:67], v[166:169], v[186:189], v[64:67]
	v_mfma_f32_16x16x32_bf16 v[60:63], v[174:177], v[186:189], v[60:63]
	v_mfma_f32_16x16x32_bf16 v[48:51], v[166:169], v[194:197], v[48:51]
	v_mfma_f32_16x16x32_bf16 v[44:47], v[174:177], v[194:197], v[44:47]
	v_mfma_f32_16x16x32_bf16 v[32:35], v[166:169], v[202:205], v[32:35]
	v_mfma_f32_16x16x32_bf16 v[28:31], v[174:177], v[202:205], v[28:31]
	v_mfma_f32_16x16x32_bf16 v[16:19], v[166:169], v[218:221], v[16:19]
	v_mfma_f32_16x16x32_bf16 v[12:15], v[174:177], v[218:221], v[12:15]
	s_barrier
	s_add_u32 s74, s34, 0x40000
	s_addc_u32 s75, s35, 0
	s_add_i32 s36, s36, s26
	v_lshl_add_u64 v[162:163], s[74:75], 0, v[132:133]
	s_mov_b32 m0, s36
	s_nop 0
	global_load_lds_dwordx4 v[162:163], off
	v_lshl_add_u64 v[162:163], s[74:75], 0, v[134:135]
	s_add_i32 m0, s36, 0x2000
	s_nop 0
	global_load_lds_dwordx4 v[162:163], off
	s_waitcnt vmcnt(6)
	s_barrier
	v_mfma_f32_16x16x32_bf16 v[56:59], v[222:225], v[182:185], v[56:59]
	v_mfma_f32_16x16x32_bf16 v[52:55], v[230:233], v[182:185], v[52:55]
	v_mfma_f32_16x16x32_bf16 v[40:43], v[222:225], v[190:193], v[40:43]
	v_mfma_f32_16x16x32_bf16 v[36:39], v[230:233], v[190:193], v[36:39]
	v_mfma_f32_16x16x32_bf16 v[20:23], v[222:225], v[198:201], v[20:23]
	v_mfma_f32_16x16x32_bf16 v[24:27], v[230:233], v[198:201], v[24:27]
	v_mfma_f32_16x16x32_bf16 v[4:7], v[222:225], v[214:217], v[4:7]
	v_mfma_f32_16x16x32_bf16 v[8:11], v[230:233], v[214:217], v[8:11]
	v_mfma_f32_16x16x32_bf16 v[56:59], v[226:229], v[186:189], v[56:59]
	v_mfma_f32_16x16x32_bf16 v[52:55], v[234:237], v[186:189], v[52:55]
	v_mfma_f32_16x16x32_bf16 v[40:43], v[226:229], v[194:197], v[40:43]
	v_mfma_f32_16x16x32_bf16 v[36:39], v[234:237], v[194:197], v[36:39]
	v_mfma_f32_16x16x32_bf16 v[20:23], v[226:229], v[202:205], v[20:23]
	v_mfma_f32_16x16x32_bf16 v[24:27], v[234:237], v[202:205], v[24:27]
	v_mfma_f32_16x16x32_bf16 v[4:7], v[226:229], v[218:221], v[4:7]
	v_mfma_f32_16x16x32_bf16 v[8:11], v[234:237], v[218:221], v[8:11]
	s_add_i32 s36, 0, 0x18000
	v_add_u32_e32 v2, s36, v155
	s_barrier
	ds_read_b128 v[162:165], v2
	ds_read_b128 v[166:169], v2 offset:1024
	ds_read_b128 v[170:173], v2 offset:2048
	ds_read_b128 v[174:177], v2 offset:3072
	s_mov_b32 m0, s60
	ds_read_b128 v[182:185], v157 offset:32768
	ds_read_b128 v[186:189], v157 offset:33792
	ds_read_b128 v[190:193], v157 offset:34816
	ds_read_b128 v[194:197], v157 offset:35840
	ds_read_b128 v[198:201], v157 offset:36864
	ds_read_b128 v[202:205], v157 offset:37888
	ds_read_b128 v[214:217], v157 offset:38912
	ds_read_b128 v[218:221], v157 offset:39936
	global_load_lds_dwordx4 v139, s[44:45]
	s_mov_b32 m0, s61
	s_nop 0
	global_load_lds_dwordx4 v141, s[44:45]
	s_waitcnt lgkmcnt(8)
	s_barrier
	s_waitcnt lgkmcnt(0)
	s_waitcnt lgkmcnt(0)
	v_mfma_f32_16x16x32_bf16 v[128:131], v[162:165], v[182:185], v[128:131]
	v_mfma_f32_16x16x32_bf16 v[124:127], v[170:173], v[182:185], v[124:127]
	v_mfma_f32_16x16x32_bf16 v[112:115], v[162:165], v[190:193], v[112:115]
	v_mfma_f32_16x16x32_bf16 v[108:111], v[170:173], v[190:193], v[108:111]
	v_mfma_f32_16x16x32_bf16 v[96:99], v[162:165], v[198:201], v[96:99]
	v_mfma_f32_16x16x32_bf16 v[92:95], v[170:173], v[198:201], v[92:95]
	v_mfma_f32_16x16x32_bf16 v[80:83], v[162:165], v[214:217], v[80:83]
	v_mfma_f32_16x16x32_bf16 v[76:79], v[170:173], v[214:217], v[76:79]
	v_mfma_f32_16x16x32_bf16 v[128:131], v[166:169], v[186:189], v[128:131]
	v_mfma_f32_16x16x32_bf16 v[124:127], v[174:177], v[186:189], v[124:127]
	v_mfma_f32_16x16x32_bf16 v[112:115], v[166:169], v[194:197], v[112:115]
	v_mfma_f32_16x16x32_bf16 v[108:111], v[174:177], v[194:197], v[108:111]
	v_mfma_f32_16x16x32_bf16 v[96:99], v[166:169], v[202:205], v[96:99]
	v_mfma_f32_16x16x32_bf16 v[92:95], v[174:177], v[202:205], v[92:95]
	v_mfma_f32_16x16x32_bf16 v[80:83], v[166:169], v[218:221], v[80:83]
	v_mfma_f32_16x16x32_bf16 v[76:79], v[174:177], v[218:221], v[76:79]
	s_barrier
	s_add_i32 s44, 0, 0x1c000
	s_add_i32 s36, s36, s26
	v_add_u32_e32 v2, s44, v155
	v_lshl_add_u64 v[206:207], v[206:207], 0, s[8:9]
	s_mov_b32 m0, s36
	ds_read_b128 v[222:225], v2
	ds_read_b128 v[226:229], v2 offset:1024
	ds_read_b128 v[230:233], v2 offset:2048
	ds_read_b128 v[234:237], v2 offset:3072
	global_load_lds_dwordx4 v[206:207], off
	v_lshl_add_u64 v[206:207], v[238:239], 0, s[8:9]
	s_add_i32 m0, s36, 0x2000
	s_nop 0
	global_load_lds_dwordx4 v[206:207], off
	s_barrier
	s_waitcnt lgkmcnt(0)
	s_waitcnt lgkmcnt(0)
	v_mfma_f32_16x16x32_bf16 v[120:123], v[222:225], v[182:185], v[120:123]
	v_mfma_f32_16x16x32_bf16 v[116:119], v[230:233], v[182:185], v[116:119]
	v_mfma_f32_16x16x32_bf16 v[104:107], v[222:225], v[190:193], v[104:107]
	v_mfma_f32_16x16x32_bf16 v[100:103], v[230:233], v[190:193], v[100:103]
	v_mfma_f32_16x16x32_bf16 v[88:91], v[222:225], v[198:201], v[88:91]
	v_mfma_f32_16x16x32_bf16 v[84:87], v[230:233], v[198:201], v[84:87]
	v_mfma_f32_16x16x32_bf16 v[72:75], v[222:225], v[214:217], v[72:75]
	v_mfma_f32_16x16x32_bf16 v[68:71], v[230:233], v[214:217], v[68:71]
	v_mfma_f32_16x16x32_bf16 v[120:123], v[226:229], v[186:189], v[120:123]
	v_mfma_f32_16x16x32_bf16 v[116:119], v[234:237], v[186:189], v[116:119]
	v_mfma_f32_16x16x32_bf16 v[104:107], v[226:229], v[194:197], v[104:107]
	v_mfma_f32_16x16x32_bf16 v[100:103], v[234:237], v[194:197], v[100:103]
	v_mfma_f32_16x16x32_bf16 v[88:91], v[226:229], v[202:205], v[88:91]
	v_mfma_f32_16x16x32_bf16 v[84:87], v[234:237], v[202:205], v[84:87]
	v_mfma_f32_16x16x32_bf16 v[72:75], v[226:229], v[218:221], v[72:75]
	v_mfma_f32_16x16x32_bf16 v[68:71], v[234:237], v[218:221], v[68:71]
	s_mov_b32 m0, s63
	v_lshl_add_u64 v[206:207], v[240:241], 0, s[8:9]
	s_barrier
	ds_read_b128 v[182:185], v157 offset:49152
	ds_read_b128 v[186:189], v157 offset:50176
	ds_read_b128 v[190:193], v157 offset:51200
	ds_read_b128 v[194:197], v157 offset:52224
	ds_read_b128 v[198:201], v157 offset:53248
	ds_read_b128 v[202:205], v157 offset:54272
	ds_read_b128 v[214:217], v157 offset:55296
	ds_read_b128 v[218:221], v157 offset:56320
	global_load_lds_dwordx4 v[206:207], off
	v_lshl_add_u64 v[178:179], v[178:179], 0, s[8:9]
	s_mov_b32 m0, s64
	s_nop 0
	global_load_lds_dwordx4 v[178:179], off
	s_barrier
	s_waitcnt lgkmcnt(0)
	s_waitcnt lgkmcnt(0)
	v_mfma_f32_16x16x32_bf16 v[64:67], v[162:165], v[182:185], v[64:67]
	v_mfma_f32_16x16x32_bf16 v[60:63], v[170:173], v[182:185], v[60:63]
	v_mfma_f32_16x16x32_bf16 v[48:51], v[162:165], v[190:193], v[48:51]
	v_mfma_f32_16x16x32_bf16 v[44:47], v[170:173], v[190:193], v[44:47]
	v_mfma_f32_16x16x32_bf16 v[32:35], v[162:165], v[198:201], v[32:35]
	v_mfma_f32_16x16x32_bf16 v[28:31], v[170:173], v[198:201], v[28:31]
	v_mfma_f32_16x16x32_bf16 v[16:19], v[162:165], v[214:217], v[16:19]
	v_mfma_f32_16x16x32_bf16 v[12:15], v[170:173], v[214:217], v[12:15]
	v_mfma_f32_16x16x32_bf16 v[64:67], v[166:169], v[186:189], v[64:67]
	v_mfma_f32_16x16x32_bf16 v[60:63], v[174:177], v[186:189], v[60:63]
	v_mfma_f32_16x16x32_bf16 v[48:51], v[166:169], v[194:197], v[48:51]
	v_mfma_f32_16x16x32_bf16 v[44:47], v[174:177], v[194:197], v[44:47]
	v_mfma_f32_16x16x32_bf16 v[32:35], v[166:169], v[202:205], v[32:35]
	v_mfma_f32_16x16x32_bf16 v[28:31], v[174:177], v[202:205], v[28:31]
	v_mfma_f32_16x16x32_bf16 v[16:19], v[166:169], v[218:221], v[16:19]
	v_mfma_f32_16x16x32_bf16 v[12:15], v[174:177], v[218:221], v[12:15]
	s_barrier
	s_add_u32 s34, s34, 0x40080
	s_addc_u32 s35, s35, 0
	s_add_i32 s36, s44, s26
	v_lshl_add_u64 v[162:163], s[34:35], 0, v[132:133]
	s_mov_b32 m0, s36
	s_nop 0
	global_load_lds_dwordx4 v[162:163], off
	v_lshl_add_u64 v[162:163], s[34:35], 0, v[134:135]
	s_add_i32 m0, s36, 0x2000
	s_nop 0
	global_load_lds_dwordx4 v[162:163], off
	s_waitcnt vmcnt(6)
	s_barrier
	v_mfma_f32_16x16x32_bf16 v[56:59], v[222:225], v[182:185], v[56:59]
	v_mfma_f32_16x16x32_bf16 v[52:55], v[230:233], v[182:185], v[52:55]
	v_mfma_f32_16x16x32_bf16 v[40:43], v[222:225], v[190:193], v[40:43]
	v_mfma_f32_16x16x32_bf16 v[36:39], v[230:233], v[190:193], v[36:39]
	v_mfma_f32_16x16x32_bf16 v[20:23], v[222:225], v[198:201], v[20:23]
	v_mfma_f32_16x16x32_bf16 v[24:27], v[230:233], v[198:201], v[24:27]
	v_mfma_f32_16x16x32_bf16 v[4:7], v[222:225], v[214:217], v[4:7]
	v_mfma_f32_16x16x32_bf16 v[8:11], v[230:233], v[214:217], v[8:11]
	v_mfma_f32_16x16x32_bf16 v[56:59], v[226:229], v[186:189], v[56:59]
	v_mfma_f32_16x16x32_bf16 v[52:55], v[234:237], v[186:189], v[52:55]
	v_mfma_f32_16x16x32_bf16 v[40:43], v[226:229], v[194:197], v[40:43]
	v_mfma_f32_16x16x32_bf16 v[36:39], v[234:237], v[194:197], v[36:39]
	v_mfma_f32_16x16x32_bf16 v[20:23], v[226:229], v[202:205], v[20:23]
	v_mfma_f32_16x16x32_bf16 v[24:27], v[234:237], v[202:205], v[24:27]
	v_mfma_f32_16x16x32_bf16 v[4:7], v[226:229], v[218:221], v[4:7]
	v_mfma_f32_16x16x32_bf16 v[8:11], v[234:237], v[218:221], v[8:11]
	s_add_i32 s57, s57, 2
	s_add_u32 s2, s2, 0x100
	s_addc_u32 s3, s3, 0
	s_cmp_gt_u32 s57, 13
	s_barrier
	s_cbranch_scc0 .LBB0_376
	v_lshl_add_u32 v140, s20, 8, v154
	v_ashrrev_i32_e32 v141, 31, v140
	v_lshl_or_b32 v138, s46, 8, v156
	v_lshlrev_b64 v[142:143], 12, v[140:141]
	v_ashrrev_i32_e32 v139, 31, v138
	v_lshl_add_u64 v[142:143], s[48:49], 0, v[142:143]
	s_cmp_eq_u32 s46, 7
	v_cvt_pk_bf16_f32 v146, v128, v129
	v_cvt_pk_bf16_f32 v147, v130, v131
	v_cvt_pk_bf16_f32 v148, v124, v125
	v_cvt_pk_bf16_f32 v149, v126, v127
	v_lshl_add_u64 v[144:145], v[138:139], 1, v[142:143]
	s_cselect_b64 s[2:3], -1, 0
	s_cmp_lt_i32 s46, 6
	global_store_dwordx4 v[144:145], v[146:149], off
	s_cbranch_scc1 .LBB0_381
	s_cmp_eq_u32 s46, 6
	s_mov_b64 s[0:1], -1
	s_cbranch_scc0 .LBB0_380
	s_mov_b64 s[0:1], 0

.LBB0_764:
	s_add_u32 s34, s46, s2
	s_addc_u32 s35, s47, s3
	s_add_u32 s36, s34, 0x1f41bb00
	s_addc_u32 s40, s35, 0
	s_add_u32 s72, s0, s2
	s_addc_u32 s73, s1, s3
	s_add_i32 s74, 0, 0x10000
	v_add_u32_e32 v133, s74, v188
	ds_read_b128 v[144:147], v133
	ds_read_b128 v[148:151], v133 offset:1024
	ds_read_b128 v[152:155], v133 offset:2048
	ds_read_b128 v[156:159], v133 offset:3072
	s_cmpk_eq_i32 s2, 0x200
	s_cselect_b64 vcc, -1, 0
	s_and_b64 s[34:35], vcc, exec
	v_cndmask_b32_e32 v2, v132, v190, vcc
	s_cselect_b32 s41, s49, s40
	s_cselect_b32 s40, s48, s36
	v_cndmask_b32_e32 v206, v134, v191, vcc
	v_cndmask_b32_e32 v133, v136, v192, vcc
	v_cndmask_b32_e32 v135, v138, v193, vcc
	s_cselect_b32 s35, s43, s73
	s_cselect_b32 s34, s42, s72
	v_lshl_add_u64 v[222:223], v[142:143], 0, s[2:3]
	s_add_i32 m0, s59, 0xc000
	ds_read_b128 v[160:163], v189
	ds_read_b128 v[164:167], v189 offset:1024
	ds_read_b128 v[182:185], v189 offset:2048
	ds_read_b128 v[194:197], v189 offset:3072
	ds_read_b128 v[198:201], v189 offset:4096
	ds_read_b128 v[202:205], v189 offset:5120
	ds_read_b128 v[214:217], v189 offset:6144
	ds_read_b128 v[218:221], v189 offset:7168
	global_load_lds_dwordx4 v[222:223], off
	v_lshl_add_u64 v[222:223], v[140:141], 0, s[2:3]
	s_add_i32 m0, s59, 0xe000
	s_nop 0
	global_load_lds_dwordx4 v[222:223], off
	s_waitcnt lgkmcnt(8)
	s_barrier
	s_waitcnt lgkmcnt(0)
	s_waitcnt lgkmcnt(0)
	v_mfma_f32_16x16x32_bf16 v[128:131], v[144:147], v[160:163], v[128:131]
	v_mfma_f32_16x16x32_bf16 v[124:127], v[152:155], v[160:163], v[124:127]
	v_mfma_f32_16x16x32_bf16 v[120:123], v[144:147], v[182:185], v[120:123]
	v_mfma_f32_16x16x32_bf16 v[112:115], v[152:155], v[182:185], v[112:115]
	v_mfma_f32_16x16x32_bf16 v[104:107], v[144:147], v[198:201], v[104:107]
	v_mfma_f32_16x16x32_bf16 v[96:99], v[152:155], v[198:201], v[96:99]
	v_mfma_f32_16x16x32_bf16 v[88:91], v[144:147], v[214:217], v[88:91]
	v_mfma_f32_16x16x32_bf16 v[80:83], v[152:155], v[214:217], v[80:83]
	v_mfma_f32_16x16x32_bf16 v[128:131], v[148:151], v[164:167], v[128:131]
	v_mfma_f32_16x16x32_bf16 v[124:127], v[156:159], v[164:167], v[124:127]
	v_mfma_f32_16x16x32_bf16 v[120:123], v[148:151], v[194:197], v[120:123]
	v_mfma_f32_16x16x32_bf16 v[112:115], v[156:159], v[194:197], v[112:115]
	v_mfma_f32_16x16x32_bf16 v[104:107], v[148:151], v[202:205], v[104:107]
	v_mfma_f32_16x16x32_bf16 v[96:99], v[156:159], v[202:205], v[96:99]
	v_mfma_f32_16x16x32_bf16 v[88:91], v[148:151], v[218:221], v[88:91]
	v_mfma_f32_16x16x32_bf16 v[80:83], v[156:159], v[218:221], v[80:83]
	s_barrier
	s_add_i32 s36, 0, 0x14000
	s_add_i32 s72, s74, s58
	v_add_u32_e32 v137, s36, v188
	v_lshl_add_u64 v[238:239], s[34:35], 0, v[168:169]
	s_mov_b32 m0, s72
	ds_read_b128 v[222:225], v137
	ds_read_b128 v[226:229], v137 offset:1024
	ds_read_b128 v[230:233], v137 offset:2048
	ds_read_b128 v[234:237], v137 offset:3072
	global_load_lds_dwordx4 v[238:239], off
	v_lshl_add_u64 v[240:241], s[34:35], 0, v[170:171]
	s_add_i32 m0, s72, 0x2000
	s_nop 0
	global_load_lds_dwordx4 v[240:241], off
	s_barrier
	s_waitcnt lgkmcnt(0)
	s_waitcnt lgkmcnt(0)
	v_mfma_f32_16x16x32_bf16 v[116:119], v[222:225], v[160:163], v[116:119]
	v_mfma_f32_16x16x32_bf16 v[108:111], v[230:233], v[160:163], v[108:111]
	v_mfma_f32_16x16x32_bf16 v[100:103], v[222:225], v[182:185], v[100:103]
	v_mfma_f32_16x16x32_bf16 v[92:95], v[230:233], v[182:185], v[92:95]
	v_mfma_f32_16x16x32_bf16 v[84:87], v[222:225], v[198:201], v[84:87]
	v_mfma_f32_16x16x32_bf16 v[76:79], v[230:233], v[198:201], v[76:79]
	v_mfma_f32_16x16x32_bf16 v[72:75], v[222:225], v[214:217], v[72:75]
	v_mfma_f32_16x16x32_bf16 v[68:71], v[230:233], v[214:217], v[68:71]
	v_mfma_f32_16x16x32_bf16 v[116:119], v[226:229], v[164:167], v[116:119]
	v_mfma_f32_16x16x32_bf16 v[108:111], v[234:237], v[164:167], v[108:111]
	v_mfma_f32_16x16x32_bf16 v[100:103], v[226:229], v[194:197], v[100:103]
	v_mfma_f32_16x16x32_bf16 v[92:95], v[234:237], v[194:197], v[92:95]
	v_mfma_f32_16x16x32_bf16 v[84:87], v[226:229], v[202:205], v[84:87]
	v_mfma_f32_16x16x32_bf16 v[76:79], v[234:237], v[202:205], v[76:79]
	v_mfma_f32_16x16x32_bf16 v[72:75], v[226:229], v[218:221], v[72:75]
	v_mfma_f32_16x16x32_bf16 v[68:71], v[234:237], v[218:221], v[68:71]
	s_mov_b32 m0, s59
	s_barrier
	ds_read_b128 v[160:163], v189 offset:16384
	ds_read_b128 v[164:167], v189 offset:17408
	ds_read_b128 v[182:185], v189 offset:18432
	ds_read_b128 v[194:197], v189 offset:19456
	ds_read_b128 v[198:201], v189 offset:20480
	ds_read_b128 v[202:205], v189 offset:21504
	ds_read_b128 v[214:217], v189 offset:22528
	ds_read_b128 v[218:221], v189 offset:23552
	global_load_lds_dwordx4 v2, s[40:41]
	s_mov_b32 m0, s60
	v_mov_b32_e32 v207, v3
	global_load_lds_dwordx4 v206, s[40:41]
	s_barrier
	s_waitcnt lgkmcnt(0)
	v_lshl_add_u64 v[242:243], s[40:41], 0, v[2:3]
	v_lshl_add_u64 v[206:207], s[40:41], 0, v[206:207]
	s_waitcnt lgkmcnt(0)
	v_mfma_f32_16x16x32_bf16 v[64:67], v[144:147], v[160:163], v[64:67]
	v_mfma_f32_16x16x32_bf16 v[60:63], v[152:155], v[160:163], v[60:63]
	v_mfma_f32_16x16x32_bf16 v[48:51], v[144:147], v[182:185], v[48:51]
	v_mfma_f32_16x16x32_bf16 v[40:43], v[152:155], v[182:185], v[40:43]
	v_mfma_f32_16x16x32_bf16 v[24:27], v[144:147], v[198:201], v[24:27]
	v_mfma_f32_16x16x32_bf16 v[16:19], v[152:155], v[198:201], v[16:19]
	v_mfma_f32_16x16x32_bf16 v[8:11], v[144:147], v[214:217], v[8:11]
	v_mfma_f32_16x16x32_bf16 v[4:7], v[152:155], v[214:217], v[4:7]
	v_mfma_f32_16x16x32_bf16 v[64:67], v[148:151], v[164:167], v[64:67]
	v_mfma_f32_16x16x32_bf16 v[60:63], v[156:159], v[164:167], v[60:63]
	v_mfma_f32_16x16x32_bf16 v[48:51], v[148:151], v[194:197], v[48:51]
	v_mfma_f32_16x16x32_bf16 v[40:43], v[156:159], v[194:197], v[40:43]
	v_mfma_f32_16x16x32_bf16 v[24:27], v[148:151], v[202:205], v[24:27]
	v_mfma_f32_16x16x32_bf16 v[16:19], v[156:159], v[202:205], v[16:19]
	v_mfma_f32_16x16x32_bf16 v[8:11], v[148:151], v[218:221], v[8:11]
	v_mfma_f32_16x16x32_bf16 v[4:7], v[156:159], v[218:221], v[4:7]
	s_barrier
	s_add_u32 s72, s34, 0x18000
	s_addc_u32 s73, s35, 0
	s_add_i32 s36, s36, s58
	v_lshl_add_u64 v[144:145], s[72:73], 0, v[168:169]
	s_mov_b32 m0, s36
	s_nop 0
	global_load_lds_dwordx4 v[144:145], off
	v_lshl_add_u64 v[144:145], s[72:73], 0, v[170:171]
	s_add_i32 m0, s36, 0x2000
	s_nop 0
	global_load_lds_dwordx4 v[144:145], off
	s_waitcnt vmcnt(6)
	s_barrier
	v_mfma_f32_16x16x32_bf16 v[44:47], v[222:225], v[160:163], v[44:47]
	v_mfma_f32_16x16x32_bf16 v[36:39], v[230:233], v[160:163], v[36:39]
	v_mfma_f32_16x16x32_bf16 v[20:23], v[222:225], v[182:185], v[20:23]
	v_mfma_f32_16x16x32_bf16 v[12:15], v[230:233], v[182:185], v[12:15]
	v_mfma_f32_16x16x32_bf16 v[52:55], v[222:225], v[198:201], v[52:55]
	v_mfma_f32_16x16x32_bf16 v[56:59], v[230:233], v[198:201], v[56:59]
	v_mfma_f32_16x16x32_bf16 v[28:31], v[222:225], v[214:217], v[28:31]
	v_mfma_f32_16x16x32_bf16 v[32:35], v[230:233], v[214:217], v[32:35]
	v_mfma_f32_16x16x32_bf16 v[44:47], v[226:229], v[164:167], v[44:47]
	v_mfma_f32_16x16x32_bf16 v[36:39], v[234:237], v[164:167], v[36:39]
	v_mfma_f32_16x16x32_bf16 v[20:23], v[226:229], v[194:197], v[20:23]
	v_mfma_f32_16x16x32_bf16 v[12:15], v[234:237], v[194:197], v[12:15]
	v_mfma_f32_16x16x32_bf16 v[52:55], v[226:229], v[202:205], v[52:55]
	v_mfma_f32_16x16x32_bf16 v[56:59], v[234:237], v[202:205], v[56:59]
	v_mfma_f32_16x16x32_bf16 v[28:31], v[226:229], v[218:221], v[28:31]
	v_mfma_f32_16x16x32_bf16 v[32:35], v[234:237], v[218:221], v[32:35]
	s_add_i32 s36, 0, 0x18000
	v_add_u32_e32 v2, s36, v188
	s_barrier
	ds_read_b128 v[144:147], v2
	ds_read_b128 v[148:151], v2 offset:1024
	ds_read_b128 v[152:155], v2 offset:2048
	ds_read_b128 v[156:159], v2 offset:3072
	s_mov_b32 m0, s61
	ds_read_b128 v[160:163], v189 offset:32768
	ds_read_b128 v[164:167], v189 offset:33792
	ds_read_b128 v[182:185], v189 offset:34816
	ds_read_b128 v[194:197], v189 offset:35840
	ds_read_b128 v[198:201], v189 offset:36864
	ds_read_b128 v[202:205], v189 offset:37888
	ds_read_b128 v[214:217], v189 offset:38912
	ds_read_b128 v[218:221], v189 offset:39936
	global_load_lds_dwordx4 v133, s[40:41]
	s_mov_b32 m0, s62
	s_nop 0
	global_load_lds_dwordx4 v135, s[40:41]
	s_waitcnt lgkmcnt(8)
	s_barrier
	s_waitcnt lgkmcnt(0)
	s_waitcnt lgkmcnt(0)
	v_mfma_f32_16x16x32_bf16 v[128:131], v[144:147], v[160:163], v[128:131]
	v_mfma_f32_16x16x32_bf16 v[124:127], v[152:155], v[160:163], v[124:127]
	v_mfma_f32_16x16x32_bf16 v[120:123], v[144:147], v[182:185], v[120:123]
	v_mfma_f32_16x16x32_bf16 v[112:115], v[152:155], v[182:185], v[112:115]
	v_mfma_f32_16x16x32_bf16 v[104:107], v[144:147], v[198:201], v[104:107]
	v_mfma_f32_16x16x32_bf16 v[96:99], v[152:155], v[198:201], v[96:99]
	v_mfma_f32_16x16x32_bf16 v[88:91], v[144:147], v[214:217], v[88:91]
	v_mfma_f32_16x16x32_bf16 v[80:83], v[152:155], v[214:217], v[80:83]
	v_mfma_f32_16x16x32_bf16 v[128:131], v[148:151], v[164:167], v[128:131]
	v_mfma_f32_16x16x32_bf16 v[124:127], v[156:159], v[164:167], v[124:127]
	v_mfma_f32_16x16x32_bf16 v[120:123], v[148:151], v[194:197], v[120:123]
	v_mfma_f32_16x16x32_bf16 v[112:115], v[156:159], v[194:197], v[112:115]
	v_mfma_f32_16x16x32_bf16 v[104:107], v[148:151], v[202:205], v[104:107]
	v_mfma_f32_16x16x32_bf16 v[96:99], v[156:159], v[202:205], v[96:99]
	v_mfma_f32_16x16x32_bf16 v[88:91], v[148:151], v[218:221], v[88:91]
	v_mfma_f32_16x16x32_bf16 v[80:83], v[156:159], v[218:221], v[80:83]
	s_barrier
	s_add_i32 s40, 0, 0x1c000
	s_add_i32 s36, s36, s58
	v_add_u32_e32 v2, s40, v188
	v_lshl_add_u64 v[238:239], v[238:239], 0, s[8:9]
	s_mov_b32 m0, s36
	ds_read_b128 v[222:225], v2
	ds_read_b128 v[226:229], v2 offset:1024
	ds_read_b128 v[230:233], v2 offset:2048
	ds_read_b128 v[234:237], v2 offset:3072
	global_load_lds_dwordx4 v[238:239], off
	v_lshl_add_u64 v[238:239], v[240:241], 0, s[8:9]
	s_add_i32 m0, s36, 0x2000
	s_nop 0
	global_load_lds_dwordx4 v[238:239], off
	s_barrier
	s_waitcnt lgkmcnt(0)
	s_waitcnt lgkmcnt(0)
	v_mfma_f32_16x16x32_bf16 v[116:119], v[222:225], v[160:163], v[116:119]
	v_mfma_f32_16x16x32_bf16 v[108:111], v[230:233], v[160:163], v[108:111]
	v_mfma_f32_16x16x32_bf16 v[100:103], v[222:225], v[182:185], v[100:103]
	v_mfma_f32_16x16x32_bf16 v[92:95], v[230:233], v[182:185], v[92:95]
	v_mfma_f32_16x16x32_bf16 v[84:87], v[222:225], v[198:201], v[84:87]
	v_mfma_f32_16x16x32_bf16 v[76:79], v[230:233], v[198:201], v[76:79]
	v_mfma_f32_16x16x32_bf16 v[72:75], v[222:225], v[214:217], v[72:75]
	v_mfma_f32_16x16x32_bf16 v[68:71], v[230:233], v[214:217], v[68:71]
	v_mfma_f32_16x16x32_bf16 v[116:119], v[226:229], v[164:167], v[116:119]
	v_mfma_f32_16x16x32_bf16 v[108:111], v[234:237], v[164:167], v[108:111]
	v_mfma_f32_16x16x32_bf16 v[100:103], v[226:229], v[194:197], v[100:103]
	v_mfma_f32_16x16x32_bf16 v[92:95], v[234:237], v[194:197], v[92:95]
	v_mfma_f32_16x16x32_bf16 v[84:87], v[226:229], v[202:205], v[84:87]
	v_mfma_f32_16x16x32_bf16 v[76:79], v[234:237], v[202:205], v[76:79]
	v_mfma_f32_16x16x32_bf16 v[72:75], v[226:229], v[218:221], v[72:75]
	v_mfma_f32_16x16x32_bf16 v[68:71], v[234:237], v[218:221], v[68:71]
	s_mov_b32 m0, s63
	v_lshl_add_u64 v[238:239], v[242:243], 0, s[8:9]
	s_barrier
	ds_read_b128 v[160:163], v189 offset:49152
	ds_read_b128 v[164:167], v189 offset:50176
	ds_read_b128 v[182:185], v189 offset:51200
	ds_read_b128 v[194:197], v189 offset:52224
	ds_read_b128 v[198:201], v189 offset:53248
	ds_read_b128 v[202:205], v189 offset:54272
	ds_read_b128 v[214:217], v189 offset:55296
	ds_read_b128 v[218:221], v189 offset:56320
	global_load_lds_dwordx4 v[238:239], off
	v_lshl_add_u64 v[206:207], v[206:207], 0, s[8:9]
	s_mov_b32 m0, s64
	s_nop 0
	global_load_lds_dwordx4 v[206:207], off
	s_barrier
	s_waitcnt lgkmcnt(0)
	s_waitcnt lgkmcnt(0)
	v_mfma_f32_16x16x32_bf16 v[64:67], v[144:147], v[160:163], v[64:67]
	v_mfma_f32_16x16x32_bf16 v[60:63], v[152:155], v[160:163], v[60:63]
	v_mfma_f32_16x16x32_bf16 v[48:51], v[144:147], v[182:185], v[48:51]
	v_mfma_f32_16x16x32_bf16 v[40:43], v[152:155], v[182:185], v[40:43]
	v_mfma_f32_16x16x32_bf16 v[24:27], v[144:147], v[198:201], v[24:27]
	v_mfma_f32_16x16x32_bf16 v[16:19], v[152:155], v[198:201], v[16:19]
	v_mfma_f32_16x16x32_bf16 v[8:11], v[144:147], v[214:217], v[8:11]
	v_mfma_f32_16x16x32_bf16 v[4:7], v[152:155], v[214:217], v[4:7]
	v_mfma_f32_16x16x32_bf16 v[64:67], v[148:151], v[164:167], v[64:67]
	v_mfma_f32_16x16x32_bf16 v[60:63], v[156:159], v[164:167], v[60:63]
	v_mfma_f32_16x16x32_bf16 v[48:51], v[148:151], v[194:197], v[48:51]
	v_mfma_f32_16x16x32_bf16 v[40:43], v[156:159], v[194:197], v[40:43]
	v_mfma_f32_16x16x32_bf16 v[24:27], v[148:151], v[202:205], v[24:27]
	v_mfma_f32_16x16x32_bf16 v[16:19], v[156:159], v[202:205], v[16:19]
	v_mfma_f32_16x16x32_bf16 v[8:11], v[148:151], v[218:221], v[8:11]
	v_mfma_f32_16x16x32_bf16 v[4:7], v[156:159], v[218:221], v[4:7]
	s_barrier
	s_add_u32 s34, s34, 0x18080
	s_addc_u32 s35, s35, 0
	s_add_i32 s36, s40, s58
	v_lshl_add_u64 v[144:145], s[34:35], 0, v[168:169]
	s_mov_b32 m0, s36
	s_nop 0
	global_load_lds_dwordx4 v[144:145], off
	v_lshl_add_u64 v[144:145], s[34:35], 0, v[170:171]
	s_add_i32 m0, s36, 0x2000
	s_nop 0
	global_load_lds_dwordx4 v[144:145], off
	s_waitcnt vmcnt(6)
	s_barrier
	v_mfma_f32_16x16x32_bf16 v[44:47], v[222:225], v[160:163], v[44:47]
	v_mfma_f32_16x16x32_bf16 v[36:39], v[230:233], v[160:163], v[36:39]
	v_mfma_f32_16x16x32_bf16 v[20:23], v[222:225], v[182:185], v[20:23]
	v_mfma_f32_16x16x32_bf16 v[12:15], v[230:233], v[182:185], v[12:15]
	v_mfma_f32_16x16x32_bf16 v[52:55], v[222:225], v[198:201], v[52:55]
	v_mfma_f32_16x16x32_bf16 v[56:59], v[230:233], v[198:201], v[56:59]
	v_mfma_f32_16x16x32_bf16 v[28:31], v[222:225], v[214:217], v[28:31]
	v_mfma_f32_16x16x32_bf16 v[32:35], v[230:233], v[214:217], v[32:35]
	v_mfma_f32_16x16x32_bf16 v[44:47], v[226:229], v[164:167], v[44:47]
	v_mfma_f32_16x16x32_bf16 v[36:39], v[234:237], v[164:167], v[36:39]
	v_mfma_f32_16x16x32_bf16 v[20:23], v[226:229], v[194:197], v[20:23]
	v_mfma_f32_16x16x32_bf16 v[12:15], v[234:237], v[194:197], v[12:15]
	v_mfma_f32_16x16x32_bf16 v[52:55], v[226:229], v[202:205], v[52:55]
	v_mfma_f32_16x16x32_bf16 v[56:59], v[234:237], v[202:205], v[56:59]
	v_mfma_f32_16x16x32_bf16 v[28:31], v[226:229], v[218:221], v[28:31]
	v_mfma_f32_16x16x32_bf16 v[32:35], v[234:237], v[218:221], v[32:35]
	s_add_i32 s71, s71, 2
	s_add_u32 s2, s2, 0x100
	s_addc_u32 s3, s3, 0
	s_cmp_gt_u32 s71, 3
	s_barrier
	s_cbranch_scc0 .LBB0_764
	v_lshl_add_u32 v173, s70, 8, v187
	v_mov_b64_e32 v[184:185], s[52:53]
	v_mad_i64_i32 v[140:141], s[0:1], v173, s6, v[184:185]
	global_load_dwordx4 v[132:135], v[140:141], off offset:32
	global_load_dwordx4 v[136:139], v[140:141], off offset:16
	s_nop 0
	global_load_dwordx4 v[140:143], v[140:141], off
	v_or_b32_e32 v196, 16, v173
	v_mad_i64_i32 v[152:153], s[0:1], v196, s6, v[184:185]
	global_load_dwordx4 v[144:147], v[152:153], off offset:32
	global_load_dwordx4 v[148:151], v[152:153], off offset:16
	s_nop 0
	global_load_dwordx4 v[152:155], v[152:153], off
	v_or_b32_e32 v195, 32, v173
	v_mad_i64_i32 v[164:165], s[0:1], v195, s6, v[184:185]
	global_load_dwordx4 v[156:159], v[164:165], off offset:32
	global_load_dwordx4 v[160:163], v[164:165], off offset:16
	s_nop 0
	global_load_dwordx4 v[164:167], v[164:165], off
	v_or_b32_e32 v194, 48, v173
	v_mad_i64_i32 v[182:183], s[0:1], v194, s6, v[184:185]
	global_load_dwordx4 v[198:201], v[182:183], off offset:32
	global_load_dwordx4 v[202:205], v[182:183], off offset:16
	global_load_dwordx4 v[214:217], v[182:183], off
	s_mov_b32 s0, 0x358637bd
	v_mov_b64_e32 v[182:183], s[0:1]
	s_mov_b32 s2, 0x3b2aaaab
	v_add_u32_e32 v197, 0xa0, v173
	s_movk_i32 s34, 0x600
	s_mov_b32 s70, s68
	s_movk_i32 s36, 0x1ff
	s_waitcnt vmcnt(0)
	v_add_f32_e32 v136, v136, v137
	v_add_f32_e32 v140, v140, v141
	v_add_f32_e32 v142, v142, v143
	v_add_f32_e32 v138, v138, v139
	v_mov_b32_e32 v141, v132
	v_mov_b32_e32 v143, v133
	v_mov_b32_e32 v137, v134
	v_mov_b32_e32 v139, v135
	v_pk_add_f32 v[132:133], v[140:141], v[142:143]
	v_pk_add_f32 v[134:135], v[136:137], v[138:139]
	v_add_f32_e32 v136, v154, v155
	v_pk_add_f32 v[132:133], v[132:133], v[134:135]
	v_add_f32_e32 v134, v152, v153
	v_add_f32_e32 v138, v148, v149
	v_add_f32_e32 v140, v150, v151
	v_mov_b32_e32 v135, v144
	v_mov_b32_e32 v137, v145
	v_mov_b32_e32 v139, v146
	v_mov_b32_e32 v141, v147
	v_pk_add_f32 v[134:135], v[134:135], v[136:137]
	v_pk_add_f32 v[136:137], v[138:139], v[140:141]
	v_add_f32_e32 v138, v162, v163
	v_pk_add_f32 v[134:135], v[134:135], v[136:137]
	v_mov_b32_e32 v137, v132
	v_mov_b32_e32 v136, v134
	v_mov_b32_e32 v132, v135
	v_pk_add_f32 v[132:133], v[136:137], v[132:133]
	v_add_f32_e32 v134, v166, v167
	v_pk_fma_f32 v[132:133], v[132:133], s[2:3], v[182:183] op_sel_hi:[1,0,0]
	v_add_f32_e32 v136, v160, v161
	v_mul_f32_e32 v2, 0x4b800000, v133
	v_cmp_gt_f32_e64 s[40:41], s33, v133
	v_cmp_gt_f32_e32 vcc, s33, v132
	v_mov_b32_e32 v135, v157
	v_cndmask_b32_e64 v2, v133, v2, s[40:41]
	v_rsq_f32_e32 v2, v2
	v_mov_b32_e32 v137, v158
	v_mov_b32_e32 v139, v159
	v_add_f32_e32 v140, v204, v205
	v_mul_f32_e32 v133, 0x45800000, v2
	v_cndmask_b32_e64 v2, v2, v133, s[40:41]
	v_mul_f32_e32 v178, 0x3e16c740, v2
	v_mul_f32_e32 v2, 0x4b800000, v132
	v_cndmask_b32_e32 v2, v132, v2, vcc
	v_rsq_f32_e32 v2, v2
	v_mov_b32_e32 v133, v156
	v_mov_b32_e32 v141, v201
	v_pk_mul_f32 v[128:129], v[128:129], v[178:179] op_sel_hi:[1,0]
	v_mul_f32_e32 v132, 0x45800000, v2
	v_cndmask_b32_e32 v2, v2, v132, vcc
	v_add_f32_e32 v132, v164, v165
	v_pk_add_f32 v[132:133], v[132:133], v[134:135]
	v_pk_add_f32 v[134:135], v[136:137], v[138:139]
	v_add_f32_e32 v136, v216, v217
	v_pk_add_f32 v[132:133], v[132:133], v[134:135]
	v_add_f32_e32 v134, v214, v215
	v_add_f32_e32 v138, v202, v203
	v_mov_b32_e32 v135, v198
	v_mov_b32_e32 v137, v199
	v_mov_b32_e32 v139, v200
	v_pk_add_f32 v[134:135], v[134:135], v[136:137]
	v_pk_add_f32 v[136:137], v[138:139], v[140:141]
	v_mul_f32_e32 v176, 0x3e16c740, v2
	v_pk_add_f32 v[134:135], v[134:135], v[136:137]
	v_mov_b32_e32 v137, v132
	v_mov_b32_e32 v136, v134
	v_mov_b32_e32 v132, v135
	v_pk_add_f32 v[132:133], v[136:137], v[132:133]
	v_add_u32_e32 v199, 0x80, v173
	v_pk_fma_f32 v[132:133], v[132:133], s[2:3], v[182:183] op_sel_hi:[1,0,0]
	v_add_u32_e32 v198, 0x90, v173
	v_mul_f32_e32 v2, 0x4b800000, v133
	v_cmp_gt_f32_e64 s[40:41], s33, v133
	v_cmp_gt_f32_e32 vcc, s33, v132
	v_mad_i64_i32 v[164:165], s[0:1], v197, s6, v[184:185]
	v_cndmask_b32_e64 v2, v133, v2, s[40:41]
	v_rsq_f32_e32 v2, v2
	v_add_u32_e32 v200, 0xb0, v173
	v_pk_mul_f32 v[124:125], v[124:125], v[178:179] op_sel_hi:[1,0]
	v_pk_mul_f32 v[130:131], v[130:131], v[178:179] op_sel_hi:[1,0]
	v_mul_f32_e32 v133, 0x45800000, v2
	v_cndmask_b32_e64 v2, v2, v133, s[40:41]
	v_mul_f32_e32 v174, 0x3e16c740, v2
	v_mul_f32_e32 v2, 0x4b800000, v132
	v_cndmask_b32_e32 v2, v132, v2, vcc
	v_rsq_f32_e32 v2, v2
	v_pk_mul_f32 v[118:119], v[118:119], v[178:179] op_sel_hi:[1,0]
	v_pk_mul_f32 v[116:117], v[116:117], v[178:179] op_sel_hi:[1,0]
	v_pk_mul_f32 v[112:113], v[112:113], v[176:177] op_sel_hi:[1,0]
	v_mul_f32_e32 v132, 0x45800000, v2
	v_cndmask_b32_e32 v2, v2, v132, vcc
	v_mad_i64_i32 v[132:133], s[0:1], v199, s6, v[184:185]
	global_load_dwordx4 v[136:139], v[132:133], off offset:32
	global_load_dwordx4 v[144:147], v[132:133], off offset:16
	global_load_dwordx4 v[148:151], v[132:133], off
	v_mad_i64_i32 v[132:133], s[0:1], v198, s6, v[184:185]
	global_load_dwordx4 v[140:143], v[132:133], off offset:32
	global_load_dwordx4 v[156:159], v[132:133], off offset:16
	global_load_dwordx4 v[160:163], v[132:133], off
	s_nop 0
	global_load_dwordx4 v[132:135], v[164:165], off offset:32
	global_load_dwordx4 v[152:155], v[164:165], off offset:16
	s_nop 0
	global_load_dwordx4 v[164:167], v[164:165], off
	v_mad_i64_i32 v[184:185], s[0:1], v200, s6, v[184:185]
	global_load_dwordx4 v[202:205], v[184:185], off offset:32
	global_load_dwordx4 v[214:217], v[184:185], off offset:16
	global_load_dwordx4 v[218:221], v[184:185], off
	s_lshl_b32 s0, s69, 8
	s_ashr_i32 s1, s0, 31
	v_pk_mul_f32 v[114:115], v[114:115], v[176:177] op_sel_hi:[1,0]
	v_pk_mul_f32 v[102:103], v[102:103], v[176:177] op_sel_hi:[1,0]
	v_pk_mul_f32 v[100:101], v[100:101], v[176:177] op_sel_hi:[1,0]
	v_pk_mul_f32 v[96:97], v[96:97], v[174:175] op_sel_hi:[1,0]
	v_pk_mul_f32 v[98:99], v[98:99], v[174:175] op_sel_hi:[1,0]
	v_pk_mul_f32 v[86:87], v[86:87], v[174:175] op_sel_hi:[1,0]
	v_pk_mul_f32 v[84:85], v[84:85], v[174:175] op_sel_hi:[1,0]
	v_mul_f32_e32 v2, 0x3e16c740, v2
	v_pk_mul_f32 v[80:81], v[80:81], v[2:3] op_sel_hi:[1,0]
	v_pk_mul_f32 v[82:83], v[82:83], v[2:3] op_sel_hi:[1,0]
	v_pk_mul_f32 v[74:75], v[74:75], v[2:3] op_sel_hi:[1,0]
	v_pk_mul_f32 v[72:73], v[72:73], v[2:3] op_sel_hi:[1,0]
	s_mov_b32 s69, s67
	s_waitcnt vmcnt(0)
	v_add_f32_e32 v144, v144, v145
	v_add_f32_e32 v148, v148, v149
	v_add_f32_e32 v150, v150, v151
	v_add_f32_e32 v146, v146, v147
	v_mov_b32_e32 v149, v136
	v_mov_b32_e32 v151, v137
	v_mov_b32_e32 v145, v138
	v_mov_b32_e32 v147, v139
	v_pk_add_f32 v[136:137], v[148:149], v[150:151]
	v_pk_add_f32 v[138:139], v[144:145], v[146:147]
	v_add_f32_e32 v144, v162, v163
	v_pk_add_f32 v[136:137], v[136:137], v[138:139]
	v_add_f32_e32 v138, v160, v161
	v_add_f32_e32 v146, v156, v157
	v_add_f32_e32 v148, v158, v159
	v_mov_b32_e32 v139, v140
	v_mov_b32_e32 v145, v141
	v_mov_b32_e32 v147, v142
	v_mov_b32_e32 v149, v143
	v_pk_add_f32 v[138:139], v[138:139], v[144:145]
	v_pk_add_f32 v[140:141], v[146:147], v[148:149]
	v_add_f32_e32 v142, v166, v167
	v_pk_add_f32 v[138:139], v[138:139], v[140:141]
	v_mov_b32_e32 v141, v136
	v_mov_b32_e32 v140, v138
	v_mov_b32_e32 v136, v139
	v_pk_add_f32 v[136:137], v[140:141], v[136:137]
	v_add_f32_e32 v140, v164, v165
	v_add_f32_e32 v144, v152, v153
	v_add_f32_e32 v146, v154, v155
	v_mov_b32_e32 v141, v132
	v_mov_b32_e32 v143, v133
	v_mov_b32_e32 v145, v134
	v_mov_b32_e32 v147, v135
	v_pk_add_f32 v[132:133], v[140:141], v[142:143]
	v_pk_add_f32 v[134:135], v[144:145], v[146:147]
	v_add_f32_e32 v140, v220, v221
	v_pk_add_f32 v[132:133], v[132:133], v[134:135]
	v_add_f32_e32 v134, v218, v219
	v_add_f32_e32 v142, v214, v215
	v_add_f32_e32 v144, v216, v217
	v_mov_b32_e32 v135, v202
	v_mov_b32_e32 v141, v203
	v_mov_b32_e32 v143, v204
	v_mov_b32_e32 v145, v205
	v_pk_add_f32 v[134:135], v[134:135], v[140:141]
	v_pk_add_f32 v[140:141], v[142:143], v[144:145]
	v_pk_fma_f32 v[136:137], v[136:137], s[2:3], v[182:183] op_sel_hi:[1,0,0]
	v_pk_add_f32 v[134:135], v[134:135], v[140:141]
	v_mov_b32_e32 v141, v132
	v_mov_b32_e32 v140, v134
	v_mov_b32_e32 v132, v135
	v_pk_add_f32 v[132:133], v[140:141], v[132:133]
	v_pk_mul_f32 v[140:141], v[126:127], v[178:179] op_sel_hi:[1,0]
	v_cvt_pk_bf16_f32 v126, v128, v129
	v_cvt_pk_bf16_f32 v128, v124, v125
	v_mov_b64_e32 v[124:125], s[50:51]
	v_pk_fma_f32 v[132:133], v[132:133], s[2:3], v[182:183] op_sel_hi:[1,0,0]
	v_cvt_pk_bf16_f32 v127, v130, v131
	v_mad_i64_i32 v[130:131], s[2:3], v173, s34, v[124:125]
	s_lshl_b64 s[2:3], s[0:1], 1
	s_nop 0
	v_lshl_add_u64 v[130:131], v[130:131], 0, s[2:3]
	v_lshl_add_u64 v[130:131], v[130:131], 0, s[30:31]
	v_mov_b32_e32 v173, v3
	v_cvt_pk_bf16_f32 v129, v140, v141
	v_lshl_add_u64 v[130:131], v[130:131], 0, v[172:173]
	global_store_dwordx4 v[130:131], v[126:129], off
	v_mul_f32_e32 v138, 0x4b800000, v137
	v_cmp_gt_f32_e64 s[40:41], s33, v137
	v_pk_mul_f32 v[126:127], v[110:111], v[178:179] op_sel_hi:[1,0]
	v_pk_mul_f32 v[110:111], v[108:109], v[178:179] op_sel_hi:[1,0]
	v_cvt_pk_bf16_f32 v108, v116, v117
	v_cvt_pk_bf16_f32 v109, v118, v119
	v_cvt_pk_bf16_f32 v110, v110, v111
	v_cvt_pk_bf16_f32 v111, v126, v127
	global_store_dwordx4 v[130:131], v[108:111], off offset:256
	v_cndmask_b32_e64 v137, v137, v138, s[40:41]
	v_rsq_f32_e32 v137, v137
	v_pk_mul_f32 v[110:111], v[122:123], v[176:177] op_sel_hi:[1,0]
	v_pk_mul_f32 v[108:109], v[120:121], v[176:177] op_sel_hi:[1,0]
	v_cmp_gt_f32_e32 vcc, s33, v136
	v_cvt_pk_bf16_f32 v108, v108, v109
	v_cvt_pk_bf16_f32 v109, v110, v111
	v_cvt_pk_bf16_f32 v110, v112, v113
	v_mad_i64_i32 v[112:113], s[0:1], v196, s34, v[124:125]
	v_lshl_add_u64 v[112:113], v[112:113], 0, s[2:3]
	v_lshl_add_u64 v[112:113], v[112:113], 0, s[30:31]
	v_cvt_pk_bf16_f32 v111, v114, v115
	v_lshl_add_u64 v[112:113], v[112:113], 0, v[172:173]
	global_store_dwordx4 v[112:113], v[108:111], off
	v_mul_f32_e32 v138, 0x45800000, v137
	v_cndmask_b32_e64 v137, v137, v138, s[40:41]
	v_pk_mul_f32 v[108:109], v[94:95], v[176:177] op_sel_hi:[1,0]
	v_pk_mul_f32 v[94:95], v[92:93], v[176:177] op_sel_hi:[1,0]
	v_cvt_pk_bf16_f32 v92, v100, v101
	v_cvt_pk_bf16_f32 v93, v102, v103
	v_cvt_pk_bf16_f32 v94, v94, v95
	v_cvt_pk_bf16_f32 v95, v108, v109
	global_store_dwordx4 v[112:113], v[92:95], off offset:256
	v_mul_f32_e32 v138, 0x3e16c740, v137
	v_mul_f32_e32 v137, 0x4b800000, v136
	v_pk_mul_f32 v[94:95], v[106:107], v[174:175] op_sel_hi:[1,0]
	v_pk_mul_f32 v[92:93], v[104:105], v[174:175] op_sel_hi:[1,0]
	v_cndmask_b32_e32 v136, v136, v137, vcc
	v_cvt_pk_bf16_f32 v92, v92, v93
	v_cvt_pk_bf16_f32 v93, v94, v95
	v_cvt_pk_bf16_f32 v94, v96, v97
	v_mad_i64_i32 v[96:97], s[0:1], v195, s34, v[124:125]
	v_lshl_add_u64 v[96:97], v[96:97], 0, s[2:3]
	v_lshl_add_u64 v[96:97], v[96:97], 0, s[30:31]
	v_cvt_pk_bf16_f32 v95, v98, v99
	v_lshl_add_u64 v[96:97], v[96:97], 0, v[172:173]
	global_store_dwordx4 v[96:97], v[92:95], off
	v_rsq_f32_e32 v136, v136
	v_pk_mul_f32 v[64:65], v[64:65], v[138:139] op_sel_hi:[1,0]
	v_pk_mul_f32 v[92:93], v[78:79], v[174:175] op_sel_hi:[1,0]
	v_pk_mul_f32 v[78:79], v[76:77], v[174:175] op_sel_hi:[1,0]
	v_cvt_pk_bf16_f32 v76, v84, v85
	v_cvt_pk_bf16_f32 v77, v86, v87
	v_cvt_pk_bf16_f32 v78, v78, v79
	v_cvt_pk_bf16_f32 v79, v92, v93
	global_store_dwordx4 v[96:97], v[76:79], off offset:256
	v_mul_f32_e32 v134, 0x4b800000, v133
	v_cmp_gt_f32_e64 s[40:41], s33, v133
	v_pk_mul_f32 v[78:79], v[90:91], v[2:3] op_sel_hi:[1,0]
	v_pk_mul_f32 v[76:77], v[88:89], v[2:3] op_sel_hi:[1,0]
	v_pk_mul_f32 v[66:67], v[66:67], v[138:139] op_sel_hi:[1,0]
	v_cvt_pk_bf16_f32 v76, v76, v77
	v_cvt_pk_bf16_f32 v77, v78, v79
	v_cvt_pk_bf16_f32 v78, v80, v81
	v_mad_i64_i32 v[80:81], s[0:1], v194, s34, v[124:125]
	v_lshl_add_u64 v[80:81], v[80:81], 0, s[2:3]
	v_lshl_add_u64 v[80:81], v[80:81], 0, s[30:31]
	v_cvt_pk_bf16_f32 v79, v82, v83
	v_lshl_add_u64 v[80:81], v[80:81], 0, v[172:173]
	global_store_dwordx4 v[80:81], v[76:79], off
	v_mul_f32_e32 v137, 0x45800000, v136
	v_cndmask_b32_e64 v133, v133, v134, s[40:41]
	v_pk_mul_f32 v[76:77], v[70:71], v[2:3] op_sel_hi:[1,0]
	v_pk_mul_f32 v[70:71], v[68:69], v[2:3] op_sel_hi:[1,0]
	v_cvt_pk_bf16_f32 v68, v72, v73
	v_cvt_pk_bf16_f32 v69, v74, v75
	v_cvt_pk_bf16_f32 v70, v70, v71
	v_cvt_pk_bf16_f32 v71, v76, v77
	global_store_dwordx4 v[80:81], v[68:71], off offset:256
	v_cndmask_b32_e32 v136, v136, v137, vcc
	v_rsq_f32_e32 v133, v133
	v_pk_mul_f32 v[68:69], v[62:63], v[138:139] op_sel_hi:[1,0]
	v_pk_mul_f32 v[62:63], v[60:61], v[138:139] op_sel_hi:[1,0]
	v_cvt_pk_bf16_f32 v60, v64, v65
	v_mad_i64_i32 v[64:65], s[0:1], v199, s34, v[124:125]
	v_lshl_add_u64 v[64:65], v[64:65], 0, s[2:3]
	v_lshl_add_u64 v[64:65], v[64:65], 0, s[30:31]
	v_cvt_pk_bf16_f32 v61, v66, v67
	v_cvt_pk_bf16_f32 v62, v62, v63
	v_cvt_pk_bf16_f32 v63, v68, v69
	v_lshl_add_u64 v[64:65], v[64:65], 0, v[172:173]
	global_store_dwordx4 v[64:65], v[60:63], off
	v_pk_mul_f32 v[46:47], v[46:47], v[138:139] op_sel_hi:[1,0]
	v_pk_mul_f32 v[44:45], v[44:45], v[138:139] op_sel_hi:[1,0]
	v_pk_mul_f32 v[60:61], v[38:39], v[138:139] op_sel_hi:[1,0]
	v_pk_mul_f32 v[38:39], v[36:37], v[138:139] op_sel_hi:[1,0]
	v_mul_f32_e32 v136, 0x3e16c740, v136
	v_cvt_pk_bf16_f32 v36, v44, v45
	v_cvt_pk_bf16_f32 v37, v46, v47
	v_cvt_pk_bf16_f32 v38, v38, v39
	v_cvt_pk_bf16_f32 v39, v60, v61
	global_store_dwordx4 v[64:65], v[36:39], off offset:256
	v_pk_mul_f32 v[40:41], v[40:41], v[136:137] op_sel_hi:[1,0]
	v_mul_f32_e32 v134, 0x45800000, v133
	v_pk_mul_f32 v[38:39], v[50:51], v[136:137] op_sel_hi:[1,0]
	v_pk_mul_f32 v[36:37], v[48:49], v[136:137] op_sel_hi:[1,0]
	v_cndmask_b32_e64 v133, v133, v134, s[40:41]
	v_cvt_pk_bf16_f32 v36, v36, v37
	v_cvt_pk_bf16_f32 v37, v38, v39
	v_cvt_pk_bf16_f32 v38, v40, v41
	v_mad_i64_i32 v[40:41], s[0:1], v198, s34, v[124:125]
	v_lshl_add_u64 v[40:41], v[40:41], 0, s[2:3]
	v_pk_mul_f32 v[42:43], v[42:43], v[136:137] op_sel_hi:[1,0]
	v_lshl_add_u64 v[40:41], v[40:41], 0, s[30:31]
	v_cmp_gt_f32_e32 vcc, s33, v132
	v_mul_f32_e32 v134, 0x3e16c740, v133
	v_mul_f32_e32 v133, 0x4b800000, v132
	v_cvt_pk_bf16_f32 v39, v42, v43
	v_lshl_add_u64 v[40:41], v[40:41], 0, v[172:173]
	v_cndmask_b32_e32 v132, v132, v133, vcc
	global_store_dwordx4 v[40:41], v[36:39], off
	v_pk_mul_f32 v[22:23], v[22:23], v[136:137] op_sel_hi:[1,0]
	v_pk_mul_f32 v[20:21], v[20:21], v[136:137] op_sel_hi:[1,0]
	v_pk_mul_f32 v[36:37], v[14:15], v[136:137] op_sel_hi:[1,0]
	v_pk_mul_f32 v[14:15], v[12:13], v[136:137] op_sel_hi:[1,0]
	v_rsq_f32_e32 v132, v132
	v_cvt_pk_bf16_f32 v12, v20, v21
	v_cvt_pk_bf16_f32 v13, v22, v23
	v_cvt_pk_bf16_f32 v14, v14, v15
	v_cvt_pk_bf16_f32 v15, v36, v37
	global_store_dwordx4 v[40:41], v[12:15], off offset:256
	v_pk_mul_f32 v[16:17], v[16:17], v[134:135] op_sel_hi:[1,0]
	v_mul_f32_e32 v133, 0x45800000, v132
	v_pk_mul_f32 v[14:15], v[26:27], v[134:135] op_sel_hi:[1,0]
	v_pk_mul_f32 v[12:13], v[24:25], v[134:135] op_sel_hi:[1,0]
	v_pk_mul_f32 v[18:19], v[18:19], v[134:135] op_sel_hi:[1,0]
	v_cvt_pk_bf16_f32 v12, v12, v13
	v_cvt_pk_bf16_f32 v13, v14, v15
	v_cvt_pk_bf16_f32 v14, v16, v17
	v_mad_i64_i32 v[16:17], s[0:1], v197, s34, v[124:125]
	v_lshl_add_u64 v[16:17], v[16:17], 0, s[2:3]
	v_lshl_add_u64 v[16:17], v[16:17], 0, s[30:31]
	v_cndmask_b32_e32 v132, v132, v133, vcc
	v_cvt_pk_bf16_f32 v15, v18, v19
	v_lshl_add_u64 v[16:17], v[16:17], 0, v[172:173]
	v_mul_f32_e32 v132, 0x3e16c740, v132
	global_store_dwordx4 v[16:17], v[12:15], off
	v_pk_mul_f32 v[18:19], v[58:59], v[134:135] op_sel_hi:[1,0]
	v_pk_mul_f32 v[20:21], v[56:57], v[134:135] op_sel_hi:[1,0]
	v_pk_mul_f32 v[14:15], v[54:55], v[134:135] op_sel_hi:[1,0]
	v_pk_mul_f32 v[12:13], v[52:53], v[134:135] op_sel_hi:[1,0]
	v_pk_mul_f32 v[8:9], v[8:9], v[132:133] op_sel_hi:[1,0]
	v_cvt_pk_bf16_f32 v12, v12, v13
	v_cvt_pk_bf16_f32 v13, v14, v15
	v_cvt_pk_bf16_f32 v14, v20, v21
	v_cvt_pk_bf16_f32 v15, v18, v19
	global_store_dwordx4 v[16:17], v[12:15], off offset:256
	v_pk_mul_f32 v[10:11], v[10:11], v[132:133] op_sel_hi:[1,0]
	s_and_b64 vcc, exec, s[38:39]
	v_pk_mul_f32 v[12:13], v[6:7], v[132:133] op_sel_hi:[1,0]
	v_pk_mul_f32 v[6:7], v[4:5], v[132:133] op_sel_hi:[1,0]
	v_cvt_pk_bf16_f32 v4, v8, v9
	v_mad_i64_i32 v[8:9], s[0:1], v200, s34, v[124:125]
	v_lshl_add_u64 v[8:9], v[8:9], 0, s[2:3]
	v_lshl_add_u64 v[8:9], v[8:9], 0, s[30:31]
	v_cvt_pk_bf16_f32 v5, v10, v11
	v_cvt_pk_bf16_f32 v6, v6, v7
	v_cvt_pk_bf16_f32 v7, v12, v13
	v_lshl_add_u64 v[8:9], v[8:9], 0, v[172:173]
	global_store_dwordx4 v[8:9], v[4:7], off
	v_pk_mul_f32 v[10:11], v[34:35], v[132:133] op_sel_hi:[1,0]
	v_pk_mul_f32 v[12:13], v[32:33], v[132:133] op_sel_hi:[1,0]
	v_pk_mul_f32 v[6:7], v[30:31], v[132:133] op_sel_hi:[1,0]
	v_pk_mul_f32 v[4:5], v[28:29], v[132:133] op_sel_hi:[1,0]
	v_mov_b32_e32 v138, v193
	v_cvt_pk_bf16_f32 v4, v4, v5
	v_cvt_pk_bf16_f32 v5, v6, v7
	v_cvt_pk_bf16_f32 v6, v12, v13
	v_cvt_pk_bf16_f32 v7, v10, v11
	global_store_dwordx4 v[8:9], v[4:7], off offset:256
	v_mov_b32_e32 v136, v192
	v_mov_b32_e32 v134, v191
	v_mov_b32_e32 v132, v190
	s_mov_b64 s[2:3], s[42:43]
	s_cbranch_vccz .LBB0_755
	s_waitcnt vmcnt(0)
	s_cmpk_gt_u32 s24, 0xff
	s_cbranch_scc1 .LBB0_768
	s_barrier

.LBB0_781:
	s_add_u32 s62, s44, s34
	s_addc_u32 s63, s45, s35
	s_add_u32 s26, s62, 0x100
	s_addc_u32 s27, s63, 0
	s_and_b64 s[24:25], s[14:15], exec
	s_cselect_b32 s40, s44, s26
	s_cselect_b32 s41, s45, s27
	s_add_u32 s24, s2, s34
	s_addc_u32 s25, s3, s35
	s_add_u32 s26, s24, 0x100
	s_addc_u32 s27, s25, 0
	s_add_i32 s36, 0, 0x10000
	s_and_b64 s[24:25], s[14:15], exec
	s_cselect_b32 s61, s0, s27
	s_cselect_b32 s60, s1, s26
	s_add_i32 s81, s36, s66
	v_add_u32_e32 v2, s36, v217
	s_add_i32 m0, s47, 0xc000
	s_add_i32 s82, s47, 0xe000
	s_add_i32 s80, 0, 0x14000
	s_add_i32 s79, s81, 0x2000
	ds_read_b128 v[96:99], v2
	ds_read_b128 v[100:103], v2 offset:1024
	ds_read_b128 v[132:135], v2 offset:2048
	ds_read_b128 v[136:139], v2 offset:3072
	s_add_u32 s42, s60, 0x10000
	s_addc_u32 s43, s61, 0
	s_add_i32 s57, 0, 0x18000
	s_add_i32 s78, s80, s66
	s_add_i32 s30, s57, s66
	s_add_i32 s77, s78, 0x2000
	s_add_i32 s27, 0, 0x1c000
	s_add_i32 s26, s30, 0x2000
	s_add_u32 s34, s60, 0x10080
	s_addc_u32 s35, s61, 0
	s_add_i32 s25, s27, s66
	s_add_i32 s24, s25, 0x2000
	v_cndmask_b32_e64 v2, v84, v222, s[14:15]
	v_cndmask_b32_e64 v234, v86, v223, s[14:15]
	v_cndmask_b32_e64 v85, v88, v224, s[14:15]
	v_cndmask_b32_e64 v87, v90, v225, s[14:15]
	v_lshl_add_u64 v[200:201], s[62:63], 0, v[88:89]
	v_lshl_add_u64 v[200:201], v[200:201], 0, s[8:9]
	ds_read_b128 v[140:143], v221
	ds_read_b128 v[144:147], v221 offset:1024
	ds_read_b128 v[160:163], v221 offset:2048
	ds_read_b128 v[168:171], v221 offset:3072
	ds_read_b128 v[172:175], v221 offset:4096
	ds_read_b128 v[176:179], v221 offset:5120
	ds_read_b128 v[192:195], v221 offset:6144
	ds_read_b128 v[196:199], v221 offset:7168
	global_load_lds_dwordx4 v[200:201], off
	v_lshl_add_u64 v[200:201], s[62:63], 0, v[90:91]
	v_lshl_add_u64 v[200:201], v[200:201], 0, s[8:9]
	s_mov_b32 m0, s82
	s_nop 0
	global_load_lds_dwordx4 v[200:201], off
	s_waitcnt lgkmcnt(8)
	s_barrier
	s_waitcnt lgkmcnt(0)
	s_waitcnt lgkmcnt(0)
	v_mfma_f32_16x16x32_bf16 v[164:167], v[96:99], v[140:143], v[164:167]
	v_mfma_f32_16x16x32_bf16 v[156:159], v[132:135], v[140:143], v[156:159]
	v_mfma_f32_16x16x32_bf16 v[128:131], v[96:99], v[160:163], v[128:131]
	v_mfma_f32_16x16x32_bf16 v[124:127], v[132:135], v[160:163], v[124:127]
	v_mfma_f32_16x16x32_bf16 v[112:115], v[96:99], v[172:175], v[112:115]
	v_mfma_f32_16x16x32_bf16 v[108:111], v[132:135], v[172:175], v[108:111]
	v_mfma_f32_16x16x32_bf16 v[80:83], v[96:99], v[192:195], v[80:83]
	v_mfma_f32_16x16x32_bf16 v[76:79], v[132:135], v[192:195], v[76:79]
	v_mfma_f32_16x16x32_bf16 v[164:167], v[100:103], v[144:147], v[164:167]
	v_mfma_f32_16x16x32_bf16 v[156:159], v[136:139], v[144:147], v[156:159]
	v_mfma_f32_16x16x32_bf16 v[128:131], v[100:103], v[168:171], v[128:131]
	v_mfma_f32_16x16x32_bf16 v[124:127], v[136:139], v[168:171], v[124:127]
	v_mfma_f32_16x16x32_bf16 v[112:115], v[100:103], v[176:179], v[112:115]
	v_mfma_f32_16x16x32_bf16 v[108:111], v[136:139], v[176:179], v[108:111]
	v_mfma_f32_16x16x32_bf16 v[80:83], v[100:103], v[196:199], v[80:83]
	v_mfma_f32_16x16x32_bf16 v[76:79], v[136:139], v[196:199], v[76:79]
	s_barrier
	s_mov_b32 m0, s81
	v_add_u32_e32 v208, s80, v217
	v_lshl_add_u64 v[236:237], s[60:61], 0, v[182:183]
	ds_read_b128 v[200:203], v208
	ds_read_b128 v[204:207], v208 offset:1024
	ds_read_b128 v[226:229], v208 offset:2048
	ds_read_b128 v[230:233], v208 offset:3072
	global_load_lds_dwordx4 v[236:237], off
	v_lshl_add_u64 v[238:239], s[60:61], 0, v[184:185]
	s_mov_b32 m0, s79
	s_nop 0
	global_load_lds_dwordx4 v[238:239], off
	s_barrier
	s_waitcnt lgkmcnt(0)
	s_waitcnt lgkmcnt(0)
	v_mfma_f32_16x16x32_bf16 v[152:155], v[200:203], v[140:143], v[152:155]
	v_mfma_f32_16x16x32_bf16 v[120:123], v[200:203], v[160:163], v[120:123]
	v_mfma_f32_16x16x32_bf16 v[116:119], v[226:229], v[160:163], v[116:119]
	v_mfma_f32_16x16x32_bf16 v[104:107], v[200:203], v[172:175], v[104:107]
	v_mfma_f32_16x16x32_bf16 v[92:95], v[226:229], v[172:175], v[92:95]
	v_mfma_f32_16x16x32_bf16 v[72:75], v[200:203], v[192:195], v[72:75]
	v_mfma_f32_16x16x32_bf16 v[68:71], v[226:229], v[192:195], v[68:71]
	v_mfma_f32_16x16x32_bf16 v[152:155], v[204:207], v[144:147], v[152:155]
	v_mfma_f32_16x16x32_bf16 v[140:143], v[226:229], v[140:143], v[148:151]
	v_mfma_f32_16x16x32_bf16 v[120:123], v[204:207], v[168:171], v[120:123]
	v_mfma_f32_16x16x32_bf16 v[116:119], v[230:233], v[168:171], v[116:119]
	v_mfma_f32_16x16x32_bf16 v[104:107], v[204:207], v[176:179], v[104:107]
	v_mfma_f32_16x16x32_bf16 v[92:95], v[230:233], v[176:179], v[92:95]
	v_mfma_f32_16x16x32_bf16 v[72:75], v[204:207], v[196:199], v[72:75]
	v_mfma_f32_16x16x32_bf16 v[68:71], v[230:233], v[196:199], v[68:71]
	v_mfma_f32_16x16x32_bf16 v[140:143], v[230:233], v[144:147], v[140:143]
	s_mov_b32 m0, s47
	s_barrier
	ds_read_b128 v[144:147], v221 offset:16384
	ds_read_b128 v[148:151], v221 offset:17408
	ds_read_b128 v[160:163], v221 offset:18432
	ds_read_b128 v[168:171], v221 offset:19456
	ds_read_b128 v[172:175], v221 offset:20480
	ds_read_b128 v[176:179], v221 offset:21504
	ds_read_b128 v[192:195], v221 offset:22528
	ds_read_b128 v[196:199], v221 offset:23552
	global_load_lds_dwordx4 v2, s[40:41]
	s_mov_b32 m0, s67
	v_mov_b32_e32 v235, v3
	global_load_lds_dwordx4 v234, s[40:41]
	s_barrier
	s_waitcnt lgkmcnt(0)
	v_lshl_add_u64 v[240:241], s[40:41], 0, v[2:3]
	v_lshl_add_u64 v[234:235], s[40:41], 0, v[234:235]
	s_waitcnt lgkmcnt(0)
	v_mfma_f32_16x16x32_bf16 v[64:67], v[96:99], v[144:147], v[64:67]
	v_mfma_f32_16x16x32_bf16 v[60:63], v[132:135], v[144:147], v[60:63]
	v_mfma_f32_16x16x32_bf16 v[48:51], v[96:99], v[160:163], v[48:51]
	v_mfma_f32_16x16x32_bf16 v[44:47], v[132:135], v[160:163], v[44:47]
	v_mfma_f32_16x16x32_bf16 v[32:35], v[96:99], v[172:175], v[32:35]
	v_mfma_f32_16x16x32_bf16 v[28:31], v[132:135], v[172:175], v[28:31]
	v_mfma_f32_16x16x32_bf16 v[16:19], v[96:99], v[192:195], v[16:19]
	v_mfma_f32_16x16x32_bf16 v[12:15], v[132:135], v[192:195], v[12:15]
	v_mfma_f32_16x16x32_bf16 v[64:67], v[100:103], v[148:151], v[64:67]
	v_mfma_f32_16x16x32_bf16 v[60:63], v[136:139], v[148:151], v[60:63]
	v_mfma_f32_16x16x32_bf16 v[48:51], v[100:103], v[168:171], v[48:51]
	v_mfma_f32_16x16x32_bf16 v[44:47], v[136:139], v[168:171], v[44:47]
	v_mfma_f32_16x16x32_bf16 v[32:35], v[100:103], v[176:179], v[32:35]
	v_mfma_f32_16x16x32_bf16 v[28:31], v[136:139], v[176:179], v[28:31]
	v_mfma_f32_16x16x32_bf16 v[16:19], v[100:103], v[196:199], v[16:19]
	v_mfma_f32_16x16x32_bf16 v[12:15], v[136:139], v[196:199], v[12:15]
	s_barrier
	s_mov_b32 m0, s78
	v_lshl_add_u64 v[96:97], s[42:43], 0, v[182:183]
	global_load_lds_dwordx4 v[96:97], off
	v_lshl_add_u64 v[96:97], s[42:43], 0, v[184:185]
	s_mov_b32 m0, s77
	s_nop 0
	global_load_lds_dwordx4 v[96:97], off
	s_waitcnt vmcnt(6)
	s_barrier
	v_mfma_f32_16x16x32_bf16 v[56:59], v[200:203], v[144:147], v[56:59]
	v_mfma_f32_16x16x32_bf16 v[52:55], v[226:229], v[144:147], v[52:55]
	v_mfma_f32_16x16x32_bf16 v[40:43], v[200:203], v[160:163], v[40:43]
	v_mfma_f32_16x16x32_bf16 v[36:39], v[226:229], v[160:163], v[36:39]
	v_mfma_f32_16x16x32_bf16 v[20:23], v[200:203], v[172:175], v[20:23]
	v_mfma_f32_16x16x32_bf16 v[24:27], v[226:229], v[172:175], v[24:27]
	v_mfma_f32_16x16x32_bf16 v[4:7], v[200:203], v[192:195], v[4:7]
	v_mfma_f32_16x16x32_bf16 v[8:11], v[226:229], v[192:195], v[8:11]
	v_mfma_f32_16x16x32_bf16 v[56:59], v[204:207], v[148:151], v[56:59]
	v_mfma_f32_16x16x32_bf16 v[52:55], v[230:233], v[148:151], v[52:55]
	v_mfma_f32_16x16x32_bf16 v[40:43], v[204:207], v[168:171], v[40:43]
	v_mfma_f32_16x16x32_bf16 v[36:39], v[230:233], v[168:171], v[36:39]
	v_mfma_f32_16x16x32_bf16 v[20:23], v[204:207], v[176:179], v[20:23]
	v_mfma_f32_16x16x32_bf16 v[24:27], v[230:233], v[176:179], v[24:27]
	v_mfma_f32_16x16x32_bf16 v[4:7], v[204:207], v[196:199], v[4:7]
	v_mfma_f32_16x16x32_bf16 v[8:11], v[230:233], v[196:199], v[8:11]
	v_add_u32_e32 v2, s57, v217
	s_barrier
	ds_read_b128 v[96:99], v2
	ds_read_b128 v[100:103], v2 offset:1024
	ds_read_b128 v[132:135], v2 offset:2048
	ds_read_b128 v[136:139], v2 offset:3072
	s_mov_b32 m0, s68
	ds_read_b128 v[144:147], v221 offset:32768
	ds_read_b128 v[148:151], v221 offset:33792
	ds_read_b128 v[160:163], v221 offset:34816
	ds_read_b128 v[168:171], v221 offset:35840
	ds_read_b128 v[172:175], v221 offset:36864
	ds_read_b128 v[176:179], v221 offset:37888
	ds_read_b128 v[192:195], v221 offset:38912
	ds_read_b128 v[196:199], v221 offset:39936
	global_load_lds_dwordx4 v85, s[40:41]
	s_mov_b32 m0, s69
	s_nop 0
	global_load_lds_dwordx4 v87, s[40:41]
	s_waitcnt lgkmcnt(8)
	s_barrier
	s_waitcnt lgkmcnt(0)
	s_waitcnt lgkmcnt(0)
	v_mfma_f32_16x16x32_bf16 v[164:167], v[96:99], v[144:147], v[164:167]
	v_mfma_f32_16x16x32_bf16 v[156:159], v[132:135], v[144:147], v[156:159]
	v_mfma_f32_16x16x32_bf16 v[128:131], v[96:99], v[160:163], v[128:131]
	v_mfma_f32_16x16x32_bf16 v[124:127], v[132:135], v[160:163], v[124:127]
	v_mfma_f32_16x16x32_bf16 v[112:115], v[96:99], v[172:175], v[112:115]
	v_mfma_f32_16x16x32_bf16 v[108:111], v[132:135], v[172:175], v[108:111]
	v_mfma_f32_16x16x32_bf16 v[80:83], v[96:99], v[192:195], v[80:83]
	v_mfma_f32_16x16x32_bf16 v[76:79], v[132:135], v[192:195], v[76:79]
	v_mfma_f32_16x16x32_bf16 v[164:167], v[100:103], v[148:151], v[164:167]
	v_mfma_f32_16x16x32_bf16 v[156:159], v[136:139], v[148:151], v[156:159]
	v_mfma_f32_16x16x32_bf16 v[128:131], v[100:103], v[168:171], v[128:131]
	v_mfma_f32_16x16x32_bf16 v[124:127], v[136:139], v[168:171], v[124:127]
	v_mfma_f32_16x16x32_bf16 v[112:115], v[100:103], v[176:179], v[112:115]
	v_mfma_f32_16x16x32_bf16 v[108:111], v[136:139], v[176:179], v[108:111]
	v_mfma_f32_16x16x32_bf16 v[80:83], v[100:103], v[196:199], v[80:83]
	v_mfma_f32_16x16x32_bf16 v[76:79], v[136:139], v[196:199], v[76:79]
	s_barrier
	s_mov_b32 m0, s30
	v_add_u32_e32 v2, s27, v217
	v_lshl_add_u64 v[236:237], v[236:237], 0, s[8:9]
	ds_read_b128 v[200:203], v2
	ds_read_b128 v[204:207], v2 offset:1024
	ds_read_b128 v[226:229], v2 offset:2048
	ds_read_b128 v[230:233], v2 offset:3072
	global_load_lds_dwordx4 v[236:237], off
	v_lshl_add_u64 v[236:237], v[238:239], 0, s[8:9]
	s_mov_b32 m0, s26
	s_nop 0
	global_load_lds_dwordx4 v[236:237], off
	s_barrier
	s_waitcnt lgkmcnt(0)
	s_waitcnt lgkmcnt(0)
	v_mfma_f32_16x16x32_bf16 v[152:155], v[200:203], v[144:147], v[152:155]
	v_mfma_f32_16x16x32_bf16 v[140:143], v[226:229], v[144:147], v[140:143]
	v_mfma_f32_16x16x32_bf16 v[120:123], v[200:203], v[160:163], v[120:123]
	v_mfma_f32_16x16x32_bf16 v[116:119], v[226:229], v[160:163], v[116:119]
	v_mfma_f32_16x16x32_bf16 v[104:107], v[200:203], v[172:175], v[104:107]
	v_mfma_f32_16x16x32_bf16 v[92:95], v[226:229], v[172:175], v[92:95]
	v_mfma_f32_16x16x32_bf16 v[72:75], v[200:203], v[192:195], v[72:75]
	v_mfma_f32_16x16x32_bf16 v[68:71], v[226:229], v[192:195], v[68:71]
	v_mfma_f32_16x16x32_bf16 v[152:155], v[204:207], v[148:151], v[152:155]
	v_mfma_f32_16x16x32_bf16 v[148:151], v[230:233], v[148:151], v[140:143]
	v_mfma_f32_16x16x32_bf16 v[120:123], v[204:207], v[168:171], v[120:123]
	v_mfma_f32_16x16x32_bf16 v[116:119], v[230:233], v[168:171], v[116:119]
	v_mfma_f32_16x16x32_bf16 v[104:107], v[204:207], v[176:179], v[104:107]
	v_mfma_f32_16x16x32_bf16 v[92:95], v[230:233], v[176:179], v[92:95]
	v_mfma_f32_16x16x32_bf16 v[72:75], v[204:207], v[196:199], v[72:75]
	v_mfma_f32_16x16x32_bf16 v[68:71], v[230:233], v[196:199], v[68:71]
	s_mov_b32 m0, s71
	v_lshl_add_u64 v[236:237], v[240:241], 0, s[8:9]
	s_barrier
	ds_read_b128 v[140:143], v221 offset:49152
	ds_read_b128 v[144:147], v221 offset:50176
	ds_read_b128 v[160:163], v221 offset:51200
	ds_read_b128 v[168:171], v221 offset:52224
	ds_read_b128 v[172:175], v221 offset:53248
	ds_read_b128 v[176:179], v221 offset:54272
	ds_read_b128 v[192:195], v221 offset:55296
	ds_read_b128 v[196:199], v221 offset:56320
	global_load_lds_dwordx4 v[236:237], off
	v_lshl_add_u64 v[234:235], v[234:235], 0, s[8:9]
	s_mov_b32 m0, s72
	s_nop 0
	global_load_lds_dwordx4 v[234:235], off
	s_barrier
	s_waitcnt lgkmcnt(0)
	s_waitcnt lgkmcnt(0)
	v_mfma_f32_16x16x32_bf16 v[64:67], v[96:99], v[140:143], v[64:67]
	v_mfma_f32_16x16x32_bf16 v[60:63], v[132:135], v[140:143], v[60:63]
	v_mfma_f32_16x16x32_bf16 v[48:51], v[96:99], v[160:163], v[48:51]
	v_mfma_f32_16x16x32_bf16 v[44:47], v[132:135], v[160:163], v[44:47]
	v_mfma_f32_16x16x32_bf16 v[32:35], v[96:99], v[172:175], v[32:35]
	v_mfma_f32_16x16x32_bf16 v[28:31], v[132:135], v[172:175], v[28:31]
	v_mfma_f32_16x16x32_bf16 v[16:19], v[96:99], v[192:195], v[16:19]
	v_mfma_f32_16x16x32_bf16 v[12:15], v[132:135], v[192:195], v[12:15]
	v_mfma_f32_16x16x32_bf16 v[64:67], v[100:103], v[144:147], v[64:67]
	v_mfma_f32_16x16x32_bf16 v[60:63], v[136:139], v[144:147], v[60:63]
	v_mfma_f32_16x16x32_bf16 v[48:51], v[100:103], v[168:171], v[48:51]
	v_mfma_f32_16x16x32_bf16 v[44:47], v[136:139], v[168:171], v[44:47]
	v_mfma_f32_16x16x32_bf16 v[32:35], v[100:103], v[176:179], v[32:35]
	v_mfma_f32_16x16x32_bf16 v[28:31], v[136:139], v[176:179], v[28:31]
	v_mfma_f32_16x16x32_bf16 v[16:19], v[100:103], v[196:199], v[16:19]
	v_mfma_f32_16x16x32_bf16 v[12:15], v[136:139], v[196:199], v[12:15]
	s_barrier
	s_mov_b32 m0, s25
	v_lshl_add_u64 v[96:97], s[34:35], 0, v[182:183]
	global_load_lds_dwordx4 v[96:97], off
	v_lshl_add_u64 v[96:97], s[34:35], 0, v[184:185]
	s_mov_b32 m0, s24
	s_nop 0
	global_load_lds_dwordx4 v[96:97], off
	s_waitcnt vmcnt(6)
	s_barrier
	v_mfma_f32_16x16x32_bf16 v[56:59], v[200:203], v[140:143], v[56:59]
	v_mfma_f32_16x16x32_bf16 v[52:55], v[226:229], v[140:143], v[52:55]
	v_mfma_f32_16x16x32_bf16 v[40:43], v[200:203], v[160:163], v[40:43]
	v_mfma_f32_16x16x32_bf16 v[36:39], v[226:229], v[160:163], v[36:39]
	v_mfma_f32_16x16x32_bf16 v[20:23], v[200:203], v[172:175], v[20:23]
	v_mfma_f32_16x16x32_bf16 v[24:27], v[226:229], v[172:175], v[24:27]
	v_mfma_f32_16x16x32_bf16 v[4:7], v[200:203], v[192:195], v[4:7]
	v_mfma_f32_16x16x32_bf16 v[8:11], v[226:229], v[192:195], v[8:11]
	v_mfma_f32_16x16x32_bf16 v[56:59], v[204:207], v[144:147], v[56:59]
	v_mfma_f32_16x16x32_bf16 v[52:55], v[230:233], v[144:147], v[52:55]
	v_mfma_f32_16x16x32_bf16 v[40:43], v[204:207], v[168:171], v[40:43]
	v_mfma_f32_16x16x32_bf16 v[36:39], v[230:233], v[168:171], v[36:39]
	v_mfma_f32_16x16x32_bf16 v[20:23], v[204:207], v[176:179], v[20:23]
	v_mfma_f32_16x16x32_bf16 v[24:27], v[230:233], v[176:179], v[24:27]
	v_mfma_f32_16x16x32_bf16 v[4:7], v[204:207], v[196:199], v[4:7]
	v_mfma_f32_16x16x32_bf16 v[8:11], v[230:233], v[196:199], v[8:11]
	s_andn2_b64 vcc, exec, s[12:13]
	s_mov_b64 s[14:15], -1
	s_mov_b64 s[12:13], 0
	s_mov_b64 s[34:35], 0x100
	s_barrier
	s_cbranch_vccz .LBB0_781
	s_lshl_b32 s15, s7, 8
	v_add_u32_e32 v202, s15, v186
	v_mov_b64_e32 v[206:207], s[52:53]
	v_mad_i64_i32 v[88:89], s[2:3], v202, s6, v[206:207]
	global_load_dwordx4 v[84:87], v[88:89], off offset:48
	s_nop 0
	global_load_dwordx4 v[88:91], v[88:89], off offset:64
	v_or_b32_e32 v2, 16, v202
	v_mad_i64_i32 v[100:101], s[2:3], v2, s6, v[206:207]
	global_load_dwordx4 v[96:99], v[100:101], off offset:48
	s_nop 0
	global_load_dwordx4 v[100:103], v[100:101], off offset:64
	v_or_b32_e32 v2, 32, v202
	v_mad_i64_i32 v[132:133], s[2:3], v2, s6, v[206:207]
	v_or_b32_e32 v2, 48, v202
	global_load_dwordx4 v[172:175], v[132:133], off offset:64
	global_load_dwordx4 v[176:179], v[132:133], off offset:48
	v_mad_i64_i32 v[132:133], s[2:3], v2, s6, v[206:207]
	global_load_dwordx4 v[160:163], v[132:133], off offset:64
	global_load_dwordx4 v[168:171], v[132:133], off offset:48
	s_mov_b32 s2, 0x3b800000
	v_add_u32_e32 v198, 0x80, v202
	v_add_u32_e32 v196, 0x90, v202
	v_add_u32_e32 v194, 0xa0, v202
	v_add_u32_e32 v192, 0xb0, v202
	s_mul_hi_i32 s0, s7, 0x3e0f83e1
	s_lshr_b32 s1, s0, 31
	s_ashr_i32 s0, s0, 3
	s_add_i32 s0, s0, s1
	s_mul_i32 s1, s0, 33
	s_sub_i32 s1, s7, s1
	s_lshl_b32 s12, s1, 8
	s_lshl_b32 s14, s46, 1
	s_lshl_b32 s7, s0, 3
	s_mov_b32 s13, 0x8000
	s_waitcnt vmcnt(0)
	v_mov_b32_e32 v132, v84
	v_mov_b32_e32 v133, v88
	v_mov_b32_e32 v88, v85
	v_pk_add_f32 v[84:85], v[132:133], v[88:89]
	v_mov_b32_e32 v88, v86
	v_mov_b32_e32 v89, v90
	v_mov_b32_e32 v90, v87
	v_pk_add_f32 v[86:87], v[88:89], v[90:91]
	v_mov_b32_e32 v88, v98
	v_pk_add_f32 v[84:85], v[84:85], v[86:87]
	v_mov_b32_e32 v86, v96
	v_mov_b32_e32 v87, v100
	v_mov_b32_e32 v100, v97
	v_mov_b32_e32 v89, v102
	v_mov_b32_e32 v102, v99
	v_pk_add_f32 v[86:87], v[86:87], v[100:101]
	v_pk_add_f32 v[88:89], v[88:89], v[102:103]
	s_nop 0
	v_pk_add_f32 v[86:87], v[86:87], v[88:89]
	v_mov_b32_e32 v89, v84
	v_mov_b32_e32 v88, v86
	v_mov_b32_e32 v84, v87
	v_pk_add_f32 v[84:85], v[88:89], v[84:85]
	s_nop 0
	v_pk_fma_f32 v[200:201], v[84:85], s[2:3], v[180:181] op_sel_hi:[1,0,0]
	v_mad_i64_i32 v[88:89], s[2:3], v192, s6, v[206:207]
	v_mul_f32_e32 v2, 0x4b800000, v201
	v_cmp_gt_f32_e32 vcc, s33, v201
	v_cmp_gt_f32_e64 s[42:43], s33, v200
	s_nop 0
	v_cndmask_b32_e32 v2, v201, v2, vcc
	v_rsq_f32_e32 v2, v2
	s_nop 0
	v_mul_f32_e32 v84, 0x45800000, v2
	v_cndmask_b32_e32 v204, v2, v84, vcc
	v_mad_i64_i32 v[84:85], s[2:3], v198, s6, v[206:207]
	global_load_dwordx4 v[140:143], v[84:85], off offset:64
	global_load_dwordx4 v[144:147], v[84:85], off offset:48
	v_mad_i64_i32 v[84:85], s[2:3], v196, s6, v[206:207]
	global_load_dwordx4 v[132:135], v[84:85], off offset:64
	global_load_dwordx4 v[136:139], v[84:85], off offset:48
	v_mad_i64_i32 v[84:85], s[2:3], v194, s6, v[206:207]
	global_load_dwordx4 v[96:99], v[84:85], off offset:64
	global_load_dwordx4 v[100:103], v[84:85], off offset:48
	s_nop 0
	global_load_dwordx4 v[84:87], v[88:89], off offset:64
	s_nop 0
	global_load_dwordx4 v[88:91], v[88:89], off offset:48
	v_add_u32_e32 v206, s12, v186
	v_ashrrev_i32_e32 v207, 31, v206
	v_pk_mul_f32 v[164:165], v[164:165], v[204:205] op_sel_hi:[1,0]
	v_pk_mul_f32 v[156:157], v[156:157], v[204:205] op_sel_hi:[1,0]
	v_pk_mul_f32 v[166:167], v[166:167], v[204:205] op_sel_hi:[1,0]
	v_pk_mul_f32 v[158:159], v[158:159], v[204:205] op_sel_hi:[1,0]
	s_mov_b64 s[2:3], -1
	s_and_b64 vcc, exec, s[54:55]
	s_cbranch_vccz .LBB0_784
	s_add_i32 s0, s7, s14
	s_ashr_i32 s1, s0, 31
	s_lshl_b64 s[0:1], s[0:1], 6
	v_lshl_add_u64 v[226:227], s[0:1], 0, v[190:191]
	v_mov_b64_e32 v[228:229], s[50:51]
	v_mad_u64_u32 v[228:229], s[0:1], v226, s28, v[228:229]
	v_mad_i32_i24 v229, v227, s28, v229
	v_bfe_u32 v2, v164, 16, 1
	v_lshl_add_u64 v[226:227], v[206:207], 1, v[228:229]
	v_add3_u32 v2, v164, v2, s29
	s_movk_i32 s0, 0x4000
	global_store_short_d16_hi v[226:227], v2, off
	v_bfe_u32 v2, v165, 16, 1
	v_add_co_u32_e32 v228, vcc, s0, v226
	v_add3_u32 v2, v165, v2, s29
	s_nop 0
	v_addc_co_u32_e32 v229, vcc, 0, v227, vcc
	global_store_short_d16_hi v[228:229], v2, off offset:512
	v_bfe_u32 v2, v166, 16, 1
	v_add_co_u32_e32 v228, vcc, s13, v226
	v_add3_u32 v2, v166, v2, s29
	s_nop 0
	v_addc_co_u32_e32 v229, vcc, 0, v227, vcc
	s_mov_b32 s0, 0xc000
	global_store_short_d16_hi v[228:229], v2, off offset:1024
	v_bfe_u32 v2, v167, 16, 1
	v_add_co_u32_e32 v228, vcc, s0, v226
	v_add3_u32 v2, v167, v2, s29
	s_nop 0
	v_addc_co_u32_e32 v229, vcc, 0, v227, vcc
	s_mov_b32 s0, 0x10000
	global_store_short_d16_hi v[228:229], v2, off offset:1536
	v_bfe_u32 v2, v156, 16, 1
	v_add_co_u32_e32 v228, vcc, s0, v226
	v_add3_u32 v2, v156, v2, s29
	s_nop 0
	v_addc_co_u32_e32 v229, vcc, 0, v227, vcc
	s_mov_b32 s0, 0x14000
	global_store_short_d16_hi v[228:229], v2, off offset:2048
	v_bfe_u32 v2, v157, 16, 1
	v_add_co_u32_e32 v228, vcc, s0, v226
	v_add3_u32 v2, v157, v2, s29
	s_nop 0
	v_addc_co_u32_e32 v229, vcc, 0, v227, vcc
	global_store_short_d16_hi v[228:229], v2, off offset:2560
	v_bfe_u32 v2, v158, 16, 1
	v_add_co_u32_e32 v228, vcc, 0x18000, v226
	v_add3_u32 v2, v158, v2, s29
	s_nop 0
	v_addc_co_u32_e32 v229, vcc, 0, v227, vcc
	global_store_short_d16_hi v[228:229], v2, off offset:3072
	v_bfe_u32 v2, v159, 16, 1
	v_add_co_u32_e32 v226, vcc, 0x1c000, v226
	v_add3_u32 v2, v159, v2, s29
	s_nop 0
	v_addc_co_u32_e32 v227, vcc, 0, v227, vcc
	global_store_short_d16_hi v[226:227], v2, off offset:3584
	s_mov_b64 s[2:3], 0

.LBB0_1324:
	s_add_u32 s14, s46, s12
	s_addc_u32 s15, s47, s13
	s_add_u32 s26, s14, 0x1701b100
	s_addc_u32 s27, s15, 0
	s_add_u32 s36, s3, s12
	s_addc_u32 s40, s24, s13
	s_add_i32 s41, 0, 0x10000
	v_add_u32_e32 v37, s41, v175
	ds_read_b128 v[48:51], v37
	ds_read_b128 v[184:187], v37 offset:1024
	ds_read_b128 v[188:191], v37 offset:2048
	ds_read_b128 v[192:195], v37 offset:3072
	s_cmpk_eq_i32 s12, 0x700
	s_cselect_b64 vcc, -1, 0
	s_and_b64 s[14:15], vcc, exec
	v_cndmask_b32_e32 v2, v36, v177, vcc
	s_cselect_b32 s35, s49, s27
	s_cselect_b32 s34, s48, s26
	v_cndmask_b32_e32 v170, v38, v178, vcc
	v_cndmask_b32_e32 v37, v40, v179, vcc
	v_cndmask_b32_e32 v39, v42, v182, vcc
	s_cselect_b32 s15, s0, s40
	s_cselect_b32 s14, s1, s36
	v_lshl_add_u64 v[234:235], v[46:47], 0, s[12:13]
	s_add_i32 m0, s62, 0xc000
	ds_read_b128 v[196:199], v176
	ds_read_b128 v[200:203], v176 offset:1024
	ds_read_b128 v[204:207], v176 offset:2048
	ds_read_b128 v[214:217], v176 offset:3072
	ds_read_b128 v[218:221], v176 offset:4096
	ds_read_b128 v[222:225], v176 offset:5120
	ds_read_b128 v[226:229], v176 offset:6144
	ds_read_b128 v[230:233], v176 offset:7168
	global_load_lds_dwordx4 v[234:235], off
	v_lshl_add_u64 v[234:235], v[44:45], 0, s[12:13]
	s_add_i32 m0, s62, 0xe000
	s_nop 0
	global_load_lds_dwordx4 v[234:235], off
	s_waitcnt lgkmcnt(8)
	s_barrier
	s_waitcnt lgkmcnt(0)
	s_waitcnt lgkmcnt(0)
	v_mfma_f32_16x16x32_bf16 v[144:147], v[48:51], v[196:199], v[144:147]
	v_mfma_f32_16x16x32_bf16 v[140:143], v[188:191], v[196:199], v[140:143]
	v_mfma_f32_16x16x32_bf16 v[136:139], v[48:51], v[204:207], v[136:139]
	v_mfma_f32_16x16x32_bf16 v[132:135], v[188:191], v[204:207], v[132:135]
	v_mfma_f32_16x16x32_bf16 v[112:115], v[48:51], v[218:221], v[112:115]
	v_mfma_f32_16x16x32_bf16 v[108:111], v[188:191], v[218:221], v[108:111]
	v_mfma_f32_16x16x32_bf16 v[104:107], v[48:51], v[226:229], v[104:107]
	v_mfma_f32_16x16x32_bf16 v[100:103], v[188:191], v[226:229], v[100:103]
	v_mfma_f32_16x16x32_bf16 v[144:147], v[184:187], v[200:203], v[144:147]
	v_mfma_f32_16x16x32_bf16 v[140:143], v[192:195], v[200:203], v[140:143]
	v_mfma_f32_16x16x32_bf16 v[136:139], v[184:187], v[214:217], v[136:139]
	v_mfma_f32_16x16x32_bf16 v[132:135], v[192:195], v[214:217], v[132:135]
	v_mfma_f32_16x16x32_bf16 v[112:115], v[184:187], v[222:225], v[112:115]
	v_mfma_f32_16x16x32_bf16 v[108:111], v[192:195], v[222:225], v[108:111]
	v_mfma_f32_16x16x32_bf16 v[104:107], v[184:187], v[230:233], v[104:107]
	v_mfma_f32_16x16x32_bf16 v[100:103], v[192:195], v[230:233], v[100:103]
	s_barrier
	s_add_i32 s36, 0, 0x14000
	s_add_i32 s26, s41, s61
	v_add_u32_e32 v41, s36, v175
	v_lshl_add_u64 v[250:251], s[14:15], 0, v[148:149]
	s_mov_b32 m0, s26
	ds_read_b128 v[234:237], v41
	ds_read_b128 v[238:241], v41 offset:1024
	ds_read_b128 v[242:245], v41 offset:2048
	ds_read_b128 v[246:249], v41 offset:3072
	global_load_lds_dwordx4 v[250:251], off
	v_lshl_add_u64 v[252:253], s[14:15], 0, v[150:151]
	s_add_i32 m0, s26, 0x2000
	s_nop 0
	global_load_lds_dwordx4 v[252:253], off
	s_barrier
	s_waitcnt lgkmcnt(0)
	s_waitcnt lgkmcnt(0)
	v_mfma_f32_16x16x32_bf16 v[128:131], v[234:237], v[196:199], v[128:131]
	v_mfma_f32_16x16x32_bf16 v[124:127], v[242:245], v[196:199], v[124:127]
	v_mfma_f32_16x16x32_bf16 v[120:123], v[234:237], v[204:207], v[120:123]
	v_mfma_f32_16x16x32_bf16 v[116:119], v[242:245], v[204:207], v[116:119]
	v_mfma_f32_16x16x32_bf16 v[96:99], v[234:237], v[218:221], v[96:99]
	v_mfma_f32_16x16x32_bf16 v[92:95], v[242:245], v[218:221], v[92:95]
	v_mfma_f32_16x16x32_bf16 v[88:91], v[234:237], v[226:229], v[88:91]
	v_mfma_f32_16x16x32_bf16 v[84:87], v[242:245], v[226:229], v[84:87]
	v_mfma_f32_16x16x32_bf16 v[128:131], v[238:241], v[200:203], v[128:131]
	v_mfma_f32_16x16x32_bf16 v[124:127], v[246:249], v[200:203], v[124:127]
	v_mfma_f32_16x16x32_bf16 v[120:123], v[238:241], v[214:217], v[120:123]
	v_mfma_f32_16x16x32_bf16 v[116:119], v[246:249], v[214:217], v[116:119]
	v_mfma_f32_16x16x32_bf16 v[96:99], v[238:241], v[222:225], v[96:99]
	v_mfma_f32_16x16x32_bf16 v[92:95], v[246:249], v[222:225], v[92:95]
	v_mfma_f32_16x16x32_bf16 v[88:91], v[238:241], v[230:233], v[88:91]
	v_mfma_f32_16x16x32_bf16 v[84:87], v[246:249], v[230:233], v[84:87]
	s_mov_b32 m0, s62
	s_barrier
	ds_read_b128 v[196:199], v176 offset:16384
	ds_read_b128 v[200:203], v176 offset:17408
	ds_read_b128 v[204:207], v176 offset:18432
	ds_read_b128 v[214:217], v176 offset:19456
	ds_read_b128 v[218:221], v176 offset:20480
	ds_read_b128 v[222:225], v176 offset:21504
	ds_read_b128 v[226:229], v176 offset:22528
	ds_read_b128 v[230:233], v176 offset:23552
	global_load_lds_dwordx4 v2, s[34:35]
	s_mov_b32 m0, s63
	v_mov_b32_e32 v171, v3
	global_load_lds_dwordx4 v170, s[34:35]
	s_barrier
	s_waitcnt lgkmcnt(0)
	v_lshl_add_u64 v[208:209], s[34:35], 0, v[2:3]
	v_lshl_add_u64 v[170:171], s[34:35], 0, v[170:171]
	s_waitcnt lgkmcnt(0)
	v_mfma_f32_16x16x32_bf16 v[80:83], v[48:51], v[196:199], v[80:83]
	v_mfma_f32_16x16x32_bf16 v[76:79], v[188:191], v[196:199], v[76:79]
	v_mfma_f32_16x16x32_bf16 v[72:75], v[48:51], v[204:207], v[72:75]
	v_mfma_f32_16x16x32_bf16 v[68:71], v[188:191], v[204:207], v[68:71]
	v_mfma_f32_16x16x32_bf16 v[16:19], v[48:51], v[218:221], v[16:19]
	v_mfma_f32_16x16x32_bf16 v[12:15], v[188:191], v[218:221], v[12:15]
	v_mfma_f32_16x16x32_bf16 v[8:11], v[48:51], v[226:229], v[8:11]
	v_mfma_f32_16x16x32_bf16 v[4:7], v[188:191], v[226:229], v[4:7]
	v_mfma_f32_16x16x32_bf16 v[80:83], v[184:187], v[200:203], v[80:83]
	v_mfma_f32_16x16x32_bf16 v[76:79], v[192:195], v[200:203], v[76:79]
	v_mfma_f32_16x16x32_bf16 v[72:75], v[184:187], v[214:217], v[72:75]
	v_mfma_f32_16x16x32_bf16 v[68:71], v[192:195], v[214:217], v[68:71]
	v_mfma_f32_16x16x32_bf16 v[16:19], v[184:187], v[222:225], v[16:19]
	v_mfma_f32_16x16x32_bf16 v[12:15], v[192:195], v[222:225], v[12:15]
	v_mfma_f32_16x16x32_bf16 v[8:11], v[184:187], v[230:233], v[8:11]
	v_mfma_f32_16x16x32_bf16 v[4:7], v[192:195], v[230:233], v[4:7]
	s_barrier
	s_add_u32 s26, s14, 0x40000
	s_addc_u32 s27, s15, 0
	s_add_i32 s36, s36, s61
	v_lshl_add_u64 v[48:49], s[26:27], 0, v[148:149]
	s_mov_b32 m0, s36
	s_nop 0
	global_load_lds_dwordx4 v[48:49], off
	v_lshl_add_u64 v[48:49], s[26:27], 0, v[150:151]
	s_add_i32 m0, s36, 0x2000
	s_nop 0
	global_load_lds_dwordx4 v[48:49], off
	s_waitcnt vmcnt(6)
	s_barrier
	v_mfma_f32_16x16x32_bf16 v[60:63], v[242:245], v[196:199], v[60:63]
	v_mfma_f32_16x16x32_bf16 v[56:59], v[234:237], v[204:207], v[56:59]
	v_mfma_f32_16x16x32_bf16 v[52:55], v[242:245], v[204:207], v[52:55]
	v_mfma_f32_16x16x32_bf16 v[32:35], v[234:237], v[218:221], v[32:35]
	v_mfma_f32_16x16x32_bf16 v[28:31], v[242:245], v[218:221], v[28:31]
	v_mfma_f32_16x16x32_bf16 v[24:27], v[234:237], v[226:229], v[24:27]
	v_mfma_f32_16x16x32_bf16 v[20:23], v[242:245], v[226:229], v[20:23]
	v_mfma_f32_16x16x32_bf16 v[48:51], v[234:237], v[196:199], v[64:67]
	v_mfma_f32_16x16x32_bf16 v[60:63], v[246:249], v[200:203], v[60:63]
	v_mfma_f32_16x16x32_bf16 v[56:59], v[238:241], v[214:217], v[56:59]
	v_mfma_f32_16x16x32_bf16 v[52:55], v[246:249], v[214:217], v[52:55]
	v_mfma_f32_16x16x32_bf16 v[32:35], v[238:241], v[222:225], v[32:35]
	v_mfma_f32_16x16x32_bf16 v[28:31], v[246:249], v[222:225], v[28:31]
	v_mfma_f32_16x16x32_bf16 v[24:27], v[238:241], v[230:233], v[24:27]
	v_mfma_f32_16x16x32_bf16 v[20:23], v[246:249], v[230:233], v[20:23]
	v_mfma_f32_16x16x32_bf16 v[48:51], v[238:241], v[200:203], v[48:51]
	s_add_i32 s26, 0, 0x18000
	v_add_u32_e32 v2, s26, v175
	s_barrier
	ds_read_b128 v[64:67], v2
	ds_read_b128 v[184:187], v2 offset:1024
	ds_read_b128 v[188:191], v2 offset:2048
	ds_read_b128 v[192:195], v2 offset:3072
	s_mov_b32 m0, s64
	ds_read_b128 v[196:199], v176 offset:32768
	ds_read_b128 v[200:203], v176 offset:33792
	ds_read_b128 v[204:207], v176 offset:34816
	ds_read_b128 v[214:217], v176 offset:35840
	ds_read_b128 v[218:221], v176 offset:36864
	ds_read_b128 v[222:225], v176 offset:37888
	ds_read_b128 v[226:229], v176 offset:38912
	ds_read_b128 v[230:233], v176 offset:39936
	global_load_lds_dwordx4 v37, s[34:35]
	s_mov_b32 m0, s65
	s_nop 0
	global_load_lds_dwordx4 v39, s[34:35]
	s_waitcnt lgkmcnt(8)
	s_barrier
	s_waitcnt lgkmcnt(0)
	s_waitcnt lgkmcnt(0)
	v_mfma_f32_16x16x32_bf16 v[144:147], v[64:67], v[196:199], v[144:147]
	v_mfma_f32_16x16x32_bf16 v[140:143], v[188:191], v[196:199], v[140:143]
	v_mfma_f32_16x16x32_bf16 v[136:139], v[64:67], v[204:207], v[136:139]
	v_mfma_f32_16x16x32_bf16 v[132:135], v[188:191], v[204:207], v[132:135]
	v_mfma_f32_16x16x32_bf16 v[112:115], v[64:67], v[218:221], v[112:115]
	v_mfma_f32_16x16x32_bf16 v[108:111], v[188:191], v[218:221], v[108:111]
	v_mfma_f32_16x16x32_bf16 v[104:107], v[64:67], v[226:229], v[104:107]
	v_mfma_f32_16x16x32_bf16 v[100:103], v[188:191], v[226:229], v[100:103]
	v_mfma_f32_16x16x32_bf16 v[144:147], v[184:187], v[200:203], v[144:147]
	v_mfma_f32_16x16x32_bf16 v[140:143], v[192:195], v[200:203], v[140:143]
	v_mfma_f32_16x16x32_bf16 v[136:139], v[184:187], v[214:217], v[136:139]
	v_mfma_f32_16x16x32_bf16 v[132:135], v[192:195], v[214:217], v[132:135]
	v_mfma_f32_16x16x32_bf16 v[112:115], v[184:187], v[222:225], v[112:115]
	v_mfma_f32_16x16x32_bf16 v[108:111], v[192:195], v[222:225], v[108:111]
	v_mfma_f32_16x16x32_bf16 v[104:107], v[184:187], v[230:233], v[104:107]
	v_mfma_f32_16x16x32_bf16 v[100:103], v[192:195], v[230:233], v[100:103]
	s_barrier
	s_add_i32 s27, 0, 0x1c000
	s_add_i32 s26, s26, s61
	v_add_u32_e32 v2, s27, v175
	v_lshl_add_u64 v[250:251], v[250:251], 0, s[8:9]
	s_mov_b32 m0, s26
	ds_read_b128 v[234:237], v2
	ds_read_b128 v[238:241], v2 offset:1024
	ds_read_b128 v[242:245], v2 offset:2048
	ds_read_b128 v[246:249], v2 offset:3072
	global_load_lds_dwordx4 v[250:251], off
	v_lshl_add_u64 v[250:251], v[252:253], 0, s[8:9]
	s_add_i32 m0, s26, 0x2000
	s_nop 0
	global_load_lds_dwordx4 v[250:251], off
	s_barrier
	s_waitcnt lgkmcnt(0)
	s_waitcnt lgkmcnt(0)
	v_mfma_f32_16x16x32_bf16 v[128:131], v[234:237], v[196:199], v[128:131]
	v_mfma_f32_16x16x32_bf16 v[124:127], v[242:245], v[196:199], v[124:127]
	v_mfma_f32_16x16x32_bf16 v[120:123], v[234:237], v[204:207], v[120:123]
	v_mfma_f32_16x16x32_bf16 v[116:119], v[242:245], v[204:207], v[116:119]
	v_mfma_f32_16x16x32_bf16 v[96:99], v[234:237], v[218:221], v[96:99]
	v_mfma_f32_16x16x32_bf16 v[92:95], v[242:245], v[218:221], v[92:95]
	v_mfma_f32_16x16x32_bf16 v[88:91], v[234:237], v[226:229], v[88:91]
	v_mfma_f32_16x16x32_bf16 v[84:87], v[242:245], v[226:229], v[84:87]
	v_mfma_f32_16x16x32_bf16 v[128:131], v[238:241], v[200:203], v[128:131]
	v_mfma_f32_16x16x32_bf16 v[124:127], v[246:249], v[200:203], v[124:127]
	v_mfma_f32_16x16x32_bf16 v[120:123], v[238:241], v[214:217], v[120:123]
	v_mfma_f32_16x16x32_bf16 v[116:119], v[246:249], v[214:217], v[116:119]
	v_mfma_f32_16x16x32_bf16 v[96:99], v[238:241], v[222:225], v[96:99]
	v_mfma_f32_16x16x32_bf16 v[92:95], v[246:249], v[222:225], v[92:95]
	v_mfma_f32_16x16x32_bf16 v[88:91], v[238:241], v[230:233], v[88:91]
	v_mfma_f32_16x16x32_bf16 v[84:87], v[246:249], v[230:233], v[84:87]
	s_mov_b32 m0, s72
	v_lshl_add_u64 v[208:209], v[208:209], 0, s[8:9]
	s_barrier
	ds_read_b128 v[196:199], v176 offset:49152
	ds_read_b128 v[200:203], v176 offset:50176
	ds_read_b128 v[204:207], v176 offset:51200
	ds_read_b128 v[214:217], v176 offset:52224
	ds_read_b128 v[218:221], v176 offset:53248
	ds_read_b128 v[222:225], v176 offset:54272
	ds_read_b128 v[226:229], v176 offset:55296
	ds_read_b128 v[230:233], v176 offset:56320
	global_load_lds_dwordx4 v[208:209], off
	v_lshl_add_u64 v[170:171], v[170:171], 0, s[8:9]
	s_mov_b32 m0, s73
	s_nop 0
	global_load_lds_dwordx4 v[170:171], off
	s_barrier
	s_waitcnt lgkmcnt(0)
	s_waitcnt lgkmcnt(0)
	v_mfma_f32_16x16x32_bf16 v[80:83], v[64:67], v[196:199], v[80:83]
	v_mfma_f32_16x16x32_bf16 v[76:79], v[188:191], v[196:199], v[76:79]
	v_mfma_f32_16x16x32_bf16 v[72:75], v[64:67], v[204:207], v[72:75]
	v_mfma_f32_16x16x32_bf16 v[68:71], v[188:191], v[204:207], v[68:71]
	v_mfma_f32_16x16x32_bf16 v[16:19], v[64:67], v[218:221], v[16:19]
	v_mfma_f32_16x16x32_bf16 v[12:15], v[188:191], v[218:221], v[12:15]
	v_mfma_f32_16x16x32_bf16 v[8:11], v[64:67], v[226:229], v[8:11]
	v_mfma_f32_16x16x32_bf16 v[4:7], v[188:191], v[226:229], v[4:7]
	v_mfma_f32_16x16x32_bf16 v[80:83], v[184:187], v[200:203], v[80:83]
	v_mfma_f32_16x16x32_bf16 v[76:79], v[192:195], v[200:203], v[76:79]
	v_mfma_f32_16x16x32_bf16 v[72:75], v[184:187], v[214:217], v[72:75]
	v_mfma_f32_16x16x32_bf16 v[68:71], v[192:195], v[214:217], v[68:71]
	v_mfma_f32_16x16x32_bf16 v[16:19], v[184:187], v[222:225], v[16:19]
	v_mfma_f32_16x16x32_bf16 v[12:15], v[192:195], v[222:225], v[12:15]
	v_mfma_f32_16x16x32_bf16 v[8:11], v[184:187], v[230:233], v[8:11]
	v_mfma_f32_16x16x32_bf16 v[4:7], v[192:195], v[230:233], v[4:7]
	s_barrier
	s_add_u32 s14, s14, 0x40080
	s_addc_u32 s15, s15, 0
	s_add_i32 s26, s27, s61
	v_lshl_add_u64 v[64:65], s[14:15], 0, v[148:149]
	s_mov_b32 m0, s26
	s_nop 0
	global_load_lds_dwordx4 v[64:65], off
	v_lshl_add_u64 v[64:65], s[14:15], 0, v[150:151]
	s_add_i32 m0, s26, 0x2000
	s_nop 0
	global_load_lds_dwordx4 v[64:65], off
	s_waitcnt vmcnt(6)
	s_barrier
	v_mfma_f32_16x16x32_bf16 v[48:51], v[234:237], v[196:199], v[48:51]
	v_mfma_f32_16x16x32_bf16 v[64:67], v[238:241], v[200:203], v[48:51]
	v_mfma_f32_16x16x32_bf16 v[48:51], v[242:245], v[196:199], v[60:63]
	v_mfma_f32_16x16x32_bf16 v[60:63], v[246:249], v[200:203], v[48:51]
	v_mfma_f32_16x16x32_bf16 v[48:51], v[234:237], v[204:207], v[56:59]
	v_mfma_f32_16x16x32_bf16 v[56:59], v[238:241], v[214:217], v[48:51]
	v_mfma_f32_16x16x32_bf16 v[48:51], v[242:245], v[204:207], v[52:55]
	v_mfma_f32_16x16x32_bf16 v[32:35], v[234:237], v[218:221], v[32:35]
	v_mfma_f32_16x16x32_bf16 v[28:31], v[242:245], v[218:221], v[28:31]
	v_mfma_f32_16x16x32_bf16 v[24:27], v[234:237], v[226:229], v[24:27]
	v_mfma_f32_16x16x32_bf16 v[20:23], v[242:245], v[226:229], v[20:23]
	v_mfma_f32_16x16x32_bf16 v[52:55], v[246:249], v[214:217], v[48:51]
	v_mfma_f32_16x16x32_bf16 v[32:35], v[238:241], v[222:225], v[32:35]
	v_mfma_f32_16x16x32_bf16 v[28:31], v[246:249], v[222:225], v[28:31]
	v_mfma_f32_16x16x32_bf16 v[24:27], v[238:241], v[230:233], v[24:27]
	v_mfma_f32_16x16x32_bf16 v[20:23], v[246:249], v[230:233], v[20:23]
	s_add_i32 s25, s25, 2
	s_add_u32 s12, s12, 0x100
	s_addc_u32 s13, s13, 0
	s_cmp_gt_u32 s25, 13
	s_barrier
	s_cbranch_scc0 .LBB0_1324
	s_mul_hi_i32 s0, s2, 0x3e0f83e1
	s_lshr_b32 s1, s0, 31
	s_ashr_i32 s0, s0, 3
	s_add_i32 s0, s0, s1
	s_mul_i32 s1, s0, 33
	s_sub_i32 s1, s2, s1
	s_cmp_lg_u32 s1, 0
	s_cselect_b32 s0, s0, 8
	s_mul_hi_i32 s1, s0, 0x6000
	s_mulk_i32 s0, 0x6000
	s_add_u32 s14, s69, s0
	s_addc_u32 s15, s70, s1
	s_ashr_i32 s3, s2, 31
	s_lshl_b64 s[0:1], s[2:3], 19
	s_lshl_b32 s2, s7, 8
	s_ashr_i32 s3, s2, 31
	s_lshl_b64 s[12:13], s[2:3], 2
	s_add_u32 s7, s14, s12
	s_addc_u32 s13, s15, s13
	s_lshl_b32 s12, s71, 2
	s_add_u32 s12, s7, s12
	s_addc_u32 s13, s13, 0
	v_lshlrev_b32_e32 v2, 2, v152
	v_lshl_add_u64 v[36:37], s[12:13], 0, v[2:3]
	s_mov_b64 s[12:13], 0x6000
	s_movk_i32 s7, 0x6000
	v_lshl_add_u64 v[38:39], v[36:37], 0, s[12:13]
	v_add_co_u32_e32 v36, vcc, s7, v36
	s_add_u32 s7, s66, s0
	s_addc_u32 s12, s67, s1
	s_lshl_b64 s[0:1], s[2:3], 1
	s_add_u32 s0, s7, s0
	s_addc_u32 s1, s12, s1
	s_lshl_b32 s2, s71, 1
	s_add_u32 s0, s0, s2
	s_addc_u32 s1, s1, 0
	v_lshlrev_b32_e32 v2, 1, v152
	v_lshl_add_u64 v[170:171], s[0:1], 0, v[2:3]
	v_addc_co_u32_e32 v37, vcc, 0, v37, vcc
	v_lshl_add_u64 v[184:185], v[170:171], 0, v[154:155]
	global_load_dwordx4 v[48:51], v[36:37], off
	global_load_dwordx4 v[44:47], v[38:39], off offset:64
	global_load_dwordx4 v[40:43], v[38:39], off offset:512
	s_nop 0
	global_load_dwordx4 v[36:39], v[38:39], off offset:576
	v_lshl_add_u64 v[202:203], v[170:171], 0, v[156:157]
	global_load_dwordx2 v[186:187], v[184:185], off
	global_load_dwordx2 v[190:191], v[184:185], off offset:32
	global_load_dwordx2 v[194:195], v[184:185], off offset:256
	global_load_dwordx2 v[198:199], v[184:185], off offset:288
	global_load_dwordx2 v[204:205], v[202:203], off
	global_load_dwordx2 v[214:215], v[202:203], off offset:32
	global_load_dwordx2 v[218:219], v[202:203], off offset:256
	global_load_dwordx2 v[222:223], v[202:203], off offset:288
	s_and_b64 vcc, exec, s[38:39]
	s_mov_b32 s7, s52
	s_mov_b32 s2, s76
	s_mov_b64 s[12:13], s[54:55]
	s_movk_i32 s36, 0x1ff
	s_waitcnt vmcnt(0)
	v_lshlrev_b32_e32 v188, 16, v186
	v_and_b32_e32 v189, 0xffff0000, v186
	v_lshlrev_b32_e32 v196, 16, v194
	v_lshlrev_b32_e32 v200, 16, v198
	v_and_b32_e32 v201, 0xffff0000, v198
	v_lshlrev_b32_e32 v198, 16, v199
	v_and_b32_e32 v199, 0xffff0000, v199
	v_pk_fma_f32 v[126:127], v[126:127], v[38:39], v[198:199]
	v_pk_fma_f32 v[124:125], v[124:125], v[36:37], v[200:201]
	v_lshlrev_b32_e32 v206, 16, v204
	v_and_b32_e32 v207, 0xffff0000, v204
	v_lshlrev_b32_e32 v204, 16, v205
	v_and_b32_e32 v205, 0xffff0000, v205
	v_cvt_pk_bf16_f32 v124, v124, v125
	v_cvt_pk_bf16_f32 v125, v126, v127
	v_lshlrev_b32_e32 v224, 16, v222
	v_and_b32_e32 v225, 0xffff0000, v222
	v_lshlrev_b32_e32 v222, 16, v223
	v_and_b32_e32 v223, 0xffff0000, v223
	global_store_dwordx2 v[184:185], v[124:125], off offset:288
	v_pk_fma_f32 v[124:125], v[138:139], v[50:51], v[204:205]
	v_pk_fma_f32 v[126:127], v[136:137], v[48:49], v[206:207]
	v_lshlrev_b32_e32 v216, 16, v214
	v_and_b32_e32 v217, 0xffff0000, v214
	v_lshlrev_b32_e32 v214, 16, v215
	v_and_b32_e32 v215, 0xffff0000, v215
	v_cvt_pk_bf16_f32 v126, v126, v127
	v_cvt_pk_bf16_f32 v127, v124, v125
	v_pk_fma_f32 v[118:119], v[118:119], v[38:39], v[222:223]
	v_pk_fma_f32 v[116:117], v[116:117], v[36:37], v[224:225]
	v_and_b32_e32 v197, 0xffff0000, v194
	v_lshlrev_b32_e32 v194, 16, v195
	v_and_b32_e32 v195, 0xffff0000, v195
	v_lshlrev_b32_e32 v220, 16, v218
	v_and_b32_e32 v221, 0xffff0000, v218
	v_lshlrev_b32_e32 v218, 16, v219
	v_and_b32_e32 v219, 0xffff0000, v219
	global_store_dwordx2 v[202:203], v[126:127], off
	v_pk_fma_f32 v[124:125], v[134:135], v[46:47], v[214:215]
	v_pk_fma_f32 v[126:127], v[132:133], v[44:45], v[216:217]
	v_cvt_pk_bf16_f32 v116, v116, v117
	v_cvt_pk_bf16_f32 v117, v118, v119
	v_pk_fma_f32 v[130:131], v[130:131], v[42:43], v[194:195]
	v_pk_fma_f32 v[128:129], v[128:129], v[40:41], v[196:197]
	v_cvt_pk_bf16_f32 v126, v126, v127
	v_cvt_pk_bf16_f32 v127, v124, v125
	v_pk_fma_f32 v[122:123], v[122:123], v[42:43], v[218:219]
	v_pk_fma_f32 v[120:121], v[120:121], v[40:41], v[220:221]
	global_store_dwordx2 v[202:203], v[116:117], off offset:288
	v_lshl_add_u64 v[116:117], v[170:171], 0, v[158:159]
	v_lshlrev_b32_e32 v186, 16, v187
	v_and_b32_e32 v187, 0xffff0000, v187
	v_lshlrev_b32_e32 v192, 16, v190
	v_and_b32_e32 v193, 0xffff0000, v190
	v_lshlrev_b32_e32 v190, 16, v191
	v_and_b32_e32 v191, 0xffff0000, v191
	v_cvt_pk_bf16_f32 v128, v128, v129
	v_cvt_pk_bf16_f32 v129, v130, v131
	global_store_dwordx2 v[202:203], v[126:127], off offset:32
	v_cvt_pk_bf16_f32 v120, v120, v121
	v_cvt_pk_bf16_f32 v121, v122, v123
	global_load_dwordx2 v[118:119], v[116:117], off
	global_load_dwordx2 v[122:123], v[116:117], off offset:32
	global_load_dwordx2 v[126:127], v[116:117], off offset:256
	global_load_dwordx2 v[130:131], v[116:117], off offset:288
	v_pk_fma_f32 v[146:147], v[146:147], v[50:51], v[186:187]
	v_pk_fma_f32 v[144:145], v[144:145], v[48:49], v[188:189]
	v_pk_fma_f32 v[142:143], v[142:143], v[46:47], v[190:191]
	v_pk_fma_f32 v[140:141], v[140:141], v[44:45], v[192:193]
	v_lshl_add_u64 v[134:135], v[170:171], 0, v[160:161]
	v_cvt_pk_bf16_f32 v144, v144, v145
	v_cvt_pk_bf16_f32 v145, v146, v147
	v_cvt_pk_bf16_f32 v140, v140, v141
	v_cvt_pk_bf16_f32 v141, v142, v143
	global_load_dwordx2 v[136:137], v[134:135], off
	s_waitcnt vmcnt(0)
	v_lshlrev_b32_e32 v124, 16, v122
	global_store_dwordx2 v[184:185], v[144:145], off
	global_store_dwordx2 v[184:185], v[140:141], off offset:32
	global_store_dwordx2 v[184:185], v[128:129], off offset:256
	global_load_dwordx2 v[140:141], v[134:135], off offset:32
	v_lshlrev_b32_e32 v132, 16, v130
	global_load_dwordx2 v[144:145], v[134:135], off offset:256
	global_load_dwordx2 v[184:185], v[134:135], off offset:288
	v_and_b32_e32 v133, 0xffff0000, v130
	v_lshlrev_b32_e32 v130, 16, v131
	v_and_b32_e32 v131, 0xffff0000, v131
	v_pk_fma_f32 v[94:95], v[94:95], v[38:39], v[130:131]
	v_pk_fma_f32 v[92:93], v[92:93], v[36:37], v[132:133]
	v_lshlrev_b32_e32 v138, 16, v136
	v_and_b32_e32 v139, 0xffff0000, v136
	v_lshlrev_b32_e32 v136, 16, v137
	v_and_b32_e32 v137, 0xffff0000, v137
	v_cvt_pk_bf16_f32 v92, v92, v93
	v_cvt_pk_bf16_f32 v93, v94, v95
	global_store_dwordx2 v[116:117], v[92:93], off offset:288
	v_pk_fma_f32 v[92:93], v[106:107], v[50:51], v[136:137]
	v_pk_fma_f32 v[94:95], v[104:105], v[48:49], v[138:139]
	v_lshlrev_b32_e32 v128, 16, v126
	v_cvt_pk_bf16_f32 v94, v94, v95
	v_cvt_pk_bf16_f32 v95, v92, v93
	v_and_b32_e32 v129, 0xffff0000, v126
	v_lshlrev_b32_e32 v126, 16, v127
	v_and_b32_e32 v127, 0xffff0000, v127
	global_store_dwordx2 v[134:135], v[94:95], off
	v_pk_fma_f32 v[98:99], v[98:99], v[42:43], v[126:127]
	v_pk_fma_f32 v[96:97], v[96:97], v[40:41], v[128:129]
	global_store_dwordx2 v[202:203], v[120:121], off offset:256
	v_lshlrev_b32_e32 v120, 16, v118
	v_and_b32_e32 v121, 0xffff0000, v118
	v_lshlrev_b32_e32 v118, 16, v119
	v_and_b32_e32 v119, 0xffff0000, v119
	v_and_b32_e32 v125, 0xffff0000, v122
	v_lshlrev_b32_e32 v122, 16, v123
	v_and_b32_e32 v123, 0xffff0000, v123
	v_cvt_pk_bf16_f32 v96, v96, v97
	v_cvt_pk_bf16_f32 v97, v98, v99
	v_pk_fma_f32 v[114:115], v[114:115], v[50:51], v[118:119]
	v_pk_fma_f32 v[112:113], v[112:113], v[48:49], v[120:121]
	v_pk_fma_f32 v[110:111], v[110:111], v[46:47], v[122:123]
	v_pk_fma_f32 v[108:109], v[108:109], v[44:45], v[124:125]
	v_cvt_pk_bf16_f32 v112, v112, v113
	v_cvt_pk_bf16_f32 v113, v114, v115
	v_cvt_pk_bf16_f32 v108, v108, v109
	v_cvt_pk_bf16_f32 v109, v110, v111
	global_store_dwordx2 v[116:117], v[112:113], off
	global_store_dwordx2 v[116:117], v[108:109], off offset:32
	global_store_dwordx2 v[116:117], v[96:97], off offset:256
	s_waitcnt vmcnt(0)
	v_lshlrev_b32_e32 v142, 16, v140
	v_and_b32_e32 v143, 0xffff0000, v140
	v_lshlrev_b32_e32 v140, 16, v141
	v_lshlrev_b32_e32 v186, 16, v184
	v_and_b32_e32 v187, 0xffff0000, v184
	v_lshlrev_b32_e32 v184, 16, v185
	v_and_b32_e32 v185, 0xffff0000, v185
	v_and_b32_e32 v141, 0xffff0000, v141
	v_pk_fma_f32 v[86:87], v[86:87], v[38:39], v[184:185]
	v_pk_fma_f32 v[84:85], v[84:85], v[36:37], v[186:187]
	v_lshlrev_b32_e32 v146, 16, v144
	v_and_b32_e32 v147, 0xffff0000, v144
	v_lshlrev_b32_e32 v144, 16, v145
	v_and_b32_e32 v145, 0xffff0000, v145
	v_pk_fma_f32 v[92:93], v[102:103], v[46:47], v[140:141]
	v_pk_fma_f32 v[94:95], v[100:101], v[44:45], v[142:143]
	v_cvt_pk_bf16_f32 v84, v84, v85
	v_cvt_pk_bf16_f32 v85, v86, v87
	v_cvt_pk_bf16_f32 v94, v94, v95
	v_cvt_pk_bf16_f32 v95, v92, v93
	v_pk_fma_f32 v[90:91], v[90:91], v[42:43], v[144:145]
	v_pk_fma_f32 v[88:89], v[88:89], v[40:41], v[146:147]
	global_store_dwordx2 v[134:135], v[84:85], off offset:288
	v_lshl_add_u64 v[84:85], v[170:171], 0, v[162:163]
	global_store_dwordx2 v[134:135], v[94:95], off offset:32
	v_cvt_pk_bf16_f32 v88, v88, v89
	v_cvt_pk_bf16_f32 v89, v90, v91
	global_load_dwordx2 v[90:91], v[84:85], off offset:32
	global_load_dwordx2 v[94:95], v[84:85], off offset:256
	global_load_dwordx2 v[98:99], v[84:85], off offset:288
	v_lshl_add_u64 v[102:103], v[170:171], 0, v[164:165]
	global_load_dwordx2 v[104:105], v[102:103], off
	global_load_dwordx2 v[108:109], v[102:103], off offset:32
	global_load_dwordx2 v[112:113], v[102:103], off offset:256
	global_load_dwordx2 v[116:117], v[102:103], off offset:288
	s_waitcnt vmcnt(0)
	v_lshlrev_b32_e32 v96, 16, v94
	v_lshlrev_b32_e32 v100, 16, v98
	v_and_b32_e32 v101, 0xffff0000, v98
	v_lshlrev_b32_e32 v98, 16, v99
	v_and_b32_e32 v99, 0xffff0000, v99
	v_pk_fma_f32 v[62:63], v[62:63], v[38:39], v[98:99]
	v_pk_fma_f32 v[60:61], v[60:61], v[36:37], v[100:101]
	v_lshlrev_b32_e32 v106, 16, v104
	v_and_b32_e32 v107, 0xffff0000, v104
	v_lshlrev_b32_e32 v104, 16, v105
	v_and_b32_e32 v105, 0xffff0000, v105
	v_cvt_pk_bf16_f32 v60, v60, v61
	v_cvt_pk_bf16_f32 v61, v62, v63
	v_lshlrev_b32_e32 v118, 16, v116
	v_and_b32_e32 v119, 0xffff0000, v116
	v_lshlrev_b32_e32 v116, 16, v117
	v_and_b32_e32 v117, 0xffff0000, v117
	global_store_dwordx2 v[84:85], v[60:61], off offset:288
	v_pk_fma_f32 v[60:61], v[74:75], v[50:51], v[104:105]
	v_pk_fma_f32 v[62:63], v[72:73], v[48:49], v[106:107]
	v_lshlrev_b32_e32 v110, 16, v108
	v_and_b32_e32 v111, 0xffff0000, v108
	v_lshlrev_b32_e32 v108, 16, v109
	v_and_b32_e32 v109, 0xffff0000, v109
	v_lshlrev_b32_e32 v114, 16, v112
	v_and_b32_e32 v115, 0xffff0000, v112
	v_lshlrev_b32_e32 v112, 16, v113
	v_and_b32_e32 v113, 0xffff0000, v113
	v_cvt_pk_bf16_f32 v62, v62, v63
	v_cvt_pk_bf16_f32 v63, v60, v61
	v_pk_fma_f32 v[54:55], v[54:55], v[38:39], v[116:117]
	v_pk_fma_f32 v[52:53], v[52:53], v[36:37], v[118:119]
	global_store_dwordx2 v[102:103], v[62:63], off
	v_pk_fma_f32 v[60:61], v[70:71], v[46:47], v[108:109]
	v_pk_fma_f32 v[62:63], v[68:69], v[44:45], v[110:111]
	v_pk_fma_f32 v[58:59], v[58:59], v[42:43], v[112:113]
	v_pk_fma_f32 v[56:57], v[56:57], v[40:41], v[114:115]
	v_cvt_pk_bf16_f32 v52, v52, v53
	v_cvt_pk_bf16_f32 v53, v54, v55
	v_cvt_pk_bf16_f32 v62, v62, v63
	v_cvt_pk_bf16_f32 v63, v60, v61
	v_cvt_pk_bf16_f32 v56, v56, v57
	v_cvt_pk_bf16_f32 v57, v58, v59
	global_store_dwordx2 v[102:103], v[52:53], off offset:288
	v_lshl_add_u64 v[52:53], v[170:171], 0, v[166:167]
	global_store_dwordx2 v[134:135], v[88:89], off offset:256
	global_load_dwordx2 v[88:89], v[84:85], off
	v_and_b32_e32 v97, 0xffff0000, v94
	global_store_dwordx2 v[102:103], v[62:63], off offset:32
	global_store_dwordx2 v[102:103], v[56:57], off offset:256
	global_load_dwordx2 v[56:57], v[52:53], off
	v_lshlrev_b32_e32 v94, 16, v95
	global_load_dwordx2 v[60:61], v[52:53], off offset:32
	global_load_dwordx2 v[62:63], v[52:53], off offset:256
	v_and_b32_e32 v95, 0xffff0000, v95
	v_pk_fma_f32 v[66:67], v[66:67], v[42:43], v[94:95]
	v_pk_fma_f32 v[64:65], v[64:65], v[40:41], v[96:97]
	s_waitcnt vmcnt(0)
	v_lshlrev_b32_e32 v86, 16, v88
	v_cvt_pk_bf16_f32 v64, v64, v65
	v_cvt_pk_bf16_f32 v65, v66, v67
	global_store_dwordx2 v[84:85], v[64:65], off offset:256
	v_and_b32_e32 v87, 0xffff0000, v88
	v_lshlrev_b32_e32 v88, 16, v89
	v_and_b32_e32 v89, 0xffff0000, v89
	v_lshlrev_b32_e32 v64, 16, v62
	v_and_b32_e32 v65, 0xffff0000, v62
	v_lshlrev_b32_e32 v66, 16, v63
	v_and_b32_e32 v67, 0xffff0000, v63
	global_load_dwordx2 v[62:63], v[52:53], off offset:288
	v_lshlrev_b32_e32 v92, 16, v90
	v_and_b32_e32 v93, 0xffff0000, v90
	v_lshlrev_b32_e32 v90, 16, v91
	v_and_b32_e32 v91, 0xffff0000, v91
	v_pk_fma_f32 v[78:79], v[78:79], v[46:47], v[90:91]
	v_pk_fma_f32 v[76:77], v[76:77], v[44:45], v[92:93]
	v_pk_fma_f32 v[82:83], v[82:83], v[50:51], v[88:89]
	v_cvt_pk_bf16_f32 v76, v76, v77
	v_cvt_pk_bf16_f32 v77, v78, v79
	v_pk_fma_f32 v[80:81], v[80:81], v[48:49], v[86:87]
	global_store_dwordx2 v[84:85], v[76:77], off offset:32
	v_cvt_pk_bf16_f32 v80, v80, v81
	v_cvt_pk_bf16_f32 v81, v82, v83
	global_store_dwordx2 v[84:85], v[80:81], off
	v_lshlrev_b32_e32 v58, 16, v60
	v_and_b32_e32 v59, 0xffff0000, v60
	v_lshlrev_b32_e32 v60, 16, v61
	v_and_b32_e32 v61, 0xffff0000, v61
	v_pk_fma_f32 v[14:15], v[14:15], v[46:47], v[60:61]
	v_pk_fma_f32 v[12:13], v[12:13], v[44:45], v[58:59]
	v_lshlrev_b32_e32 v54, 16, v56
	v_cvt_pk_bf16_f32 v12, v12, v13
	v_cvt_pk_bf16_f32 v13, v14, v15
	global_store_dwordx2 v[52:53], v[12:13], off offset:32
	v_pk_fma_f32 v[12:13], v[34:35], v[42:43], v[66:67]
	v_pk_fma_f32 v[14:15], v[32:33], v[40:41], v[64:65]
	v_and_b32_e32 v55, 0xffff0000, v56
	v_lshlrev_b32_e32 v56, 16, v57
	v_and_b32_e32 v57, 0xffff0000, v57
	v_cvt_pk_bf16_f32 v14, v14, v15
	v_cvt_pk_bf16_f32 v15, v12, v13
	v_pk_fma_f32 v[18:19], v[18:19], v[50:51], v[56:57]
	v_pk_fma_f32 v[16:17], v[16:17], v[48:49], v[54:55]
	global_store_dwordx2 v[52:53], v[14:15], off offset:256
	v_cvt_pk_bf16_f32 v16, v16, v17
	v_cvt_pk_bf16_f32 v17, v18, v19
	global_store_dwordx2 v[52:53], v[16:17], off
	s_waitcnt vmcnt(0)
	v_lshlrev_b32_e32 v68, 16, v62
	v_and_b32_e32 v69, 0xffff0000, v62
	v_lshlrev_b32_e32 v70, 16, v63
	v_and_b32_e32 v71, 0xffff0000, v63
	v_lshl_add_u64 v[62:63], v[170:171], 0, v[168:169]
	global_load_dwordx2 v[74:75], v[62:63], off
	global_load_dwordx2 v[78:79], v[62:63], off offset:32
	global_load_dwordx2 v[82:83], v[62:63], off offset:256
	global_load_dwordx2 v[84:85], v[62:63], off offset:288
	v_pk_fma_f32 v[12:13], v[30:31], v[38:39], v[70:71]
	v_pk_fma_f32 v[14:15], v[28:29], v[36:37], v[68:69]
	s_waitcnt vmcnt(0)
	v_lshlrev_b32_e32 v72, 16, v74
	v_lshlrev_b32_e32 v76, 16, v78
	v_and_b32_e32 v77, 0xffff0000, v78
	v_lshlrev_b32_e32 v78, 16, v79
	v_and_b32_e32 v79, 0xffff0000, v79
	v_pk_fma_f32 v[6:7], v[6:7], v[46:47], v[78:79]
	v_pk_fma_f32 v[4:5], v[4:5], v[44:45], v[76:77]
	v_lshlrev_b32_e32 v80, 16, v82
	v_and_b32_e32 v81, 0xffff0000, v82
	v_lshlrev_b32_e32 v82, 16, v83
	v_and_b32_e32 v83, 0xffff0000, v83
	v_cvt_pk_bf16_f32 v4, v4, v5
	v_cvt_pk_bf16_f32 v5, v6, v7
	global_store_dwordx2 v[62:63], v[4:5], off offset:32
	v_pk_fma_f32 v[4:5], v[26:27], v[42:43], v[82:83]
	v_pk_fma_f32 v[6:7], v[24:25], v[40:41], v[80:81]
	v_and_b32_e32 v73, 0xffff0000, v74
	v_lshlrev_b32_e32 v74, 16, v75
	v_and_b32_e32 v75, 0xffff0000, v75
	v_lshlrev_b32_e32 v86, 16, v84
	v_and_b32_e32 v87, 0xffff0000, v84
	v_lshlrev_b32_e32 v84, 16, v85
	v_and_b32_e32 v85, 0xffff0000, v85
	v_cvt_pk_bf16_f32 v6, v6, v7
	v_cvt_pk_bf16_f32 v7, v4, v5
	v_pk_fma_f32 v[10:11], v[10:11], v[50:51], v[74:75]
	v_pk_fma_f32 v[8:9], v[8:9], v[48:49], v[72:73]
	global_store_dwordx2 v[62:63], v[6:7], off offset:256
	v_pk_fma_f32 v[4:5], v[22:23], v[38:39], v[84:85]
	v_pk_fma_f32 v[6:7], v[20:21], v[36:37], v[86:87]
	v_cvt_pk_bf16_f32 v14, v14, v15
	v_cvt_pk_bf16_f32 v15, v12, v13
	v_cvt_pk_bf16_f32 v8, v8, v9
	v_cvt_pk_bf16_f32 v9, v10, v11
	v_cvt_pk_bf16_f32 v6, v6, v7
	v_cvt_pk_bf16_f32 v7, v4, v5
	v_mov_b32_e32 v42, v182
	v_mov_b32_e32 v40, v179
	v_mov_b32_e32 v38, v178
	v_mov_b32_e32 v36, v177
	global_store_dwordx2 v[52:53], v[14:15], off offset:288
	global_store_dwordx2 v[62:63], v[8:9], off
	global_store_dwordx2 v[62:63], v[6:7], off offset:288
	s_cbranch_vccz .LBB0_1317
	s_waitcnt vmcnt(0)
	s_cmpk_gt_u32 s23, 0xff
	s_cbranch_scc1 .LBB0_1328
	s_barrier

.LBB0_2087:
	s_add_u32 s34, s46, s2
	s_addc_u32 s35, s47, s3
	s_add_u32 s36, s34, 0x1701b100
	s_addc_u32 s42, s35, 0
	s_add_u32 s68, s0, s2
	s_addc_u32 s69, s1, s3
	s_add_i32 s70, 0, 0x10000
	v_add_u32_e32 v137, s70, v154
	ds_read_b128 v[160:163], v137
	ds_read_b128 v[164:167], v137 offset:1024
	ds_read_b128 v[168:171], v137 offset:2048
	ds_read_b128 v[172:175], v137 offset:3072
	s_cmpk_eq_i32 s2, 0x700
	s_cselect_b64 vcc, -1, 0
	s_and_b64 s[34:35], vcc, exec
	v_cndmask_b32_e32 v2, v138, v156, vcc
	s_cselect_b32 s43, s49, s42
	s_cselect_b32 s42, s48, s36
	v_cndmask_b32_e32 v206, v140, v157, vcc
	v_cndmask_b32_e32 v137, v142, v158, vcc
	v_cndmask_b32_e32 v139, v144, v159, vcc
	s_cselect_b32 s35, s41, s69
	s_cselect_b32 s34, s40, s68
	v_lshl_add_u64 v[208:209], v[148:149], 0, s[2:3]
	s_add_i32 m0, s27, 0xc000
	ds_read_b128 v[176:179], v155
	ds_read_b128 v[182:185], v155 offset:1024
	ds_read_b128 v[186:189], v155 offset:2048
	ds_read_b128 v[190:193], v155 offset:3072
	ds_read_b128 v[194:197], v155 offset:4096
	ds_read_b128 v[198:201], v155 offset:5120
	ds_read_b128 v[202:205], v155 offset:6144
	ds_read_b128 v[214:217], v155 offset:7168
	global_load_lds_dwordx4 v[208:209], off
	v_lshl_add_u64 v[208:209], v[146:147], 0, s[2:3]
	s_add_i32 m0, s27, 0xe000
	s_nop 0
	global_load_lds_dwordx4 v[208:209], off
	s_waitcnt lgkmcnt(8)
	s_barrier
	s_waitcnt lgkmcnt(0)
	s_waitcnt lgkmcnt(0)
	v_mfma_f32_16x16x32_bf16 v[128:131], v[160:163], v[176:179], v[128:131]
	v_mfma_f32_16x16x32_bf16 v[120:123], v[168:171], v[176:179], v[120:123]
	v_mfma_f32_16x16x32_bf16 v[112:115], v[160:163], v[186:189], v[112:115]
	v_mfma_f32_16x16x32_bf16 v[104:107], v[168:171], v[186:189], v[104:107]
	v_mfma_f32_16x16x32_bf16 v[96:99], v[160:163], v[194:197], v[96:99]
	v_mfma_f32_16x16x32_bf16 v[88:91], v[168:171], v[194:197], v[88:91]
	v_mfma_f32_16x16x32_bf16 v[80:83], v[160:163], v[202:205], v[80:83]
	v_mfma_f32_16x16x32_bf16 v[72:75], v[168:171], v[202:205], v[72:75]
	v_mfma_f32_16x16x32_bf16 v[128:131], v[164:167], v[182:185], v[128:131]
	v_mfma_f32_16x16x32_bf16 v[120:123], v[172:175], v[182:185], v[120:123]
	v_mfma_f32_16x16x32_bf16 v[112:115], v[164:167], v[190:193], v[112:115]
	v_mfma_f32_16x16x32_bf16 v[104:107], v[172:175], v[190:193], v[104:107]
	v_mfma_f32_16x16x32_bf16 v[96:99], v[164:167], v[198:201], v[96:99]
	v_mfma_f32_16x16x32_bf16 v[88:91], v[172:175], v[198:201], v[88:91]
	v_mfma_f32_16x16x32_bf16 v[80:83], v[164:167], v[214:217], v[80:83]
	v_mfma_f32_16x16x32_bf16 v[72:75], v[172:175], v[214:217], v[72:75]
	s_barrier
	s_add_i32 s36, 0, 0x14000
	s_add_i32 s68, s70, s26
	v_add_u32_e32 v143, s36, v154
	v_lshl_add_u64 v[208:209], s[34:35], 0, v[132:133]
	s_mov_b32 m0, s68
	ds_read_b128 v[218:221], v143
	ds_read_b128 v[222:225], v143 offset:1024
	ds_read_b128 v[226:229], v143 offset:2048
	ds_read_b128 v[230:233], v143 offset:3072
	global_load_lds_dwordx4 v[208:209], off
	v_lshl_add_u64 v[234:235], s[34:35], 0, v[134:135]
	s_add_i32 m0, s68, 0x2000
	s_nop 0
	global_load_lds_dwordx4 v[234:235], off
	s_barrier
	s_waitcnt lgkmcnt(0)
	s_waitcnt lgkmcnt(0)
	v_mfma_f32_16x16x32_bf16 v[124:127], v[218:221], v[176:179], v[124:127]
	v_mfma_f32_16x16x32_bf16 v[116:119], v[226:229], v[176:179], v[116:119]
	v_mfma_f32_16x16x32_bf16 v[108:111], v[218:221], v[186:189], v[108:111]
	v_mfma_f32_16x16x32_bf16 v[100:103], v[226:229], v[186:189], v[100:103]
	v_mfma_f32_16x16x32_bf16 v[92:95], v[218:221], v[194:197], v[92:95]
	v_mfma_f32_16x16x32_bf16 v[84:87], v[226:229], v[194:197], v[84:87]
	v_mfma_f32_16x16x32_bf16 v[76:79], v[218:221], v[202:205], v[76:79]
	v_mfma_f32_16x16x32_bf16 v[68:71], v[226:229], v[202:205], v[68:71]
	v_mfma_f32_16x16x32_bf16 v[124:127], v[222:225], v[182:185], v[124:127]
	v_mfma_f32_16x16x32_bf16 v[116:119], v[230:233], v[182:185], v[116:119]
	v_mfma_f32_16x16x32_bf16 v[108:111], v[222:225], v[190:193], v[108:111]
	v_mfma_f32_16x16x32_bf16 v[100:103], v[230:233], v[190:193], v[100:103]
	v_mfma_f32_16x16x32_bf16 v[92:95], v[222:225], v[198:201], v[92:95]
	v_mfma_f32_16x16x32_bf16 v[84:87], v[230:233], v[198:201], v[84:87]
	v_mfma_f32_16x16x32_bf16 v[76:79], v[222:225], v[214:217], v[76:79]
	v_mfma_f32_16x16x32_bf16 v[68:71], v[230:233], v[214:217], v[68:71]
	s_mov_b32 m0, s27
	s_barrier
	ds_read_b128 v[176:179], v155 offset:16384
	ds_read_b128 v[182:185], v155 offset:17408
	ds_read_b128 v[186:189], v155 offset:18432
	ds_read_b128 v[190:193], v155 offset:19456
	ds_read_b128 v[194:197], v155 offset:20480
	ds_read_b128 v[198:201], v155 offset:21504
	ds_read_b128 v[202:205], v155 offset:22528
	ds_read_b128 v[214:217], v155 offset:23552
	global_load_lds_dwordx4 v2, s[42:43]
	s_mov_b32 m0, s58
	v_mov_b32_e32 v207, v3
	global_load_lds_dwordx4 v206, s[42:43]
	s_barrier
	s_waitcnt lgkmcnt(0)
	v_lshl_add_u64 v[236:237], s[42:43], 0, v[2:3]
	v_lshl_add_u64 v[206:207], s[42:43], 0, v[206:207]
	s_waitcnt lgkmcnt(0)
	v_mfma_f32_16x16x32_bf16 v[64:67], v[160:163], v[176:179], v[64:67]
	v_mfma_f32_16x16x32_bf16 v[56:59], v[168:171], v[176:179], v[56:59]
	v_mfma_f32_16x16x32_bf16 v[48:51], v[160:163], v[186:189], v[48:51]
	v_mfma_f32_16x16x32_bf16 v[40:43], v[168:171], v[186:189], v[40:43]
	v_mfma_f32_16x16x32_bf16 v[24:27], v[160:163], v[194:197], v[24:27]
	v_mfma_f32_16x16x32_bf16 v[20:23], v[168:171], v[194:197], v[20:23]
	v_mfma_f32_16x16x32_bf16 v[8:11], v[160:163], v[202:205], v[8:11]
	v_mfma_f32_16x16x32_bf16 v[4:7], v[168:171], v[202:205], v[4:7]
	v_mfma_f32_16x16x32_bf16 v[64:67], v[164:167], v[182:185], v[64:67]
	v_mfma_f32_16x16x32_bf16 v[56:59], v[172:175], v[182:185], v[56:59]
	v_mfma_f32_16x16x32_bf16 v[48:51], v[164:167], v[190:193], v[48:51]
	v_mfma_f32_16x16x32_bf16 v[40:43], v[172:175], v[190:193], v[40:43]
	v_mfma_f32_16x16x32_bf16 v[24:27], v[164:167], v[198:201], v[24:27]
	v_mfma_f32_16x16x32_bf16 v[20:23], v[172:175], v[198:201], v[20:23]
	v_mfma_f32_16x16x32_bf16 v[8:11], v[164:167], v[214:217], v[8:11]
	v_mfma_f32_16x16x32_bf16 v[4:7], v[172:175], v[214:217], v[4:7]
	s_barrier
	s_add_u32 s68, s34, 0x40000
	s_addc_u32 s69, s35, 0
	s_add_i32 s36, s36, s26
	v_lshl_add_u64 v[160:161], s[68:69], 0, v[132:133]
	s_mov_b32 m0, s36
	s_nop 0
	global_load_lds_dwordx4 v[160:161], off
	v_lshl_add_u64 v[160:161], s[68:69], 0, v[134:135]
	s_add_i32 m0, s36, 0x2000
	s_nop 0
	global_load_lds_dwordx4 v[160:161], off
	s_waitcnt vmcnt(6)
	s_barrier
	v_mfma_f32_16x16x32_bf16 v[60:63], v[218:221], v[176:179], v[60:63]
	v_mfma_f32_16x16x32_bf16 v[52:55], v[226:229], v[176:179], v[52:55]
	v_mfma_f32_16x16x32_bf16 v[44:47], v[218:221], v[186:189], v[44:47]
	v_mfma_f32_16x16x32_bf16 v[36:39], v[226:229], v[186:189], v[36:39]
	v_mfma_f32_16x16x32_bf16 v[32:35], v[218:221], v[194:197], v[32:35]
	v_mfma_f32_16x16x32_bf16 v[28:31], v[226:229], v[194:197], v[28:31]
	v_mfma_f32_16x16x32_bf16 v[16:19], v[218:221], v[202:205], v[16:19]
	v_mfma_f32_16x16x32_bf16 v[12:15], v[226:229], v[202:205], v[12:15]
	v_mfma_f32_16x16x32_bf16 v[60:63], v[222:225], v[182:185], v[60:63]
	v_mfma_f32_16x16x32_bf16 v[52:55], v[230:233], v[182:185], v[52:55]
	v_mfma_f32_16x16x32_bf16 v[44:47], v[222:225], v[190:193], v[44:47]
	v_mfma_f32_16x16x32_bf16 v[36:39], v[230:233], v[190:193], v[36:39]
	v_mfma_f32_16x16x32_bf16 v[32:35], v[222:225], v[198:201], v[32:35]
	v_mfma_f32_16x16x32_bf16 v[28:31], v[230:233], v[198:201], v[28:31]
	v_mfma_f32_16x16x32_bf16 v[16:19], v[222:225], v[214:217], v[16:19]
	v_mfma_f32_16x16x32_bf16 v[12:15], v[230:233], v[214:217], v[12:15]
	s_add_i32 s36, 0, 0x18000
	v_add_u32_e32 v2, s36, v154
	s_barrier
	ds_read_b128 v[160:163], v2
	ds_read_b128 v[164:167], v2 offset:1024
	ds_read_b128 v[168:171], v2 offset:2048
	ds_read_b128 v[172:175], v2 offset:3072
	s_mov_b32 m0, s59
	ds_read_b128 v[176:179], v155 offset:32768
	ds_read_b128 v[182:185], v155 offset:33792
	ds_read_b128 v[186:189], v155 offset:34816
	ds_read_b128 v[190:193], v155 offset:35840
	ds_read_b128 v[194:197], v155 offset:36864
	ds_read_b128 v[198:201], v155 offset:37888
	ds_read_b128 v[202:205], v155 offset:38912
	ds_read_b128 v[214:217], v155 offset:39936
	global_load_lds_dwordx4 v137, s[42:43]
	s_mov_b32 m0, s60
	s_nop 0
	global_load_lds_dwordx4 v139, s[42:43]
	s_waitcnt lgkmcnt(8)
	s_barrier
	s_waitcnt lgkmcnt(0)
	s_waitcnt lgkmcnt(0)
	v_mfma_f32_16x16x32_bf16 v[128:131], v[160:163], v[176:179], v[128:131]
	v_mfma_f32_16x16x32_bf16 v[120:123], v[168:171], v[176:179], v[120:123]
	v_mfma_f32_16x16x32_bf16 v[112:115], v[160:163], v[186:189], v[112:115]
	v_mfma_f32_16x16x32_bf16 v[104:107], v[168:171], v[186:189], v[104:107]
	v_mfma_f32_16x16x32_bf16 v[96:99], v[160:163], v[194:197], v[96:99]
	v_mfma_f32_16x16x32_bf16 v[88:91], v[168:171], v[194:197], v[88:91]
	v_mfma_f32_16x16x32_bf16 v[80:83], v[160:163], v[202:205], v[80:83]
	v_mfma_f32_16x16x32_bf16 v[72:75], v[168:171], v[202:205], v[72:75]
	v_mfma_f32_16x16x32_bf16 v[128:131], v[164:167], v[182:185], v[128:131]
	v_mfma_f32_16x16x32_bf16 v[120:123], v[172:175], v[182:185], v[120:123]
	v_mfma_f32_16x16x32_bf16 v[112:115], v[164:167], v[190:193], v[112:115]
	v_mfma_f32_16x16x32_bf16 v[104:107], v[172:175], v[190:193], v[104:107]
	v_mfma_f32_16x16x32_bf16 v[96:99], v[164:167], v[198:201], v[96:99]
	v_mfma_f32_16x16x32_bf16 v[88:91], v[172:175], v[198:201], v[88:91]
	v_mfma_f32_16x16x32_bf16 v[80:83], v[164:167], v[214:217], v[80:83]
	v_mfma_f32_16x16x32_bf16 v[72:75], v[172:175], v[214:217], v[72:75]
	s_barrier
	s_add_i32 s42, 0, 0x1c000
	s_add_i32 s36, s36, s26
	v_add_u32_e32 v2, s42, v154
	v_lshl_add_u64 v[208:209], v[208:209], 0, s[8:9]
	s_mov_b32 m0, s36
	ds_read_b128 v[218:221], v2
	ds_read_b128 v[222:225], v2 offset:1024
	ds_read_b128 v[226:229], v2 offset:2048
	ds_read_b128 v[230:233], v2 offset:3072
	global_load_lds_dwordx4 v[208:209], off
	v_lshl_add_u64 v[208:209], v[234:235], 0, s[8:9]
	s_add_i32 m0, s36, 0x2000
	s_nop 0
	global_load_lds_dwordx4 v[208:209], off
	s_barrier
	s_waitcnt lgkmcnt(0)
	s_waitcnt lgkmcnt(0)
	v_mfma_f32_16x16x32_bf16 v[124:127], v[218:221], v[176:179], v[124:127]
	v_mfma_f32_16x16x32_bf16 v[116:119], v[226:229], v[176:179], v[116:119]
	v_mfma_f32_16x16x32_bf16 v[108:111], v[218:221], v[186:189], v[108:111]
	v_mfma_f32_16x16x32_bf16 v[100:103], v[226:229], v[186:189], v[100:103]
	v_mfma_f32_16x16x32_bf16 v[92:95], v[218:221], v[194:197], v[92:95]
	v_mfma_f32_16x16x32_bf16 v[84:87], v[226:229], v[194:197], v[84:87]
	v_mfma_f32_16x16x32_bf16 v[76:79], v[218:221], v[202:205], v[76:79]
	v_mfma_f32_16x16x32_bf16 v[68:71], v[226:229], v[202:205], v[68:71]
	v_mfma_f32_16x16x32_bf16 v[124:127], v[222:225], v[182:185], v[124:127]
	v_mfma_f32_16x16x32_bf16 v[116:119], v[230:233], v[182:185], v[116:119]
	v_mfma_f32_16x16x32_bf16 v[108:111], v[222:225], v[190:193], v[108:111]
	v_mfma_f32_16x16x32_bf16 v[100:103], v[230:233], v[190:193], v[100:103]
	v_mfma_f32_16x16x32_bf16 v[92:95], v[222:225], v[198:201], v[92:95]
	v_mfma_f32_16x16x32_bf16 v[84:87], v[230:233], v[198:201], v[84:87]
	v_mfma_f32_16x16x32_bf16 v[76:79], v[222:225], v[214:217], v[76:79]
	v_mfma_f32_16x16x32_bf16 v[68:71], v[230:233], v[214:217], v[68:71]
	s_mov_b32 m0, s61
	v_lshl_add_u64 v[208:209], v[236:237], 0, s[8:9]
	s_barrier
	ds_read_b128 v[176:179], v155 offset:49152
	ds_read_b128 v[182:185], v155 offset:50176
	ds_read_b128 v[186:189], v155 offset:51200
	ds_read_b128 v[190:193], v155 offset:52224
	ds_read_b128 v[194:197], v155 offset:53248
	ds_read_b128 v[198:201], v155 offset:54272
	ds_read_b128 v[202:205], v155 offset:55296
	ds_read_b128 v[214:217], v155 offset:56320
	global_load_lds_dwordx4 v[208:209], off
	v_lshl_add_u64 v[206:207], v[206:207], 0, s[8:9]
	s_mov_b32 m0, s62
	s_nop 0
	global_load_lds_dwordx4 v[206:207], off
	s_barrier
	s_waitcnt lgkmcnt(0)
	s_waitcnt lgkmcnt(0)
	v_mfma_f32_16x16x32_bf16 v[64:67], v[160:163], v[176:179], v[64:67]
	v_mfma_f32_16x16x32_bf16 v[56:59], v[168:171], v[176:179], v[56:59]
	v_mfma_f32_16x16x32_bf16 v[48:51], v[160:163], v[186:189], v[48:51]
	v_mfma_f32_16x16x32_bf16 v[40:43], v[168:171], v[186:189], v[40:43]
	v_mfma_f32_16x16x32_bf16 v[24:27], v[160:163], v[194:197], v[24:27]
	v_mfma_f32_16x16x32_bf16 v[20:23], v[168:171], v[194:197], v[20:23]
	v_mfma_f32_16x16x32_bf16 v[8:11], v[160:163], v[202:205], v[8:11]
	v_mfma_f32_16x16x32_bf16 v[4:7], v[168:171], v[202:205], v[4:7]
	v_mfma_f32_16x16x32_bf16 v[64:67], v[164:167], v[182:185], v[64:67]
	v_mfma_f32_16x16x32_bf16 v[56:59], v[172:175], v[182:185], v[56:59]
	v_mfma_f32_16x16x32_bf16 v[48:51], v[164:167], v[190:193], v[48:51]
	v_mfma_f32_16x16x32_bf16 v[40:43], v[172:175], v[190:193], v[40:43]
	v_mfma_f32_16x16x32_bf16 v[24:27], v[164:167], v[198:201], v[24:27]
	v_mfma_f32_16x16x32_bf16 v[20:23], v[172:175], v[198:201], v[20:23]
	v_mfma_f32_16x16x32_bf16 v[8:11], v[164:167], v[214:217], v[8:11]
	v_mfma_f32_16x16x32_bf16 v[4:7], v[172:175], v[214:217], v[4:7]
	s_barrier
	s_add_u32 s34, s34, 0x40080
	s_addc_u32 s35, s35, 0
	s_add_i32 s36, s42, s26
	v_lshl_add_u64 v[160:161], s[34:35], 0, v[132:133]
	s_mov_b32 m0, s36
	s_nop 0
	global_load_lds_dwordx4 v[160:161], off
	v_lshl_add_u64 v[160:161], s[34:35], 0, v[134:135]
	s_add_i32 m0, s36, 0x2000
	s_nop 0
	global_load_lds_dwordx4 v[160:161], off
	s_waitcnt vmcnt(6)
	s_barrier
	v_mfma_f32_16x16x32_bf16 v[60:63], v[218:221], v[176:179], v[60:63]
	v_mfma_f32_16x16x32_bf16 v[52:55], v[226:229], v[176:179], v[52:55]
	v_mfma_f32_16x16x32_bf16 v[44:47], v[218:221], v[186:189], v[44:47]
	v_mfma_f32_16x16x32_bf16 v[36:39], v[226:229], v[186:189], v[36:39]
	v_mfma_f32_16x16x32_bf16 v[32:35], v[218:221], v[194:197], v[32:35]
	v_mfma_f32_16x16x32_bf16 v[28:31], v[226:229], v[194:197], v[28:31]
	v_mfma_f32_16x16x32_bf16 v[16:19], v[218:221], v[202:205], v[16:19]
	v_mfma_f32_16x16x32_bf16 v[12:15], v[226:229], v[202:205], v[12:15]
	v_mfma_f32_16x16x32_bf16 v[60:63], v[222:225], v[182:185], v[60:63]
	v_mfma_f32_16x16x32_bf16 v[52:55], v[230:233], v[182:185], v[52:55]
	v_mfma_f32_16x16x32_bf16 v[44:47], v[222:225], v[190:193], v[44:47]
	v_mfma_f32_16x16x32_bf16 v[36:39], v[230:233], v[190:193], v[36:39]
	v_mfma_f32_16x16x32_bf16 v[32:35], v[222:225], v[198:201], v[32:35]
	v_mfma_f32_16x16x32_bf16 v[28:31], v[230:233], v[198:201], v[28:31]
	v_mfma_f32_16x16x32_bf16 v[16:19], v[222:225], v[214:217], v[16:19]
	v_mfma_f32_16x16x32_bf16 v[12:15], v[230:233], v[214:217], v[12:15]
	s_add_i32 s57, s57, 2
	s_add_u32 s2, s2, 0x100
	s_addc_u32 s3, s3, 0
	s_cmp_gt_u32 s57, 13
	s_barrier
	s_cbranch_scc0 .LBB0_2087
	v_mul_f32_e32 v2, 0xbfb8aa3b, v128
	v_exp_f32_e32 v2, v2
	v_lshl_add_u32 v138, s66, 8, v141
	s_lshl_b32 s2, s67, 7
	v_ashrrev_i32_e32 v139, 31, v138
	v_add_f32_e32 v2, 1.0, v2
	v_rcp_f32_e32 v142, v2
	v_mul_f32_e32 v2, 0xbfb8aa3b, v120
	v_exp_f32_e32 v2, v2
	s_ashr_i32 s3, s2, 31
	s_lshl_b64 s[2:3], s[2:3], 1
	v_mov_b32_e32 v137, v3
	v_add_f32_e32 v2, 1.0, v2
	v_rcp_f32_e32 v144, v2
	v_mul_f32_e32 v2, 0xbfb8aa3b, v129
	v_exp_f32_e32 v2, v2
	s_mov_b32 s0, 0x40000
	v_mov_b32_e32 v140, v157
	s_mov_b32 s67, s56
	v_add_f32_e32 v2, 1.0, v2
	v_rcp_f32_e32 v143, v2
	v_mul_f32_e32 v2, 0xbfb8aa3b, v121
	v_exp_f32_e32 v2, v2
	s_mov_b32 s66, s65
	v_pk_mul_f32 v[128:129], v[128:129], v[142:143]
	v_mov_b32_e32 v142, v158
	v_add_f32_e32 v2, 1.0, v2
	v_rcp_f32_e32 v145, v2
	v_mul_f32_e32 v2, 0xbfb8aa3b, v130
	v_exp_f32_e32 v2, v2
	v_pk_mul_f32 v[124:125], v[128:129], v[124:125]
	v_pk_mul_f32 v[120:121], v[120:121], v[144:145]
	v_mov_b32_e32 v144, v159
	v_add_f32_e32 v2, 1.0, v2
	v_pk_mul_f32 v[116:117], v[120:121], v[116:117]
	v_rcp_f32_e32 v120, v2
	v_mul_f32_e32 v2, 0xbfb8aa3b, v122
	v_exp_f32_e32 v2, v2
	s_nop 0
	v_add_f32_e32 v2, 1.0, v2
	v_rcp_f32_e32 v128, v2
	v_mul_f32_e32 v2, 0xbfb8aa3b, v131
	v_exp_f32_e32 v2, v2
	s_nop 0
	v_add_f32_e32 v2, 1.0, v2
	v_rcp_f32_e32 v121, v2
	v_mul_f32_e32 v2, 0xbfb8aa3b, v123
	v_exp_f32_e32 v2, v2
	v_pk_mul_f32 v[120:121], v[130:131], v[120:121]
	s_nop 0
	v_pk_mul_f32 v[120:121], v[120:121], v[126:127]
	v_add_f32_e32 v2, 1.0, v2
	v_rcp_f32_e32 v129, v2
	v_mul_f32_e32 v2, 0xbfb8aa3b, v112
	v_exp_f32_e32 v2, v2
	v_pk_mul_f32 v[122:123], v[122:123], v[128:129]
	s_nop 0
	v_pk_mul_f32 v[122:123], v[122:123], v[118:119]
	v_cvt_pk_bf16_f32 v119, v120, v121
	v_cvt_pk_bf16_f32 v120, v116, v117
	v_lshlrev_b64 v[116:117], 11, v[138:139]
	v_lshl_add_u64 v[116:117], s[52:53], 0, v[116:117]
	v_lshl_add_u64 v[116:117], v[116:117], 0, s[2:3]
	v_lshl_add_u64 v[116:117], v[116:117], 0, s[30:31]
	v_cvt_pk_bf16_f32 v118, v124, v125
	v_cvt_pk_bf16_f32 v121, v122, v123
	v_lshl_add_u64 v[116:117], v[116:117], 0, v[136:137]
	v_add_f32_e32 v2, 1.0, v2
	global_store_dwordx4 v[116:117], v[118:121], off
	s_nop 1
	v_rcp_f32_e32 v118, v2
	v_mul_f32_e32 v2, 0xbfb8aa3b, v104
	v_exp_f32_e32 v2, v2
	s_nop 0
	v_add_f32_e32 v2, 1.0, v2
	v_rcp_f32_e32 v120, v2
	v_mul_f32_e32 v2, 0xbfb8aa3b, v113
	v_exp_f32_e32 v2, v2
	s_nop 0
	v_add_f32_e32 v2, 1.0, v2
	v_rcp_f32_e32 v119, v2
	v_mul_f32_e32 v2, 0xbfb8aa3b, v105
	v_exp_f32_e32 v2, v2
	v_pk_mul_f32 v[112:113], v[112:113], v[118:119]
	s_nop 0
	v_pk_mul_f32 v[108:109], v[112:113], v[108:109]
	v_add_f32_e32 v2, 1.0, v2
	v_rcp_f32_e32 v121, v2
	v_mul_f32_e32 v2, 0xbfb8aa3b, v114
	v_exp_f32_e32 v2, v2
	v_pk_mul_f32 v[104:105], v[104:105], v[120:121]
	s_nop 0
	v_pk_mul_f32 v[104:105], v[104:105], v[100:101]
	v_add_f32_e32 v2, 1.0, v2
	v_rcp_f32_e32 v100, v2
	v_mul_f32_e32 v2, 0xbfb8aa3b, v106
	v_exp_f32_e32 v2, v2
	s_nop 0
	v_add_f32_e32 v2, 1.0, v2
	v_rcp_f32_e32 v112, v2
	v_mul_f32_e32 v2, 0xbfb8aa3b, v115
	v_exp_f32_e32 v2, v2
	s_nop 0
	v_add_f32_e32 v2, 1.0, v2
	v_rcp_f32_e32 v101, v2
	v_mul_f32_e32 v2, 0xbfb8aa3b, v107
	v_exp_f32_e32 v2, v2
	v_pk_mul_f32 v[100:101], v[114:115], v[100:101]
	s_nop 0
	v_pk_mul_f32 v[110:111], v[100:101], v[110:111]
	v_add_f32_e32 v2, 1.0, v2
	v_rcp_f32_e32 v113, v2
	v_mul_f32_e32 v2, 0xbfb8aa3b, v96
	v_exp_f32_e32 v2, v2
	v_pk_mul_f32 v[100:101], v[106:107], v[112:113]
	v_or_b32_e32 v112, 16, v138
	v_ashrrev_i32_e32 v113, 31, v112
	v_pk_mul_f32 v[106:107], v[100:101], v[102:103]
	v_cvt_pk_bf16_f32 v102, v104, v105
	v_lshlrev_b64 v[104:105], 11, v[112:113]
	v_lshl_add_u64 v[104:105], s[52:53], 0, v[104:105]
	v_lshl_add_u64 v[104:105], v[104:105], 0, s[2:3]
	v_lshl_add_u64 v[104:105], v[104:105], 0, s[30:31]
	v_cvt_pk_bf16_f32 v100, v108, v109
	v_cvt_pk_bf16_f32 v101, v110, v111
	v_cvt_pk_bf16_f32 v103, v106, v107
	v_lshl_add_u64 v[104:105], v[104:105], 0, v[136:137]
	v_add_f32_e32 v2, 1.0, v2
	global_store_dwordx4 v[104:105], v[100:103], off
	s_nop 1
	v_rcp_f32_e32 v100, v2
	v_mul_f32_e32 v2, 0xbfb8aa3b, v88
	v_exp_f32_e32 v2, v2
	s_nop 0
	v_add_f32_e32 v2, 1.0, v2
	v_rcp_f32_e32 v102, v2
	v_mul_f32_e32 v2, 0xbfb8aa3b, v97
	v_exp_f32_e32 v2, v2
	s_nop 0
	v_add_f32_e32 v2, 1.0, v2
	v_rcp_f32_e32 v101, v2
	v_mul_f32_e32 v2, 0xbfb8aa3b, v89
	v_exp_f32_e32 v2, v2
	v_pk_mul_f32 v[96:97], v[96:97], v[100:101]
	s_nop 0
	v_pk_mul_f32 v[92:93], v[96:97], v[92:93]
	v_add_f32_e32 v2, 1.0, v2
	v_rcp_f32_e32 v103, v2
	v_mul_f32_e32 v2, 0xbfb8aa3b, v98
	v_exp_f32_e32 v2, v2
	v_pk_mul_f32 v[88:89], v[88:89], v[102:103]
	s_nop 0
	v_pk_mul_f32 v[88:89], v[88:89], v[84:85]
	v_add_f32_e32 v2, 1.0, v2
	v_rcp_f32_e32 v84, v2
	v_mul_f32_e32 v2, 0xbfb8aa3b, v90
	v_exp_f32_e32 v2, v2
	s_nop 0
	v_add_f32_e32 v2, 1.0, v2
	v_rcp_f32_e32 v96, v2
	v_mul_f32_e32 v2, 0xbfb8aa3b, v99
	v_exp_f32_e32 v2, v2
	s_nop 0
	v_add_f32_e32 v2, 1.0, v2
	v_rcp_f32_e32 v85, v2
	v_mul_f32_e32 v2, 0xbfb8aa3b, v91
	v_exp_f32_e32 v2, v2
	v_pk_mul_f32 v[84:85], v[98:99], v[84:85]
	s_nop 0
	v_pk_mul_f32 v[94:95], v[84:85], v[94:95]
	v_add_f32_e32 v2, 1.0, v2
	v_rcp_f32_e32 v97, v2
	v_mul_f32_e32 v2, 0xbfb8aa3b, v80
	v_exp_f32_e32 v2, v2
	v_pk_mul_f32 v[84:85], v[90:91], v[96:97]
	v_or_b32_e32 v96, 32, v138
	v_ashrrev_i32_e32 v97, 31, v96
	v_pk_mul_f32 v[90:91], v[84:85], v[86:87]
	v_cvt_pk_bf16_f32 v86, v88, v89
	v_lshlrev_b64 v[88:89], 11, v[96:97]
	v_lshl_add_u64 v[88:89], s[52:53], 0, v[88:89]
	v_lshl_add_u64 v[88:89], v[88:89], 0, s[2:3]
	v_lshl_add_u64 v[88:89], v[88:89], 0, s[30:31]
	v_cvt_pk_bf16_f32 v84, v92, v93
	v_cvt_pk_bf16_f32 v85, v94, v95
	v_cvt_pk_bf16_f32 v87, v90, v91
	v_lshl_add_u64 v[88:89], v[88:89], 0, v[136:137]
	v_add_f32_e32 v2, 1.0, v2
	global_store_dwordx4 v[88:89], v[84:87], off
	s_nop 1
	v_rcp_f32_e32 v84, v2
	v_mul_f32_e32 v2, 0xbfb8aa3b, v72
	v_exp_f32_e32 v2, v2
	s_nop 0
	v_add_f32_e32 v2, 1.0, v2
	v_rcp_f32_e32 v86, v2
	v_mul_f32_e32 v2, 0xbfb8aa3b, v81
	v_exp_f32_e32 v2, v2
	s_nop 0
	v_add_f32_e32 v2, 1.0, v2
	v_rcp_f32_e32 v85, v2
	v_mul_f32_e32 v2, 0xbfb8aa3b, v73
	v_exp_f32_e32 v2, v2
	v_pk_mul_f32 v[80:81], v[80:81], v[84:85]
	s_nop 0
	v_pk_mul_f32 v[76:77], v[80:81], v[76:77]
	v_add_f32_e32 v2, 1.0, v2
	v_rcp_f32_e32 v87, v2
	v_mul_f32_e32 v2, 0xbfb8aa3b, v82
	v_exp_f32_e32 v2, v2
	v_pk_mul_f32 v[72:73], v[72:73], v[86:87]
	s_nop 0
	v_pk_mul_f32 v[72:73], v[72:73], v[68:69]
	v_add_f32_e32 v2, 1.0, v2
	v_rcp_f32_e32 v68, v2
	v_mul_f32_e32 v2, 0xbfb8aa3b, v74
	v_exp_f32_e32 v2, v2
	s_nop 0
	v_add_f32_e32 v2, 1.0, v2
	v_rcp_f32_e32 v80, v2
	v_mul_f32_e32 v2, 0xbfb8aa3b, v83
	v_exp_f32_e32 v2, v2
	s_nop 0
	v_add_f32_e32 v2, 1.0, v2
	v_rcp_f32_e32 v69, v2
	v_mul_f32_e32 v2, 0xbfb8aa3b, v75
	v_exp_f32_e32 v2, v2
	v_pk_mul_f32 v[68:69], v[82:83], v[68:69]
	s_nop 0
	v_pk_mul_f32 v[78:79], v[68:69], v[78:79]
	v_add_f32_e32 v2, 1.0, v2
	v_rcp_f32_e32 v81, v2
	v_mul_f32_e32 v2, 0xbfb8aa3b, v64
	v_exp_f32_e32 v2, v2
	v_pk_mul_f32 v[68:69], v[74:75], v[80:81]
	v_or_b32_e32 v80, 48, v138
	v_ashrrev_i32_e32 v81, 31, v80
	v_pk_mul_f32 v[74:75], v[68:69], v[70:71]
	v_cvt_pk_bf16_f32 v70, v72, v73
	v_lshlrev_b64 v[72:73], 11, v[80:81]
	v_lshl_add_u64 v[72:73], s[52:53], 0, v[72:73]
	v_lshl_add_u64 v[72:73], v[72:73], 0, s[2:3]
	v_lshl_add_u64 v[72:73], v[72:73], 0, s[30:31]
	v_cvt_pk_bf16_f32 v68, v76, v77
	v_cvt_pk_bf16_f32 v69, v78, v79
	v_cvt_pk_bf16_f32 v71, v74, v75
	v_lshl_add_u64 v[72:73], v[72:73], 0, v[136:137]
	v_add_f32_e32 v2, 1.0, v2
	global_store_dwordx4 v[72:73], v[68:71], off
	v_mov_b32_e32 v138, v156
	s_mov_b64 s[2:3], s[40:41]
	v_rcp_f32_e32 v68, v2
	v_mul_f32_e32 v2, 0xbfb8aa3b, v56
	v_exp_f32_e32 v2, v2
	s_nop 0
	v_add_f32_e32 v2, 1.0, v2
	v_rcp_f32_e32 v70, v2
	v_mul_f32_e32 v2, 0xbfb8aa3b, v65
	v_exp_f32_e32 v2, v2
	s_nop 0
	v_add_f32_e32 v2, 1.0, v2
	v_rcp_f32_e32 v69, v2
	v_mul_f32_e32 v2, 0xbfb8aa3b, v57
	v_exp_f32_e32 v2, v2
	v_pk_mul_f32 v[64:65], v[64:65], v[68:69]
	s_nop 0
	v_pk_mul_f32 v[60:61], v[64:65], v[60:61]
	v_add_f32_e32 v2, 1.0, v2
	v_rcp_f32_e32 v71, v2
	v_mul_f32_e32 v2, 0xbfb8aa3b, v66
	v_exp_f32_e32 v2, v2
	v_pk_mul_f32 v[56:57], v[56:57], v[70:71]
	s_nop 0
	v_pk_mul_f32 v[56:57], v[56:57], v[52:53]
	v_add_f32_e32 v2, 1.0, v2
	v_rcp_f32_e32 v52, v2
	v_mul_f32_e32 v2, 0xbfb8aa3b, v58
	v_exp_f32_e32 v2, v2
	s_nop 0
	v_add_f32_e32 v2, 1.0, v2
	v_rcp_f32_e32 v64, v2
	v_mul_f32_e32 v2, 0xbfb8aa3b, v67
	v_exp_f32_e32 v2, v2
	s_nop 0
	v_add_f32_e32 v2, 1.0, v2
	v_rcp_f32_e32 v53, v2
	v_mul_f32_e32 v2, 0xbfb8aa3b, v59
	v_exp_f32_e32 v2, v2
	v_pk_mul_f32 v[52:53], v[66:67], v[52:53]
	s_nop 0
	v_pk_mul_f32 v[62:63], v[52:53], v[62:63]
	v_add_f32_e32 v2, 1.0, v2
	v_rcp_f32_e32 v65, v2
	v_mul_f32_e32 v2, 0xbfb8aa3b, v48
	v_exp_f32_e32 v2, v2
	v_pk_mul_f32 v[52:53], v[58:59], v[64:65]
	s_nop 0
	v_pk_mul_f32 v[58:59], v[52:53], v[54:55]
	v_cvt_pk_bf16_f32 v54, v56, v57
	v_add_co_u32_e32 v56, vcc, s0, v116
	v_cvt_pk_bf16_f32 v52, v60, v61
	v_cvt_pk_bf16_f32 v53, v62, v63
	v_cvt_pk_bf16_f32 v55, v58, v59
	v_addc_co_u32_e32 v57, vcc, 0, v117, vcc
	v_add_f32_e32 v2, 1.0, v2
	global_store_dwordx4 v[56:57], v[52:55], off
	s_mov_b32 s0, 0x48000
	s_nop 0
	v_rcp_f32_e32 v52, v2
	v_mul_f32_e32 v2, 0xbfb8aa3b, v40
	v_exp_f32_e32 v2, v2
	s_nop 0
	v_add_f32_e32 v2, 1.0, v2
	v_rcp_f32_e32 v54, v2
	v_mul_f32_e32 v2, 0xbfb8aa3b, v49
	v_exp_f32_e32 v2, v2
	s_nop 0
	v_add_f32_e32 v2, 1.0, v2
	v_rcp_f32_e32 v53, v2
	v_mul_f32_e32 v2, 0xbfb8aa3b, v41
	v_exp_f32_e32 v2, v2
	v_pk_mul_f32 v[48:49], v[48:49], v[52:53]
	s_nop 0
	v_pk_mul_f32 v[44:45], v[48:49], v[44:45]
	v_add_f32_e32 v2, 1.0, v2
	v_rcp_f32_e32 v55, v2
	v_mul_f32_e32 v2, 0xbfb8aa3b, v50
	v_exp_f32_e32 v2, v2
	v_pk_mul_f32 v[40:41], v[40:41], v[54:55]
	s_nop 0
	v_pk_mul_f32 v[40:41], v[40:41], v[36:37]
	v_add_f32_e32 v2, 1.0, v2
	v_rcp_f32_e32 v36, v2
	v_mul_f32_e32 v2, 0xbfb8aa3b, v42
	v_exp_f32_e32 v2, v2
	s_nop 0
	v_add_f32_e32 v2, 1.0, v2
	v_rcp_f32_e32 v48, v2
	v_mul_f32_e32 v2, 0xbfb8aa3b, v51
	v_exp_f32_e32 v2, v2
	s_nop 0
	v_add_f32_e32 v2, 1.0, v2
	v_rcp_f32_e32 v37, v2
	v_mul_f32_e32 v2, 0xbfb8aa3b, v43
	v_exp_f32_e32 v2, v2
	v_pk_mul_f32 v[36:37], v[50:51], v[36:37]
	s_nop 0
	v_pk_mul_f32 v[46:47], v[36:37], v[46:47]
	v_add_f32_e32 v2, 1.0, v2
	v_rcp_f32_e32 v49, v2
	v_mul_f32_e32 v2, 0xbfb8aa3b, v24
	v_exp_f32_e32 v2, v2
	v_pk_mul_f32 v[36:37], v[42:43], v[48:49]
	s_nop 0
	v_pk_mul_f32 v[42:43], v[36:37], v[38:39]
	v_cvt_pk_bf16_f32 v38, v40, v41
	v_add_co_u32_e32 v40, vcc, s0, v116
	v_cvt_pk_bf16_f32 v36, v44, v45
	v_cvt_pk_bf16_f32 v37, v46, v47
	v_cvt_pk_bf16_f32 v39, v42, v43
	v_addc_co_u32_e32 v41, vcc, 0, v117, vcc
	v_add_f32_e32 v2, 1.0, v2
	global_store_dwordx4 v[40:41], v[36:39], off
	s_mov_b32 s0, 0x50000
	s_nop 0
	v_rcp_f32_e32 v36, v2
	v_mul_f32_e32 v2, 0xbfb8aa3b, v20
	v_exp_f32_e32 v2, v2
	s_nop 0
	v_add_f32_e32 v2, 1.0, v2
	v_rcp_f32_e32 v38, v2
	v_mul_f32_e32 v2, 0xbfb8aa3b, v25
	v_exp_f32_e32 v2, v2
	s_nop 0
	v_add_f32_e32 v2, 1.0, v2
	v_rcp_f32_e32 v37, v2
	v_mul_f32_e32 v2, 0xbfb8aa3b, v21
	v_exp_f32_e32 v2, v2
	v_pk_mul_f32 v[24:25], v[24:25], v[36:37]
	s_nop 0
	v_pk_mul_f32 v[24:25], v[24:25], v[32:33]
	v_add_f32_e32 v2, 1.0, v2
	v_rcp_f32_e32 v39, v2
	v_mul_f32_e32 v2, 0xbfb8aa3b, v26
	v_exp_f32_e32 v2, v2
	v_pk_mul_f32 v[20:21], v[20:21], v[38:39]
	s_nop 0
	v_pk_mul_f32 v[28:29], v[20:21], v[28:29]
	v_add_f32_e32 v2, 1.0, v2
	v_rcp_f32_e32 v20, v2
	v_mul_f32_e32 v2, 0xbfb8aa3b, v22
	v_exp_f32_e32 v2, v2
	s_nop 0
	v_add_f32_e32 v2, 1.0, v2
	v_rcp_f32_e32 v32, v2
	v_mul_f32_e32 v2, 0xbfb8aa3b, v27
	v_exp_f32_e32 v2, v2
	s_nop 0
	v_add_f32_e32 v2, 1.0, v2
	v_rcp_f32_e32 v21, v2
	v_mul_f32_e32 v2, 0xbfb8aa3b, v23
	v_exp_f32_e32 v2, v2
	v_pk_mul_f32 v[20:21], v[26:27], v[20:21]
	s_nop 0
	v_pk_mul_f32 v[26:27], v[20:21], v[34:35]
	v_add_f32_e32 v2, 1.0, v2
	v_rcp_f32_e32 v33, v2
	v_mul_f32_e32 v2, 0xbfb8aa3b, v8
	v_exp_f32_e32 v2, v2
	v_pk_mul_f32 v[20:21], v[22:23], v[32:33]
	s_nop 0
	v_pk_mul_f32 v[30:31], v[20:21], v[30:31]
	v_cvt_pk_bf16_f32 v20, v24, v25
	v_add_co_u32_e32 v24, vcc, s0, v116
	v_cvt_pk_bf16_f32 v21, v26, v27
	v_cvt_pk_bf16_f32 v22, v28, v29
	v_cvt_pk_bf16_f32 v23, v30, v31
	v_addc_co_u32_e32 v25, vcc, 0, v117, vcc
	v_add_f32_e32 v2, 1.0, v2
	global_store_dwordx4 v[24:25], v[20:23], off
	s_nop 1
	v_rcp_f32_e32 v20, v2
	v_mul_f32_e32 v2, 0xbfb8aa3b, v4
	v_exp_f32_e32 v2, v2
	s_nop 0
	v_add_f32_e32 v2, 1.0, v2
	v_rcp_f32_e32 v22, v2
	v_mul_f32_e32 v2, 0xbfb8aa3b, v9
	v_exp_f32_e32 v2, v2
	s_nop 0
	v_add_f32_e32 v2, 1.0, v2
	v_rcp_f32_e32 v21, v2
	v_mul_f32_e32 v2, 0xbfb8aa3b, v5
	v_exp_f32_e32 v2, v2
	v_pk_mul_f32 v[8:9], v[8:9], v[20:21]
	s_nop 0
	v_pk_mul_f32 v[8:9], v[8:9], v[16:17]
	v_add_f32_e32 v2, 1.0, v2
	v_rcp_f32_e32 v23, v2
	v_mul_f32_e32 v2, 0xbfb8aa3b, v10
	v_exp_f32_e32 v2, v2
	v_pk_mul_f32 v[4:5], v[4:5], v[22:23]
	s_nop 0
	v_pk_mul_f32 v[12:13], v[4:5], v[12:13]
	v_add_f32_e32 v2, 1.0, v2
	v_rcp_f32_e32 v4, v2
	v_mul_f32_e32 v2, 0xbfb8aa3b, v6
	v_exp_f32_e32 v2, v2
	s_nop 0
	v_add_f32_e32 v2, 1.0, v2
	v_rcp_f32_e32 v16, v2
	v_mul_f32_e32 v2, 0xbfb8aa3b, v11
	v_exp_f32_e32 v2, v2
	s_nop 0
	v_add_f32_e32 v2, 1.0, v2
	v_rcp_f32_e32 v5, v2
	v_mul_f32_e32 v2, 0xbfb8aa3b, v7
	v_exp_f32_e32 v2, v2
	v_pk_mul_f32 v[4:5], v[10:11], v[4:5]
	s_nop 0
	v_pk_mul_f32 v[10:11], v[4:5], v[18:19]
	v_add_f32_e32 v2, 1.0, v2
	v_rcp_f32_e32 v17, v2
	s_nop 0
	v_pk_mul_f32 v[4:5], v[6:7], v[16:17]
	s_nop 0
	v_pk_mul_f32 v[14:15], v[4:5], v[14:15]
	v_cvt_pk_bf16_f32 v4, v8, v9
	v_add_co_u32_e32 v8, vcc, 0x58000, v116
	v_cvt_pk_bf16_f32 v5, v10, v11
	s_nop 0
	v_addc_co_u32_e32 v9, vcc, 0, v117, vcc
	v_cvt_pk_bf16_f32 v6, v12, v13
	v_cvt_pk_bf16_f32 v7, v14, v15
	s_and_b64 vcc, exec, s[38:39]
	global_store_dwordx4 v[8:9], v[4:7], off
	s_cbranch_vccz .LBB0_2078
	s_waitcnt vmcnt(0)
	s_cmpk_gt_u32 s22, 0xff
	s_movk_i32 s36, 0x1ff
	s_cbranch_scc1 .LBB0_2091
	s_barrier

.LBB0_2280:
	s_add_u32 s36, s46, s42
	s_addc_u32 s54, s47, s43
	s_add_u32 s36, s36, 0x2fc1b100
	s_addc_u32 s56, s54, 0
	s_add_u32 s70, s0, s42
	s_addc_u32 s71, s1, s43
	s_add_i32 s72, 0, 0x10000
	v_add_u32_e32 v137, s72, v157
	ds_read_b128 v[162:165], v137
	ds_read_b128 v[166:169], v137 offset:1024
	ds_read_b128 v[170:173], v137 offset:2048
	ds_read_b128 v[174:177], v137 offset:3072
	s_cmpk_eq_i32 s42, 0x700
	s_cselect_b64 vcc, -1, 0
	s_and_b64 s[54:55], vcc, exec
	v_cndmask_b32_e32 v2, v138, v141, vcc
	s_cselect_b32 s57, s3, s56
	s_cselect_b32 s56, s2, s36
	v_cndmask_b32_e32 v150, v140, v158, vcc
	v_cndmask_b32_e32 v137, v142, v159, vcc
	v_cndmask_b32_e32 v143, v144, v160, vcc
	s_cselect_b32 s55, s41, s71
	s_cselect_b32 s54, s40, s70
	v_lshl_add_u64 v[178:179], v[148:149], 0, s[42:43]
	s_add_i32 m0, s59, 0xc000
	ds_read_b128 v[182:185], v139
	ds_read_b128 v[186:189], v139 offset:1024
	ds_read_b128 v[190:193], v139 offset:2048
	ds_read_b128 v[194:197], v139 offset:3072
	ds_read_b128 v[198:201], v139 offset:4096
	ds_read_b128 v[202:205], v139 offset:5120
	ds_read_b128 v[214:217], v139 offset:6144
	ds_read_b128 v[218:221], v139 offset:7168
	global_load_lds_dwordx4 v[178:179], off
	v_lshl_add_u64 v[178:179], v[146:147], 0, s[42:43]
	s_add_i32 m0, s59, 0xe000
	s_nop 0
	global_load_lds_dwordx4 v[178:179], off
	s_waitcnt lgkmcnt(8)
	s_barrier
	s_waitcnt lgkmcnt(0)
	s_waitcnt lgkmcnt(0)
	v_mfma_f32_16x16x32_bf16 v[128:131], v[162:165], v[182:185], v[128:131]
	v_mfma_f32_16x16x32_bf16 v[124:127], v[170:173], v[182:185], v[124:127]
	v_mfma_f32_16x16x32_bf16 v[112:115], v[162:165], v[190:193], v[112:115]
	v_mfma_f32_16x16x32_bf16 v[108:111], v[170:173], v[190:193], v[108:111]
	v_mfma_f32_16x16x32_bf16 v[96:99], v[162:165], v[198:201], v[96:99]
	v_mfma_f32_16x16x32_bf16 v[92:95], v[170:173], v[198:201], v[92:95]
	v_mfma_f32_16x16x32_bf16 v[84:87], v[162:165], v[214:217], v[84:87]
	v_mfma_f32_16x16x32_bf16 v[80:83], v[170:173], v[214:217], v[80:83]
	v_mfma_f32_16x16x32_bf16 v[128:131], v[166:169], v[186:189], v[128:131]
	v_mfma_f32_16x16x32_bf16 v[124:127], v[174:177], v[186:189], v[124:127]
	v_mfma_f32_16x16x32_bf16 v[112:115], v[166:169], v[194:197], v[112:115]
	v_mfma_f32_16x16x32_bf16 v[108:111], v[174:177], v[194:197], v[108:111]
	v_mfma_f32_16x16x32_bf16 v[96:99], v[166:169], v[202:205], v[96:99]
	v_mfma_f32_16x16x32_bf16 v[92:95], v[174:177], v[202:205], v[92:95]
	v_mfma_f32_16x16x32_bf16 v[84:87], v[166:169], v[218:221], v[84:87]
	v_mfma_f32_16x16x32_bf16 v[80:83], v[174:177], v[218:221], v[80:83]
	s_barrier
	s_add_i32 s36, 0, 0x14000
	s_add_i32 s70, s72, s58
	v_add_u32_e32 v145, s36, v157
	v_lshl_add_u64 v[178:179], s[54:55], 0, v[132:133]
	s_mov_b32 m0, s70
	ds_read_b128 v[222:225], v145
	ds_read_b128 v[226:229], v145 offset:1024
	ds_read_b128 v[230:233], v145 offset:2048
	ds_read_b128 v[234:237], v145 offset:3072
	global_load_lds_dwordx4 v[178:179], off
	v_lshl_add_u64 v[206:207], s[54:55], 0, v[134:135]
	s_add_i32 m0, s70, 0x2000
	s_nop 0
	global_load_lds_dwordx4 v[206:207], off
	s_barrier
	s_waitcnt lgkmcnt(0)
	s_waitcnt lgkmcnt(0)
	v_mfma_f32_16x16x32_bf16 v[120:123], v[222:225], v[182:185], v[120:123]
	v_mfma_f32_16x16x32_bf16 v[116:119], v[230:233], v[182:185], v[116:119]
	v_mfma_f32_16x16x32_bf16 v[104:107], v[222:225], v[190:193], v[104:107]
	v_mfma_f32_16x16x32_bf16 v[100:103], v[230:233], v[190:193], v[100:103]
	v_mfma_f32_16x16x32_bf16 v[88:91], v[222:225], v[198:201], v[88:91]
	v_mfma_f32_16x16x32_bf16 v[76:79], v[230:233], v[198:201], v[76:79]
	v_mfma_f32_16x16x32_bf16 v[72:75], v[222:225], v[214:217], v[72:75]
	v_mfma_f32_16x16x32_bf16 v[68:71], v[230:233], v[214:217], v[68:71]
	v_mfma_f32_16x16x32_bf16 v[120:123], v[226:229], v[186:189], v[120:123]
	v_mfma_f32_16x16x32_bf16 v[116:119], v[234:237], v[186:189], v[116:119]
	v_mfma_f32_16x16x32_bf16 v[104:107], v[226:229], v[194:197], v[104:107]
	v_mfma_f32_16x16x32_bf16 v[100:103], v[234:237], v[194:197], v[100:103]
	v_mfma_f32_16x16x32_bf16 v[88:91], v[226:229], v[202:205], v[88:91]
	v_mfma_f32_16x16x32_bf16 v[76:79], v[234:237], v[202:205], v[76:79]
	v_mfma_f32_16x16x32_bf16 v[72:75], v[226:229], v[218:221], v[72:75]
	v_mfma_f32_16x16x32_bf16 v[68:71], v[234:237], v[218:221], v[68:71]
	s_mov_b32 m0, s59
	s_barrier
	ds_read_b128 v[182:185], v139 offset:16384
	ds_read_b128 v[186:189], v139 offset:17408
	ds_read_b128 v[190:193], v139 offset:18432
	ds_read_b128 v[194:197], v139 offset:19456
	ds_read_b128 v[198:201], v139 offset:20480
	ds_read_b128 v[202:205], v139 offset:21504
	ds_read_b128 v[214:217], v139 offset:22528
	ds_read_b128 v[218:221], v139 offset:23552
	global_load_lds_dwordx4 v2, s[56:57]
	s_mov_b32 m0, s60
	v_mov_b32_e32 v151, v3
	global_load_lds_dwordx4 v150, s[56:57]
	s_barrier
	s_waitcnt lgkmcnt(0)
	v_lshl_add_u64 v[208:209], s[56:57], 0, v[2:3]
	v_lshl_add_u64 v[150:151], s[56:57], 0, v[150:151]
	s_waitcnt lgkmcnt(0)
	v_mfma_f32_16x16x32_bf16 v[64:67], v[162:165], v[182:185], v[64:67]
	v_mfma_f32_16x16x32_bf16 v[60:63], v[170:173], v[182:185], v[60:63]
	v_mfma_f32_16x16x32_bf16 v[48:51], v[162:165], v[190:193], v[48:51]
	v_mfma_f32_16x16x32_bf16 v[40:43], v[170:173], v[190:193], v[40:43]
	v_mfma_f32_16x16x32_bf16 v[24:27], v[162:165], v[198:201], v[24:27]
	v_mfma_f32_16x16x32_bf16 v[16:19], v[170:173], v[198:201], v[16:19]
	v_mfma_f32_16x16x32_bf16 v[8:11], v[162:165], v[214:217], v[8:11]
	v_mfma_f32_16x16x32_bf16 v[4:7], v[170:173], v[214:217], v[4:7]
	v_mfma_f32_16x16x32_bf16 v[64:67], v[166:169], v[186:189], v[64:67]
	v_mfma_f32_16x16x32_bf16 v[60:63], v[174:177], v[186:189], v[60:63]
	v_mfma_f32_16x16x32_bf16 v[48:51], v[166:169], v[194:197], v[48:51]
	v_mfma_f32_16x16x32_bf16 v[40:43], v[174:177], v[194:197], v[40:43]
	v_mfma_f32_16x16x32_bf16 v[24:27], v[166:169], v[202:205], v[24:27]
	v_mfma_f32_16x16x32_bf16 v[16:19], v[174:177], v[202:205], v[16:19]
	v_mfma_f32_16x16x32_bf16 v[8:11], v[166:169], v[218:221], v[8:11]
	v_mfma_f32_16x16x32_bf16 v[4:7], v[174:177], v[218:221], v[4:7]
	s_barrier
	s_add_u32 s70, s54, 0x40000
	s_addc_u32 s71, s55, 0
	s_add_i32 s36, s36, s58
	v_lshl_add_u64 v[162:163], s[70:71], 0, v[132:133]
	s_mov_b32 m0, s36
	s_nop 0
	global_load_lds_dwordx4 v[162:163], off
	v_lshl_add_u64 v[162:163], s[70:71], 0, v[134:135]
	s_add_i32 m0, s36, 0x2000
	s_nop 0
	global_load_lds_dwordx4 v[162:163], off
	s_waitcnt vmcnt(6)
	s_barrier
	v_mfma_f32_16x16x32_bf16 v[44:47], v[222:225], v[182:185], v[44:47]
	v_mfma_f32_16x16x32_bf16 v[36:39], v[230:233], v[182:185], v[36:39]
	v_mfma_f32_16x16x32_bf16 v[20:23], v[222:225], v[190:193], v[20:23]
	v_mfma_f32_16x16x32_bf16 v[12:15], v[230:233], v[190:193], v[12:15]
	v_mfma_f32_16x16x32_bf16 v[52:55], v[222:225], v[198:201], v[52:55]
	v_mfma_f32_16x16x32_bf16 v[56:59], v[230:233], v[198:201], v[56:59]
	v_mfma_f32_16x16x32_bf16 v[28:31], v[222:225], v[214:217], v[28:31]
	v_mfma_f32_16x16x32_bf16 v[32:35], v[230:233], v[214:217], v[32:35]
	v_mfma_f32_16x16x32_bf16 v[44:47], v[226:229], v[186:189], v[44:47]
	v_mfma_f32_16x16x32_bf16 v[36:39], v[234:237], v[186:189], v[36:39]
	v_mfma_f32_16x16x32_bf16 v[20:23], v[226:229], v[194:197], v[20:23]
	v_mfma_f32_16x16x32_bf16 v[12:15], v[234:237], v[194:197], v[12:15]
	v_mfma_f32_16x16x32_bf16 v[52:55], v[226:229], v[202:205], v[52:55]
	v_mfma_f32_16x16x32_bf16 v[56:59], v[234:237], v[202:205], v[56:59]
	v_mfma_f32_16x16x32_bf16 v[28:31], v[226:229], v[218:221], v[28:31]
	v_mfma_f32_16x16x32_bf16 v[32:35], v[234:237], v[218:221], v[32:35]
	s_add_i32 s36, 0, 0x18000
	v_add_u32_e32 v2, s36, v157
	s_barrier
	ds_read_b128 v[162:165], v2
	ds_read_b128 v[166:169], v2 offset:1024
	ds_read_b128 v[170:173], v2 offset:2048
	ds_read_b128 v[174:177], v2 offset:3072
	s_mov_b32 m0, s61
	ds_read_b128 v[182:185], v139 offset:32768
	ds_read_b128 v[186:189], v139 offset:33792
	ds_read_b128 v[190:193], v139 offset:34816
	ds_read_b128 v[194:197], v139 offset:35840
	ds_read_b128 v[198:201], v139 offset:36864
	ds_read_b128 v[202:205], v139 offset:37888
	ds_read_b128 v[214:217], v139 offset:38912
	ds_read_b128 v[218:221], v139 offset:39936
	global_load_lds_dwordx4 v137, s[56:57]
	s_mov_b32 m0, s62
	s_nop 0
	global_load_lds_dwordx4 v143, s[56:57]
	s_waitcnt lgkmcnt(8)
	s_barrier
	s_waitcnt lgkmcnt(0)
	s_waitcnt lgkmcnt(0)
	v_mfma_f32_16x16x32_bf16 v[128:131], v[162:165], v[182:185], v[128:131]
	v_mfma_f32_16x16x32_bf16 v[124:127], v[170:173], v[182:185], v[124:127]
	v_mfma_f32_16x16x32_bf16 v[112:115], v[162:165], v[190:193], v[112:115]
	v_mfma_f32_16x16x32_bf16 v[108:111], v[170:173], v[190:193], v[108:111]
	v_mfma_f32_16x16x32_bf16 v[96:99], v[162:165], v[198:201], v[96:99]
	v_mfma_f32_16x16x32_bf16 v[92:95], v[170:173], v[198:201], v[92:95]
	v_mfma_f32_16x16x32_bf16 v[84:87], v[162:165], v[214:217], v[84:87]
	v_mfma_f32_16x16x32_bf16 v[80:83], v[170:173], v[214:217], v[80:83]
	v_mfma_f32_16x16x32_bf16 v[128:131], v[166:169], v[186:189], v[128:131]
	v_mfma_f32_16x16x32_bf16 v[124:127], v[174:177], v[186:189], v[124:127]
	v_mfma_f32_16x16x32_bf16 v[112:115], v[166:169], v[194:197], v[112:115]
	v_mfma_f32_16x16x32_bf16 v[108:111], v[174:177], v[194:197], v[108:111]
	v_mfma_f32_16x16x32_bf16 v[96:99], v[166:169], v[202:205], v[96:99]
	v_mfma_f32_16x16x32_bf16 v[92:95], v[174:177], v[202:205], v[92:95]
	v_mfma_f32_16x16x32_bf16 v[84:87], v[166:169], v[218:221], v[84:87]
	v_mfma_f32_16x16x32_bf16 v[80:83], v[174:177], v[218:221], v[80:83]
	s_barrier
	s_add_i32 s56, 0, 0x1c000
	s_add_i32 s36, s36, s58
	v_add_u32_e32 v2, s56, v157
	v_lshl_add_u64 v[178:179], v[178:179], 0, s[8:9]
	s_mov_b32 m0, s36
	ds_read_b128 v[222:225], v2
	ds_read_b128 v[226:229], v2 offset:1024
	ds_read_b128 v[230:233], v2 offset:2048
	ds_read_b128 v[234:237], v2 offset:3072
	global_load_lds_dwordx4 v[178:179], off
	v_lshl_add_u64 v[178:179], v[206:207], 0, s[8:9]
	s_add_i32 m0, s36, 0x2000
	s_nop 0
	global_load_lds_dwordx4 v[178:179], off
	s_barrier
	s_waitcnt lgkmcnt(0)
	s_waitcnt lgkmcnt(0)
	v_mfma_f32_16x16x32_bf16 v[120:123], v[222:225], v[182:185], v[120:123]
	v_mfma_f32_16x16x32_bf16 v[116:119], v[230:233], v[182:185], v[116:119]
	v_mfma_f32_16x16x32_bf16 v[104:107], v[222:225], v[190:193], v[104:107]
	v_mfma_f32_16x16x32_bf16 v[100:103], v[230:233], v[190:193], v[100:103]
	v_mfma_f32_16x16x32_bf16 v[88:91], v[222:225], v[198:201], v[88:91]
	v_mfma_f32_16x16x32_bf16 v[76:79], v[230:233], v[198:201], v[76:79]
	v_mfma_f32_16x16x32_bf16 v[72:75], v[222:225], v[214:217], v[72:75]
	v_mfma_f32_16x16x32_bf16 v[68:71], v[230:233], v[214:217], v[68:71]
	v_mfma_f32_16x16x32_bf16 v[120:123], v[226:229], v[186:189], v[120:123]
	v_mfma_f32_16x16x32_bf16 v[116:119], v[234:237], v[186:189], v[116:119]
	v_mfma_f32_16x16x32_bf16 v[104:107], v[226:229], v[194:197], v[104:107]
	v_mfma_f32_16x16x32_bf16 v[100:103], v[234:237], v[194:197], v[100:103]
	v_mfma_f32_16x16x32_bf16 v[88:91], v[226:229], v[202:205], v[88:91]
	v_mfma_f32_16x16x32_bf16 v[76:79], v[234:237], v[202:205], v[76:79]
	v_mfma_f32_16x16x32_bf16 v[72:75], v[226:229], v[218:221], v[72:75]
	v_mfma_f32_16x16x32_bf16 v[68:71], v[234:237], v[218:221], v[68:71]
	s_mov_b32 m0, s63
	v_lshl_add_u64 v[178:179], v[208:209], 0, s[8:9]
	s_barrier
	ds_read_b128 v[182:185], v139 offset:49152
	ds_read_b128 v[186:189], v139 offset:50176
	ds_read_b128 v[190:193], v139 offset:51200
	ds_read_b128 v[194:197], v139 offset:52224
	ds_read_b128 v[198:201], v139 offset:53248
	ds_read_b128 v[202:205], v139 offset:54272
	ds_read_b128 v[214:217], v139 offset:55296
	ds_read_b128 v[218:221], v139 offset:56320
	global_load_lds_dwordx4 v[178:179], off
	v_lshl_add_u64 v[150:151], v[150:151], 0, s[8:9]
	s_mov_b32 m0, s64
	s_nop 0
	global_load_lds_dwordx4 v[150:151], off
	s_barrier
	s_waitcnt lgkmcnt(0)
	s_waitcnt lgkmcnt(0)
	v_mfma_f32_16x16x32_bf16 v[64:67], v[162:165], v[182:185], v[64:67]
	v_mfma_f32_16x16x32_bf16 v[60:63], v[170:173], v[182:185], v[60:63]
	v_mfma_f32_16x16x32_bf16 v[48:51], v[162:165], v[190:193], v[48:51]
	v_mfma_f32_16x16x32_bf16 v[40:43], v[170:173], v[190:193], v[40:43]
	v_mfma_f32_16x16x32_bf16 v[24:27], v[162:165], v[198:201], v[24:27]
	v_mfma_f32_16x16x32_bf16 v[16:19], v[170:173], v[198:201], v[16:19]
	v_mfma_f32_16x16x32_bf16 v[8:11], v[162:165], v[214:217], v[8:11]
	v_mfma_f32_16x16x32_bf16 v[4:7], v[170:173], v[214:217], v[4:7]
	v_mfma_f32_16x16x32_bf16 v[64:67], v[166:169], v[186:189], v[64:67]
	v_mfma_f32_16x16x32_bf16 v[60:63], v[174:177], v[186:189], v[60:63]
	v_mfma_f32_16x16x32_bf16 v[48:51], v[166:169], v[194:197], v[48:51]
	v_mfma_f32_16x16x32_bf16 v[40:43], v[174:177], v[194:197], v[40:43]
	v_mfma_f32_16x16x32_bf16 v[24:27], v[166:169], v[202:205], v[24:27]
	v_mfma_f32_16x16x32_bf16 v[16:19], v[174:177], v[202:205], v[16:19]
	v_mfma_f32_16x16x32_bf16 v[8:11], v[166:169], v[218:221], v[8:11]
	v_mfma_f32_16x16x32_bf16 v[4:7], v[174:177], v[218:221], v[4:7]
	s_barrier
	s_add_u32 s54, s54, 0x40080
	s_addc_u32 s55, s55, 0
	s_add_i32 s36, s56, s58
	v_lshl_add_u64 v[150:151], s[54:55], 0, v[132:133]
	s_mov_b32 m0, s36
	s_nop 0
	global_load_lds_dwordx4 v[150:151], off
	v_lshl_add_u64 v[150:151], s[54:55], 0, v[134:135]
	s_add_i32 m0, s36, 0x2000
	s_nop 0
	global_load_lds_dwordx4 v[150:151], off
	s_waitcnt vmcnt(6)
	s_barrier
	v_mfma_f32_16x16x32_bf16 v[44:47], v[222:225], v[182:185], v[44:47]
	v_mfma_f32_16x16x32_bf16 v[36:39], v[230:233], v[182:185], v[36:39]
	v_mfma_f32_16x16x32_bf16 v[20:23], v[222:225], v[190:193], v[20:23]
	v_mfma_f32_16x16x32_bf16 v[12:15], v[230:233], v[190:193], v[12:15]
	v_mfma_f32_16x16x32_bf16 v[52:55], v[222:225], v[198:201], v[52:55]
	v_mfma_f32_16x16x32_bf16 v[56:59], v[230:233], v[198:201], v[56:59]
	v_mfma_f32_16x16x32_bf16 v[28:31], v[222:225], v[214:217], v[28:31]
	v_mfma_f32_16x16x32_bf16 v[32:35], v[230:233], v[214:217], v[32:35]
	v_mfma_f32_16x16x32_bf16 v[44:47], v[226:229], v[186:189], v[44:47]
	v_mfma_f32_16x16x32_bf16 v[36:39], v[234:237], v[186:189], v[36:39]
	v_mfma_f32_16x16x32_bf16 v[20:23], v[226:229], v[194:197], v[20:23]
	v_mfma_f32_16x16x32_bf16 v[12:15], v[234:237], v[194:197], v[12:15]
	v_mfma_f32_16x16x32_bf16 v[52:55], v[226:229], v[202:205], v[52:55]
	v_mfma_f32_16x16x32_bf16 v[56:59], v[234:237], v[202:205], v[56:59]
	v_mfma_f32_16x16x32_bf16 v[28:31], v[226:229], v[218:221], v[28:31]
	v_mfma_f32_16x16x32_bf16 v[32:35], v[234:237], v[218:221], v[32:35]
	s_add_i32 s53, s53, 2
	s_add_u32 s42, s42, 0x100
	s_addc_u32 s43, s43, 0
	s_cmp_gt_u32 s53, 13
	s_barrier
	s_cbranch_scc0 .LBB0_2280
	v_lshl_add_u32 v162, s68, 8, v156
	v_ashrrev_i32_e32 v163, 31, v162
	v_lshl_add_u64 v[164:165], v[162:163], 2, s[48:49]
	global_load_dword v166, v[164:165], off
	v_or_b32_e32 v168, 16, v162
	v_ashrrev_i32_e32 v169, 31, v168
	v_lshl_add_u64 v[142:143], v[168:169], 2, s[48:49]
	global_load_dword v170, v[142:143], off
	v_or_b32_e32 v150, 32, v162
	v_ashrrev_i32_e32 v151, 31, v150
	v_lshl_add_u64 v[142:143], v[150:151], 2, s[48:49]
	global_load_dword v148, v[142:143], off
	v_or_b32_e32 v146, 48, v162
	v_ashrrev_i32_e32 v147, 31, v146
	v_lshl_add_u64 v[142:143], v[146:147], 2, s[48:49]
	global_load_dword v144, v[142:143], off
	s_nop 0
	global_load_dword v142, v[164:165], off offset:512
	global_load_dword v140, v[164:165], off offset:576
	global_load_dword v138, v[164:165], off offset:640
	global_load_dword v2, v[164:165], off offset:704
	s_lshl_b32 s0, s69, 8
	s_ashr_i32 s1, s0, 31
	v_lshlrev_b64 v[162:163], 11, v[162:163]
	s_lshl_b64 s[42:43], s[0:1], 1
	v_mov_b32_e32 v137, v3
	s_mov_b64 s[0:1], 0x40000
	s_mov_b32 s69, s52
	s_mov_b32 s68, s67
	s_mov_b64 s[54:55], s[40:41]
	s_movk_i32 s36, 0x1ff
	s_waitcnt vmcnt(0)
	v_pk_mul_f32 v[128:129], v[128:129], v[166:167] op_sel_hi:[1,0]
	v_pk_mul_f32 v[124:125], v[124:125], v[166:167] op_sel_hi:[1,0]
	v_pk_mul_f32 v[164:165], v[126:127], v[166:167] op_sel_hi:[1,0]
	v_cvt_pk_bf16_f32 v126, v128, v129
	v_cvt_pk_bf16_f32 v128, v124, v125
	v_lshl_add_u64 v[124:125], s[34:35], 0, v[162:163]
	v_lshl_add_u64 v[124:125], v[124:125], 0, s[42:43]
	v_pk_mul_f32 v[130:131], v[130:131], v[166:167] op_sel_hi:[1,0]
	v_lshl_add_u64 v[124:125], v[124:125], 0, s[30:31]
	v_cvt_pk_bf16_f32 v127, v130, v131
	v_cvt_pk_bf16_f32 v129, v164, v165
	v_lshl_add_u64 v[124:125], v[124:125], 0, v[136:137]
	global_store_dwordx4 v[124:125], v[126:129], off
	v_pk_mul_f32 v[122:123], v[122:123], v[166:167] op_sel_hi:[1,0]
	v_pk_mul_f32 v[120:121], v[120:121], v[166:167] op_sel_hi:[1,0]
	v_pk_mul_f32 v[126:127], v[118:119], v[166:167] op_sel_hi:[1,0]
	v_pk_mul_f32 v[118:119], v[116:117], v[166:167] op_sel_hi:[1,0]
	v_cvt_pk_bf16_f32 v116, v120, v121
	v_cvt_pk_bf16_f32 v117, v122, v123
	v_cvt_pk_bf16_f32 v118, v118, v119
	v_cvt_pk_bf16_f32 v119, v126, v127
	global_store_dwordx4 v[124:125], v[116:119], off offset:256
	v_pk_mul_f32 v[112:113], v[112:113], v[170:171] op_sel_hi:[1,0]
	v_pk_mul_f32 v[114:115], v[114:115], v[170:171] op_sel_hi:[1,0]
	v_lshlrev_b64 v[116:117], 11, v[168:169]
	v_pk_mul_f32 v[118:119], v[110:111], v[170:171] op_sel_hi:[1,0]
	v_pk_mul_f32 v[110:111], v[108:109], v[170:171] op_sel_hi:[1,0]
	v_cvt_pk_bf16_f32 v108, v112, v113
	v_lshl_add_u64 v[112:113], s[34:35], 0, v[116:117]
	v_lshl_add_u64 v[112:113], v[112:113], 0, s[42:43]
	v_lshl_add_u64 v[112:113], v[112:113], 0, s[30:31]
	v_cvt_pk_bf16_f32 v109, v114, v115
	v_cvt_pk_bf16_f32 v110, v110, v111
	v_cvt_pk_bf16_f32 v111, v118, v119
	v_lshl_add_u64 v[112:113], v[112:113], 0, v[136:137]
	global_store_dwordx4 v[112:113], v[108:111], off
	v_pk_mul_f32 v[106:107], v[106:107], v[170:171] op_sel_hi:[1,0]
	v_pk_mul_f32 v[104:105], v[104:105], v[170:171] op_sel_hi:[1,0]
	v_pk_mul_f32 v[108:109], v[102:103], v[170:171] op_sel_hi:[1,0]
	v_pk_mul_f32 v[102:103], v[100:101], v[170:171] op_sel_hi:[1,0]
	v_cvt_pk_bf16_f32 v100, v104, v105
	v_cvt_pk_bf16_f32 v101, v106, v107
	v_cvt_pk_bf16_f32 v102, v102, v103
	v_cvt_pk_bf16_f32 v103, v108, v109
	global_store_dwordx4 v[112:113], v[100:103], off offset:256
	v_pk_mul_f32 v[96:97], v[96:97], v[148:149] op_sel_hi:[1,0]
	v_pk_mul_f32 v[98:99], v[98:99], v[148:149] op_sel_hi:[1,0]
	v_lshlrev_b64 v[100:101], 11, v[150:151]
	v_pk_mul_f32 v[102:103], v[94:95], v[148:149] op_sel_hi:[1,0]
	v_pk_mul_f32 v[94:95], v[92:93], v[148:149] op_sel_hi:[1,0]
	v_cvt_pk_bf16_f32 v92, v96, v97
	v_lshl_add_u64 v[96:97], s[34:35], 0, v[100:101]
	v_lshl_add_u64 v[96:97], v[96:97], 0, s[42:43]
	v_lshl_add_u64 v[96:97], v[96:97], 0, s[30:31]
	v_cvt_pk_bf16_f32 v93, v98, v99
	v_cvt_pk_bf16_f32 v94, v94, v95
	v_cvt_pk_bf16_f32 v95, v102, v103
	v_lshl_add_u64 v[96:97], v[96:97], 0, v[136:137]
	global_store_dwordx4 v[96:97], v[92:95], off
	v_pk_mul_f32 v[90:91], v[90:91], v[148:149] op_sel_hi:[1,0]
	v_pk_mul_f32 v[88:89], v[88:89], v[148:149] op_sel_hi:[1,0]
	v_pk_mul_f32 v[92:93], v[78:79], v[148:149] op_sel_hi:[1,0]
	v_pk_mul_f32 v[78:79], v[76:77], v[148:149] op_sel_hi:[1,0]
	v_cvt_pk_bf16_f32 v76, v88, v89
	v_cvt_pk_bf16_f32 v77, v90, v91
	v_cvt_pk_bf16_f32 v78, v78, v79
	v_cvt_pk_bf16_f32 v79, v92, v93
	global_store_dwordx4 v[96:97], v[76:79], off offset:256
	v_lshlrev_b64 v[88:89], 11, v[146:147]
	v_pk_mul_f32 v[80:81], v[80:81], v[144:145] op_sel_hi:[1,0]
	v_pk_mul_f32 v[78:79], v[86:87], v[144:145] op_sel_hi:[1,0]
	v_pk_mul_f32 v[76:77], v[84:85], v[144:145] op_sel_hi:[1,0]
	v_pk_mul_f32 v[82:83], v[82:83], v[144:145] op_sel_hi:[1,0]
	v_cvt_pk_bf16_f32 v76, v76, v77
	v_cvt_pk_bf16_f32 v77, v78, v79
	v_cvt_pk_bf16_f32 v78, v80, v81
	v_lshl_add_u64 v[80:81], s[34:35], 0, v[88:89]
	v_lshl_add_u64 v[80:81], v[80:81], 0, s[42:43]
	v_lshl_add_u64 v[80:81], v[80:81], 0, s[30:31]
	v_cvt_pk_bf16_f32 v79, v82, v83
	v_lshl_add_u64 v[80:81], v[80:81], 0, v[136:137]
	global_store_dwordx4 v[80:81], v[76:79], off
	v_pk_mul_f32 v[74:75], v[74:75], v[144:145] op_sel_hi:[1,0]
	v_pk_mul_f32 v[72:73], v[72:73], v[144:145] op_sel_hi:[1,0]
	v_pk_mul_f32 v[76:77], v[70:71], v[144:145] op_sel_hi:[1,0]
	v_pk_mul_f32 v[70:71], v[68:69], v[144:145] op_sel_hi:[1,0]
	v_cvt_pk_bf16_f32 v68, v72, v73
	v_cvt_pk_bf16_f32 v69, v74, v75
	v_cvt_pk_bf16_f32 v70, v70, v71
	v_cvt_pk_bf16_f32 v71, v76, v77
	v_pk_mul_f32 v[64:65], v[64:65], v[142:143] op_sel_hi:[1,0]
	global_store_dwordx4 v[80:81], v[68:71], off offset:256
	v_pk_mul_f32 v[66:67], v[66:67], v[142:143] op_sel_hi:[1,0]
	v_pk_mul_f32 v[46:47], v[46:47], v[142:143] op_sel_hi:[1,0]
	v_pk_mul_f32 v[68:69], v[62:63], v[142:143] op_sel_hi:[1,0]
	v_pk_mul_f32 v[62:63], v[60:61], v[142:143] op_sel_hi:[1,0]
	v_cvt_pk_bf16_f32 v60, v64, v65
	v_lshl_add_u64 v[64:65], v[124:125], 0, s[0:1]
	s_mov_b32 s0, 0x40000
	v_cvt_pk_bf16_f32 v61, v66, v67
	v_add_co_u32_e32 v66, vcc, s0, v124
	v_cvt_pk_bf16_f32 v62, v62, v63
	v_cvt_pk_bf16_f32 v63, v68, v69
	v_addc_co_u32_e32 v67, vcc, 0, v125, vcc
	global_store_dwordx4 v[66:67], v[60:63], off
	v_pk_mul_f32 v[44:45], v[44:45], v[142:143] op_sel_hi:[1,0]
	v_pk_mul_f32 v[40:41], v[40:41], v[140:141] op_sel_hi:[1,0]
	v_pk_mul_f32 v[60:61], v[38:39], v[142:143] op_sel_hi:[1,0]
	v_pk_mul_f32 v[38:39], v[36:37], v[142:143] op_sel_hi:[1,0]
	v_cvt_pk_bf16_f32 v36, v44, v45
	v_cvt_pk_bf16_f32 v37, v46, v47
	v_cvt_pk_bf16_f32 v38, v38, v39
	v_cvt_pk_bf16_f32 v39, v60, v61
	global_store_dwordx4 v[64:65], v[36:39], off offset:256
	s_mov_b64 s[0:1], 0x48000
	v_pk_mul_f32 v[42:43], v[42:43], v[140:141] op_sel_hi:[1,0]
	v_pk_mul_f32 v[38:39], v[50:51], v[140:141] op_sel_hi:[1,0]
	v_pk_mul_f32 v[36:37], v[48:49], v[140:141] op_sel_hi:[1,0]
	v_pk_mul_f32 v[22:23], v[22:23], v[140:141] op_sel_hi:[1,0]
	v_cvt_pk_bf16_f32 v36, v36, v37
	v_cvt_pk_bf16_f32 v37, v38, v39
	v_cvt_pk_bf16_f32 v38, v40, v41
	v_lshl_add_u64 v[40:41], v[124:125], 0, s[0:1]
	s_mov_b32 s0, 0x48000
	v_cvt_pk_bf16_f32 v39, v42, v43
	v_add_co_u32_e32 v42, vcc, s0, v124
	v_pk_mul_f32 v[20:21], v[20:21], v[140:141] op_sel_hi:[1,0]
	s_nop 0
	v_addc_co_u32_e32 v43, vcc, 0, v125, vcc
	global_store_dwordx4 v[42:43], v[36:39], off
	v_pk_mul_f32 v[16:17], v[16:17], v[138:139] op_sel_hi:[1,0]
	s_mov_b64 s[0:1], 0x50000
	v_pk_mul_f32 v[36:37], v[14:15], v[140:141] op_sel_hi:[1,0]
	v_pk_mul_f32 v[14:15], v[12:13], v[140:141] op_sel_hi:[1,0]
	v_cvt_pk_bf16_f32 v12, v20, v21
	v_cvt_pk_bf16_f32 v13, v22, v23
	v_cvt_pk_bf16_f32 v14, v14, v15
	v_cvt_pk_bf16_f32 v15, v36, v37
	global_store_dwordx4 v[40:41], v[12:15], off offset:256
	v_pk_mul_f32 v[18:19], v[18:19], v[138:139] op_sel_hi:[1,0]
	v_pk_mul_f32 v[20:21], v[56:57], v[138:139] op_sel_hi:[1,0]
	v_pk_mul_f32 v[14:15], v[26:27], v[138:139] op_sel_hi:[1,0]
	v_pk_mul_f32 v[12:13], v[24:25], v[138:139] op_sel_hi:[1,0]
	v_pk_mul_f32 v[8:9], v[8:9], v[2:3] op_sel_hi:[1,0]
	v_cvt_pk_bf16_f32 v12, v12, v13
	v_cvt_pk_bf16_f32 v13, v14, v15
	v_cvt_pk_bf16_f32 v14, v16, v17
	v_lshl_add_u64 v[16:17], v[124:125], 0, s[0:1]
	s_mov_b32 s0, 0x50000
	v_cvt_pk_bf16_f32 v15, v18, v19
	v_add_co_u32_e32 v18, vcc, s0, v124
	s_mov_b64 s[0:1], 0x58000
	s_nop 0
	v_addc_co_u32_e32 v19, vcc, 0, v125, vcc
	global_store_dwordx4 v[18:19], v[12:15], off
	v_pk_mul_f32 v[18:19], v[58:59], v[138:139] op_sel_hi:[1,0]
	v_pk_mul_f32 v[10:11], v[10:11], v[2:3] op_sel_hi:[1,0]
	v_pk_mul_f32 v[14:15], v[54:55], v[138:139] op_sel_hi:[1,0]
	v_pk_mul_f32 v[12:13], v[52:53], v[138:139] op_sel_hi:[1,0]
	v_mov_b32_e32 v144, v160
	v_cvt_pk_bf16_f32 v12, v12, v13
	v_cvt_pk_bf16_f32 v13, v14, v15
	v_cvt_pk_bf16_f32 v14, v20, v21
	v_cvt_pk_bf16_f32 v15, v18, v19
	global_store_dwordx4 v[16:17], v[12:15], off offset:256
	v_mov_b32_e32 v142, v159
	v_mov_b32_e32 v140, v158
	v_pk_mul_f32 v[12:13], v[6:7], v[2:3] op_sel_hi:[1,0]
	v_pk_mul_f32 v[6:7], v[4:5], v[2:3] op_sel_hi:[1,0]
	v_cvt_pk_bf16_f32 v4, v8, v9
	v_lshl_add_u64 v[8:9], v[124:125], 0, s[0:1]
	s_mov_b32 s0, 0x58000
	v_cvt_pk_bf16_f32 v5, v10, v11
	v_add_co_u32_e32 v10, vcc, s0, v124
	v_cvt_pk_bf16_f32 v6, v6, v7
	v_cvt_pk_bf16_f32 v7, v12, v13
	v_addc_co_u32_e32 v11, vcc, 0, v125, vcc
	global_store_dwordx4 v[10:11], v[4:7], off
	v_pk_mul_f32 v[10:11], v[34:35], v[2:3] op_sel_hi:[1,0]
	v_pk_mul_f32 v[12:13], v[32:33], v[2:3] op_sel_hi:[1,0]
	v_pk_mul_f32 v[6:7], v[30:31], v[2:3] op_sel_hi:[1,0]
	v_pk_mul_f32 v[4:5], v[28:29], v[2:3] op_sel_hi:[1,0]
	s_and_b64 vcc, exec, s[38:39]
	v_cvt_pk_bf16_f32 v4, v4, v5
	v_cvt_pk_bf16_f32 v5, v6, v7
	v_cvt_pk_bf16_f32 v6, v12, v13
	v_cvt_pk_bf16_f32 v7, v10, v11
	v_mov_b32_e32 v138, v141
	global_store_dwordx4 v[8:9], v[4:7], off offset:256
	s_cbranch_vccz .LBB0_2271
	s_waitcnt vmcnt(0)
	s_cmpk_gt_u32 s22, 0xff
	s_cbranch_scc1 .LBB0_2284
	s_barrier
